# piggyback layer-1 expert weight conversion (32 of 96 steps/wave) into MoE gate/up GEMM K-loops; hyena FFT phase converts only 64 steps
# speedup vs baseline: 1.0173x; 1.0173x over previous
; #define LAS __attribute__((address_space(3)))
; __device__ __forceinline__ KP kparams() { KP q = (KP)__builtin_amdgcn_kernarg_segment_ptr(); asm volatile("" : "+s"(q)); return q; }
; __global__ void __launch_bounds__(NTHR, 2) fwd(Params p_unused) {
;     extern __shared__ __attribute__((aligned(16))) unsigned char lds_raw[];
;     LAS unsigned char* lds = (LAS unsigned char*)lds_raw;
;     const int G = gridDim.x, bid = blockIdx.x;
;     const int vcu = (G % 8 == 0) ? (bid % 8) * (G / 8) + bid / 8 : bid;
;     if (threadIdx.x < 4) ((LAS unsigned*)(lds + LDS_MISC))[threadIdx.x] = 0u;
;     __syncthreads();
;     XcdBarrier bar;
;     { KP kp = kparams(); bar = xcd_barrier_post((unsigned*)(kp->ws + WS_CTL), (volatile LAS unsigned*)(lds + LDS_MISC)); }
_Z3fwd6Params:
	s_load_dword s3, s[0:1], 0x120
	s_add_u32 s4, s0, 0x120
	v_writelane_b32 v254, s0, 0
	s_addc_u32 s5, s1, 0
	s_mov_b32 s42, s2
	v_writelane_b32 v255, s2, 40
	v_writelane_b32 v254, s1, 1
	v_writelane_b32 v254, s4, 2
	s_waitcnt lgkmcnt(0)
	s_and_b32 s0, s3, 7
	s_cmp_lg_u32 s0, 0
	v_writelane_b32 v254, s5, 3
	v_writelane_b32 v254, s3, 4
	s_mov_b32 s0, s2
	s_cbranch_scc1 .LBB0_2
	s_ashr_i32 s1, s42, 31
	s_lshr_b32 s1, s1, 29
	s_add_i32 s1, s42, s1
	v_readlane_b32 s0, v254, 4
	s_ashr_i32 s2, s1, 3
	s_and_b32 s1, s1, -8
	s_ashr_i32 s0, s0, 3
	s_sub_i32 s1, s42, s1
	s_mul_i32 s0, s0, s1
	s_add_i32 s0, s0, s2

; __device__ __forceinline__ int tid_fresh() { int t = threadIdx.x; asm volatile("" : "+v"(t)); return t; }
; __device__ __forceinline__ unsigned cvt_pk_bf16(float lo, float hi) { unsigned r; asm volatile("v_cvt_pk_bf16_f32 %0, %1, %2" : "=v"(r) : "v"(lo), "v"(hi)); return r; }
; __device__ __forceinline__ bool bg_decode(int st, int wg, int NW, int lane, KP kp, const float*& src, int& ldS, bf16_t*& dst, int& o2) {
;     const int g = st * NW + wg;
;     if (g >= BG_STEPS) { src = kp->in[27] + lane; ldS = 0; dst = nullptr; o2 = 0; return false; }
;     const int l = g / 98304, r = g - l * 98304;
; __device__ __forceinline__ void hy_fft_phase(LAS unsigned char* lds, int bid, int G, const bf16_t* vgT, bf16_t* zT, const float* a3, const float* wout, const float* skip, float* filt, float4* gspec) {
;     ...
;             const int tid = tid_fresh(), lane = tid & 63, wave = tid >> 6, col = lane & 15, kc = lane >> 4;
;             const int ci = g0 + (col >> 1), c = bid + G * ci; const bool cok = ci < nch;
;             bf16x8 bw[2];
; #pragma unroll
;             for (int ks = 0; ks < 2; ++ks) { float wv[8];
; #pragma unroll
;                 for (int q = 0; q < 8; ++q) wv[q] = wout[(size_t)(ks * 32 + kc * 8 + q) * 4096 + (col & 1) * D + (cok ? c : bid)] * (cok ? 1.f : 0.f);
;                 u32x4 w; w.x = cvt_pk_bf16(wv[0], wv[1]); w.y = cvt_pk_bf16(wv[2], wv[3]); w.z = cvt_pk_bf16(wv[4], wv[5]); w.w = cvt_pk_bf16(wv[6], wv[7]);
;                 bw[ks] = __builtin_bit_cast(bf16x8, w); }
.LBB0_377:
	v_mov_b32_e32 v14, v0
	v_readlane_b32 s0, v254, 4
	v_bfe_u32 v2, v14, 1, 3
	v_or_b32_e32 v2, s84, v2
	v_mul_lo_u32 v3, v2, s0
	v_readlane_b32 s0, v254, 19
	v_cmp_gt_i32_e32 vcc, s61, v2
	v_lshlrev_b32_e32 v4, 13, v14
	v_add_u32_e32 v16, s0, v3
	v_cndmask_b32_e32 v2, v63, v16, vcc
	v_and_b32_e32 v60, 0x2000, v4
	v_bfe_u32 v15, v14, 4, 2
	v_ashrrev_i32_e32 v3, 31, v2
	v_lshl_add_u64 v[4:5], s[4:5], 0, v[60:61]
	v_lshl_add_u64 v[2:3], v[2:3], 2, v[4:5]
	v_lshlrev_b32_e32 v60, 17, v15
	v_readlane_b32 s1, v254, 20
	v_lshl_add_u64 v[6:7], v[2:3], 0, v[60:61]
	s_movk_i32 s0, 0x4000
	v_add_co_u32_e64 v2, s[0:1], s0, v6
	v_cndmask_b32_e64 v29, 0, 1.0, vcc
	s_nop 0
	v_addc_co_u32_e64 v3, s[0:1], 0, v7, s[0:1]
	s_mov_b32 s0, 0x8000
	s_nop 0
	v_add_co_u32_e64 v4, s[0:1], s0, v6
	s_mul_i32 s28, s60, s16
	s_nop 0
	v_addc_co_u32_e64 v5, s[0:1], 0, v7, s[0:1]
	s_mov_b32 s0, 0xc000
	s_nop 0
	v_add_co_u32_e64 v8, s[0:1], s0, v6
	s_add_i32 s28, s28, s17
	s_nop 0
	v_addc_co_u32_e64 v9, s[0:1], 0, v7, s[0:1]
	v_add_co_u32_e64 v10, s[0:1], s71, v6
	s_cmp_gt_i32 s28, 0x1ffff
	s_nop 0
	v_addc_co_u32_e64 v11, s[0:1], 0, v7, s[0:1]
	v_add_co_u32_e64 v12, s[0:1], s72, v6
	s_mov_b64 s[8:9], -1
	s_nop 0
	v_addc_co_u32_e64 v13, s[0:1], 0, v7, s[0:1]
	v_add_co_u32_e64 v18, s[0:1], s73, v6
	s_nop 1
	v_addc_co_u32_e64 v19, s[0:1], 0, v7, s[0:1]
	v_add_co_u32_e64 v20, s[0:1], s74, v6
	s_nop 1
	v_addc_co_u32_e64 v21, s[0:1], 0, v7, s[0:1]
	global_load_dword v17, v[6:7], off
	s_nop 0
	global_load_dword v2, v[2:3], off
	s_nop 0
	global_load_dword v3, v[4:5], off
	s_nop 0
	global_load_dword v4, v[8:9], off
	global_load_dword v5, v[10:11], off
	global_load_dword v26, v[12:13], off
	global_load_dword v27, v[18:19], off
	global_load_dword v28, v[20:21], off
	s_mov_b32 s0, 0x80000
	v_add_co_u32_e32 v8, vcc, s0, v6
	s_mov_b32 s0, 0x84000
	s_nop 0
	v_addc_co_u32_e32 v9, vcc, 0, v7, vcc
	v_add_co_u32_e32 v10, vcc, s0, v6
	s_mov_b32 s0, 0x88000
	s_nop 0
	v_addc_co_u32_e32 v11, vcc, 0, v7, vcc
	v_add_co_u32_e32 v12, vcc, s0, v6
	s_mov_b32 s0, 0x8c000
	s_nop 0
	v_addc_co_u32_e32 v13, vcc, 0, v7, vcc
	v_add_co_u32_e32 v18, vcc, s0, v6
	s_mov_b32 s0, 0x90000
	s_nop 0
	v_addc_co_u32_e32 v19, vcc, 0, v7, vcc
	v_add_co_u32_e32 v20, vcc, s0, v6
	s_mov_b32 s0, 0x94000
	s_nop 0
	v_addc_co_u32_e32 v21, vcc, 0, v7, vcc
	v_add_co_u32_e32 v22, vcc, s0, v6
	s_mov_b32 s0, 0x98000
	s_nop 0
	v_addc_co_u32_e32 v23, vcc, 0, v7, vcc
	v_add_co_u32_e32 v24, vcc, s0, v6
	s_mov_b32 s0, 0x9c000
	s_nop 0
	v_addc_co_u32_e32 v25, vcc, 0, v7, vcc
	v_add_co_u32_e32 v6, vcc, s0, v6
	v_readlane_b32 s0, v254, 0
	s_nop 0
	v_addc_co_u32_e32 v7, vcc, 0, v7, vcc
	v_readlane_b32 s1, v254, 1
	s_waitcnt vmcnt(7)
	v_mul_f32_e32 v17, v17, v29
	s_waitcnt vmcnt(6)
	v_mul_f32_e32 v2, v2, v29
	s_waitcnt vmcnt(5)
	v_mul_f32_e32 v3, v3, v29
	s_waitcnt vmcnt(4)
	v_mul_f32_e32 v4, v4, v29
	s_waitcnt vmcnt(3)
	v_mul_f32_e32 v5, v29, v5
	s_waitcnt vmcnt(2)
	v_mul_f32_e32 v26, v29, v26
	s_waitcnt vmcnt(1)
	v_mul_f32_e32 v27, v29, v27
	s_waitcnt vmcnt(0)
	v_mul_f32_e32 v28, v29, v28
	v_cvt_pk_bf16_f32 v2, v17, v2
	v_cvt_pk_bf16_f32 v3, v3, v4
	v_cvt_pk_bf16_f32 v4, v5, v26
	v_cvt_pk_bf16_f32 v5, v27, v28
	global_load_dword v8, v[8:9], off
	s_nop 0
	global_load_dword v9, v[10:11], off
	s_nop 0
	global_load_dword v10, v[12:13], off
	global_load_dword v11, v[18:19], off
	s_nop 0
	global_load_dword v12, v[20:21], off
	global_load_dword v13, v[22:23], off
	global_load_dword v17, v[24:25], off
	s_nop 0
	global_load_dword v6, v[6:7], off
	s_waitcnt vmcnt(7)
	v_mul_f32_e32 v7, v29, v8
	s_waitcnt vmcnt(6)
	v_mul_f32_e32 v8, v29, v9
	s_waitcnt vmcnt(5)
	v_mul_f32_e32 v9, v29, v10
	s_waitcnt vmcnt(4)
	v_mul_f32_e32 v10, v29, v11
	s_waitcnt vmcnt(3)
	v_mul_f32_e32 v11, v29, v12
	s_waitcnt vmcnt(2)
	v_mul_f32_e32 v12, v29, v13
	s_waitcnt vmcnt(1)
	v_mul_f32_e32 v13, v29, v17
	s_waitcnt vmcnt(0)
	v_mul_f32_e32 v17, v29, v6
	v_cvt_pk_bf16_f32 v6, v7, v8
	v_cvt_pk_bf16_f32 v7, v9, v10
	v_cvt_pk_bf16_f32 v8, v11, v12
	v_cvt_pk_bf16_f32 v9, v13, v17
	s_barrier
	s_cbranch_scc0 .LBB0_379
	s_load_dwordx2 s[8:9], s[0:1], 0xd8
	v_mov_b32_e32 v65, v61
	s_waitcnt lgkmcnt(0)
	v_lshl_add_u64 v[10:11], s[8:9], 0, v[64:65]
	s_mov_b64 s[8:9], 0

; __device__ __forceinline__ KP kparams() { KP q = (KP)__builtin_amdgcn_kernarg_segment_ptr(); asm volatile("" : "+s"(q)); return q; }
; __device__ __forceinline__ bool bg_decode(int st, int wg, int NW, int lane, KP kp, const float*& src, int& ldS, bf16_t*& dst, int& o2) {
;     const int g = st * NW + wg;
;     if (g >= BG_STEPS) { src = kp->in[27] + lane; ldS = 0; dst = nullptr; o2 = 0; return false; }
;     const int l = g / 98304, r = g - l * 98304;
; template <int BANK> __device__ __forceinline__ void bg_issue1(BgState& b, int wg, int NW, int lane) {
;     KP kp = kparams();
;     const float* src; int ldS; bf16_t* dst; int o2;
;     bg_decode(b.st, wg, NW, lane, kp, src, ldS, dst, o2);
;     b.dst[BANK] = dst; b.o2[BANK] = o2;
;     asm volatile("s_nop 6" ::: "memory");
.LBB0_389:
	v_readlane_b32 s0, v254, 0
	s_add_i32 s33, s28, s53
	v_readlane_b32 s1, v254, 1
	s_cmp_lt_i32 s33, 0x20000
	s_mov_b64 s[42:43], -1
	s_cbranch_scc1 .LBB0_391
	s_load_dwordx2 s[42:43], s[0:1], 0xd8
	v_mov_b32_e32 v65, v61
	s_waitcnt lgkmcnt(0)
	v_lshl_add_u64 v[10:11], s[42:43], 0, v[64:65]
	s_mov_b64 s[42:43], 0

; __device__ __forceinline__ KP kparams() { KP q = (KP)__builtin_amdgcn_kernarg_segment_ptr(); asm volatile("" : "+s"(q)); return q; }
; __device__ __forceinline__ bool bg_decode(int st, int wg, int NW, int lane, KP kp, const float*& src, int& ldS, bf16_t*& dst, int& o2) {
;     const int g = st * NW + wg;
;     if (g >= BG_STEPS) { src = kp->in[27] + lane; ldS = 0; dst = nullptr; o2 = 0; return false; }
;     const int l = g / 98304, r = g - l * 98304;
; template <int BANK> __device__ __forceinline__ void bg_issue1(BgState& b, int wg, int NW, int lane) {
;     KP kp = kparams();
;     const float* src; int ldS; bf16_t* dst; int o2;
;     bg_decode(b.st, wg, NW, lane, kp, src, ldS, dst, o2);
;     b.dst[BANK] = dst; b.o2[BANK] = o2;
;     asm volatile("s_nop 6" ::: "memory");
.LBB0_465:
	s_or_b64 exec, exec, s[42:43]
	v_readlane_b32 s42, v254, 0
	s_add_i32 s1, s49, s53
	v_readlane_b32 s43, v254, 1
	s_cmp_lt_i32 s1, 0x20000
	s_mov_b64 s[44:45], -1
	s_cbranch_scc1 .LBB0_467
	s_load_dwordx2 s[44:45], s[42:43], 0xd8
	v_mov_b32_e32 v65, v61
	s_waitcnt lgkmcnt(0)
	v_lshl_add_u64 v[10:11], s[44:45], 0, v[64:65]
	s_mov_b64 s[44:45], 0

; __device__ __forceinline__ int tid_fresh() { int t = threadIdx.x; asm volatile("" : "+v"(t)); return t; }
; #define SEG_LD32(dst, off, base) asm volatile("global_load_dword %0, %1, %2" : "=v"(dst) : "v"(off), "s"(base) : "memory")
; #define BG_I(x) bg_issue1<x>(bg, bgwg, bgNW, bglane)
; __device__ __forceinline__ void hy_fft_phase(LAS unsigned char* lds, int bid, int G, const bf16_t* vgT, bf16_t* zT, const float* a3, const float* wout, const float* skip, float* filt, float4* gspec) {
;     ...
;         for (int ci = g0; ci < g0 + 8 && ci < nch; ci += 2) {
;             const bool has2 = (ci + 1 < nch);
;             const int c1 = bid + G * ci, c2 = has2 ? bid + G * (ci + 1) : c1;
;             const bf16_t* A1 = F + (size_t)(ci - g0) * FN; const bf16_t* A2 = has2 ? A1 + FN : A1;
;             const bf16_t* v1 = vgT + (size_t)c1 * T; const bf16_t* v2 = vgT + (size_t)c2 * T;
;             __syncthreads();
; #pragma unroll 1
;             for (int rep_ = 0; rep_ < REP_F1; ++rep_) {
;             tid = tid_fresh();
;             {   unsigned pa[16], pb[16]; float sk[2];
;                 const float* skp = skip; asm volatile("" : "+s"(skp));
; #pragma unroll
;                 for (int i = 0; i < 16; ++i) { const unsigned off = 4u * tid + 2048u * i; SEG_LD32(pa[i], off, A1); SEG_LD32(pb[i], off, A2); }
;                 { const unsigned o1 = 4u * c1, o2 = 4u * c2; SEG_LD32(sk[0], o1, skp); SEG_LD32(sk[1], o2, skp); }
;                 BG_I(1);
.LBB0_543:
	s_or_b32 s0, s87, 1
	v_readlane_b32 s1, v254, 4
	s_cmp_lt_i32 s0, s61
	s_mul_i32 s0, s87, s1
	v_readlane_b32 s42, v254, 19
	s_cselect_b64 s[8:9], -1, 0
	s_add_i32 s0, s0, s42
	v_readlane_b32 s43, v254, 20
	s_add_i32 s1, s0, s1
	s_and_b64 s[42:43], s[8:9], exec
	s_cselect_b32 s28, 0x8000, 0
	s_cselect_b32 s46, s1, s0
	s_sub_i32 s12, s87, s84
	s_lshl_b64 s[42:43], s[12:13], 15
	s_add_u32 s42, s10, s42
	s_addc_u32 s43, s11, s43
	v_mov_b32_e32 v80, v0
	s_mov_b64 s[50:51], s[6:7]
	s_add_u32 s48, s42, s28
	s_barrier
	s_addc_u32 s49, s43, 0
	v_lshlrev_b32_e32 v2, 2, v80
	global_load_dword v81, v2, s[42:43]
	global_load_dword v82, v2, s[48:49]
	v_add_u32_e32 v3, 0x800, v2
	global_load_dword v78, v3, s[42:43]
	global_load_dword v79, v3, s[48:49]
	v_add_u32_e32 v3, 0x1000, v2
	global_load_dword v76, v3, s[42:43]
	global_load_dword v77, v3, s[48:49]
	v_add_u32_e32 v3, 0x1800, v2
	global_load_dword v74, v3, s[42:43]
	global_load_dword v75, v3, s[48:49]
	v_add_u32_e32 v3, 0x2000, v2
	global_load_dword v72, v3, s[42:43]
	global_load_dword v73, v3, s[48:49]
	v_add_u32_e32 v3, 0x2800, v2
	global_load_dword v70, v3, s[42:43]
	global_load_dword v71, v3, s[48:49]
	v_add_u32_e32 v3, 0x3000, v2
	global_load_dword v56, v3, s[42:43]
	global_load_dword v57, v3, s[48:49]
	v_add_u32_e32 v3, 0x3800, v2
	global_load_dword v54, v3, s[42:43]
	global_load_dword v55, v3, s[48:49]
	v_add_u32_e32 v3, 0x4000, v2
	global_load_dword v52, v3, s[42:43]
	global_load_dword v53, v3, s[48:49]
	v_add_u32_e32 v3, 0x4800, v2
	global_load_dword v50, v3, s[42:43]
	global_load_dword v51, v3, s[48:49]
	v_add_u32_e32 v3, 0x5000, v2
	global_load_dword v48, v3, s[42:43]
	global_load_dword v49, v3, s[48:49]
	v_add_u32_e32 v3, 0x5800, v2
	global_load_dword v46, v3, s[42:43]
	global_load_dword v47, v3, s[48:49]
	v_add_u32_e32 v3, 0x6000, v2
	global_load_dword v44, v3, s[42:43]
	global_load_dword v45, v3, s[48:49]
	v_add_u32_e32 v3, 0x6800, v2
	global_load_dword v42, v3, s[42:43]
	global_load_dword v43, v3, s[48:49]
	v_add_u32_e32 v3, 0x7000, v2
	global_load_dword v34, v3, s[42:43]
	global_load_dword v35, v3, s[48:49]
	v_add_u32_e32 v2, 0x7800, v2
	global_load_dword v6, v2, s[42:43]
	s_lshl_b32 s1, s0, 2
	global_load_dword v7, v2, s[48:49]
	s_lshl_b32 s12, s46, 2
	v_mov_b32_e32 v2, s1
	global_load_dword v83, v2, s[50:51]
	v_mov_b32_e32 v2, s12
	global_load_dword v84, v2, s[50:51]
	s_mul_i32 s1, s60, s16
	v_readlane_b32 s42, v254, 0
	s_add_i32 s1, s1, s17
	v_readlane_b32 s43, v254, 1
	s_cmp_lt_i32 s1, 0x20000
	s_mov_b64 s[48:49], -1
	s_cbranch_scc1 .LBB0_545
	s_load_dwordx2 s[48:49], s[42:43], 0xd8
	v_mov_b32_e32 v65, v61
	s_waitcnt lgkmcnt(0)
	v_lshl_add_u64 v[4:5], s[48:49], 0, v[64:65]
	s_mov_b64 s[48:49], 0

; __device__ __forceinline__ bool bg_decode(int st, int wg, int NW, int lane, KP kp, const float*& src, int& ldS, bf16_t*& dst, int& o2) {
;     const int g = st * NW + wg;
;     if (g >= BG_STEPS) { src = kp->in[27] + lane; ldS = 0; dst = nullptr; o2 = 0; return false; }
;     const int l = g / 98304, r = g - l * 98304;
.LBB0_555:
	s_or_b64 exec, exec, s[42:43]
	s_add_i32 s1, s60, 1
	s_mul_i32 s1, s1, s16
	v_readlane_b32 s42, v254, 0
	s_add_i32 s1, s1, s17
	v_mov_b32_e32 v57, v0
	v_readlane_b32 s43, v254, 1
	s_cmp_lt_i32 s1, 0x20000
	s_mov_b64 s[44:45], -1
	s_waitcnt lgkmcnt(0)
	s_barrier
	s_cbranch_scc1 .LBB0_557
	s_load_dwordx2 s[44:45], s[42:43], 0xd8
	v_mov_b32_e32 v65, v61
	s_waitcnt lgkmcnt(0)
	v_lshl_add_u64 v[4:5], s[44:45], 0, v[64:65]
	s_mov_b64 s[44:45], 0

; __device__ __forceinline__ bool bg_decode(int st, int wg, int NW, int lane, KP kp, const float*& src, int& ldS, bf16_t*& dst, int& o2) {
;     const int g = st * NW + wg;
;     if (g >= BG_STEPS) { src = kp->in[27] + lane; ldS = 0; dst = nullptr; o2 = 0; return false; }
;     const int l = g / 98304, r = g - l * 98304;
.LBB0_569:
	s_or_b64 exec, exec, s[44:45]
	s_add_i32 s1, s60, 2
	s_mul_i32 s1, s1, s16
	v_readlane_b32 s44, v254, 0
	s_add_i32 s1, s1, s17
	v_readlane_b32 s45, v254, 1
	s_cmp_lt_i32 s1, 0x20000
	s_mov_b64 s[48:49], -1
	s_cbranch_scc1 .LBB0_571
	s_load_dwordx2 s[48:49], s[44:45], 0xd8
	v_mov_b32_e32 v65, v61
	s_waitcnt lgkmcnt(0)
	v_lshl_add_u64 v[2:3], s[48:49], 0, v[64:65]
	s_mov_b64 s[48:49], 0

; __device__ __forceinline__ bool bg_decode(int st, int wg, int NW, int lane, KP kp, const float*& src, int& ldS, bf16_t*& dst, int& o2) {
;     const int g = st * NW + wg;
;     if (g >= BG_STEPS) { src = kp->in[27] + lane; ldS = 0; dst = nullptr; o2 = 0; return false; }
;     const int l = g / 98304, r = g - l * 98304;
.LBB0_581:
	s_or_b64 exec, exec, s[48:49]
	s_add_i32 s1, s60, 3
	s_mul_i32 s1, s1, s16
	v_readlane_b32 s42, v254, 0
	s_add_i32 s1, s1, s17
	v_readlane_b32 s43, v254, 1
	s_cmp_lt_i32 s1, 0x20000
	s_mov_b64 s[48:49], -1
	s_cbranch_scc1 .LBB0_583
	s_load_dwordx2 s[48:49], s[42:43], 0xd8
	v_mov_b32_e32 v65, v61
	s_waitcnt lgkmcnt(0)
	v_lshl_add_u64 v[2:3], s[48:49], 0, v[64:65]
	s_mov_b64 s[48:49], 0

; __device__ __forceinline__ bool bg_decode(int st, int wg, int NW, int lane, KP kp, const float*& src, int& ldS, bf16_t*& dst, int& o2) {
;     const int g = st * NW + wg;
;     if (g >= BG_STEPS) { src = kp->in[27] + lane; ldS = 0; dst = nullptr; o2 = 0; return false; }
;     const int l = g / 98304, r = g - l * 98304;
.LBB0_593:
	s_or_b64 exec, exec, s[48:49]
	s_add_i32 s1, s60, 4
	s_mul_i32 s1, s1, s16
	v_readlane_b32 s44, v254, 0
	s_add_i32 s1, s1, s17
	v_readlane_b32 s45, v254, 1
	s_cmp_lt_i32 s1, 0x20000
	s_mov_b64 s[48:49], -1
	s_cbranch_scc1 .LBB0_595
	s_load_dwordx2 s[48:49], s[44:45], 0xd8
	v_mov_b32_e32 v65, v61
	s_waitcnt lgkmcnt(0)
	v_lshl_add_u64 v[4:5], s[48:49], 0, v[64:65]
	s_mov_b64 s[48:49], 0

; __device__ __forceinline__ bool bg_decode(int st, int wg, int NW, int lane, KP kp, const float*& src, int& ldS, bf16_t*& dst, int& o2) {
;     const int g = st * NW + wg;
;     if (g >= BG_STEPS) { src = kp->in[27] + lane; ldS = 0; dst = nullptr; o2 = 0; return false; }
;     const int l = g / 98304, r = g - l * 98304;
.LBB0_608:
	s_or_b64 exec, exec, s[44:45]
	s_add_i32 s1, s60, 5
	s_mul_i32 s1, s1, s16
	v_readlane_b32 s42, v254, 0
	s_add_i32 s1, s1, s17
	v_mov_b32_e32 v6, v0
	v_readlane_b32 s43, v254, 1
	s_cmp_lt_i32 s1, 0x20000
	s_mov_b64 s[44:45], -1
	s_cbranch_scc1 .LBB0_610
	s_load_dwordx2 s[44:45], s[42:43], 0xd8
	v_mov_b32_e32 v65, v61
	s_waitcnt lgkmcnt(0)
	v_lshl_add_u64 v[8:9], s[44:45], 0, v[64:65]
	s_mov_b64 s[44:45], 0

; __device__ __forceinline__ int tid_fresh() { int t = threadIdx.x; asm volatile("" : "+v"(t)); return t; }
; #define SEG_LD32(dst, off, base) asm volatile("global_load_dword %0, %1, %2" : "=v"(dst) : "v"(off), "s"(base) : "memory")
; #define BG_I(x) bg_issue1<x>(bg, bgwg, bgNW, bglane)
; __device__ __forceinline__ bool bg_decode(int st, int wg, int NW, int lane, KP kp, const float*& src, int& ldS, bf16_t*& dst, int& o2) {
;     const int g = st * NW + wg;
;     if (g >= BG_STEPS) { src = kp->in[27] + lane; ldS = 0; dst = nullptr; o2 = 0; return false; }
;     const int l = g / 98304, r = g - l * 98304;
; __device__ __forceinline__ void hy_fft_phase(LAS unsigned char* lds, int bid, int G, const bf16_t* vgT, bf16_t* zT, const float* a3, const float* wout, const float* skip, float* filt, float4* gspec) {
;     ...
;             tid = tid_fresh();
;             {   unsigned pa[8], pb[8];
; #pragma unroll
;                 for (int i = 0; i < 8; ++i) { const unsigned off = 4u * tid + 2048u * i; SEG_LD32(pa[i], off, v1); SEG_LD32(pb[i], off, v2); }
;                 BG_I(1);
.LBB0_623:
	s_or_b64 exec, exec, s[42:43]
	s_ashr_i32 s1, s0, 31
	s_add_i32 s12, s60, 6
	s_ashr_i32 s47, s46, 31
	s_lshl_b64 s[42:43], s[0:1], 14
	s_add_u32 s42, s64, s42
	s_addc_u32 s43, s65, s43
	s_lshl_b64 s[48:49], s[46:47], 14
	v_mov_b32_e32 v54, v0
	s_add_u32 s48, s64, s48
	s_barrier
	s_addc_u32 s49, s65, s49
	v_lshlrev_b32_e32 v2, 2, v54
	global_load_dword v55, v2, s[42:43]
	global_load_dword v56, v2, s[48:49]
	v_add_u32_e32 v3, 0x800, v2
	global_load_dword v52, v3, s[42:43]
	global_load_dword v53, v3, s[48:49]
	v_add_u32_e32 v3, 0x1000, v2
	global_load_dword v50, v3, s[42:43]
	global_load_dword v51, v3, s[48:49]
	v_add_u32_e32 v3, 0x1800, v2
	global_load_dword v48, v3, s[42:43]
	global_load_dword v49, v3, s[48:49]
	v_add_u32_e32 v3, 0x2000, v2
	global_load_dword v46, v3, s[42:43]
	global_load_dword v47, v3, s[48:49]
	v_add_u32_e32 v3, 0x2800, v2
	global_load_dword v44, v3, s[42:43]
	global_load_dword v45, v3, s[48:49]
	v_add_u32_e32 v3, 0x3000, v2
	global_load_dword v42, v3, s[42:43]
	global_load_dword v43, v3, s[48:49]
	v_add_u32_e32 v2, 0x3800, v2
	global_load_dword v8, v2, s[42:43]
	global_load_dword v9, v2, s[48:49]
	s_mul_i32 s28, s12, s16
	v_readlane_b32 s42, v254, 0
	s_add_i32 s28, s28, s17
	v_readlane_b32 s43, v254, 1
	s_cmp_gt_i32 s28, 0x1ffff
	s_mov_b64 s[48:49], -1
	s_cbranch_scc0 .LBB0_625
	s_load_dwordx2 s[48:49], s[42:43], 0xd8
	v_mov_b32_e32 v65, v61
	s_waitcnt lgkmcnt(0)
	v_lshl_add_u64 v[6:7], s[48:49], 0, v[64:65]
	s_mov_b64 s[48:49], 0

; __device__ __forceinline__ bool bg_decode(int st, int wg, int NW, int lane, KP kp, const float*& src, int& ldS, bf16_t*& dst, int& o2) {
;     const int g = st * NW + wg;
;     if (g >= BG_STEPS) { src = kp->in[27] + lane; ldS = 0; dst = nullptr; o2 = 0; return false; }
;     const int l = g / 98304, r = g - l * 98304;
.LBB0_635:
	s_or_b64 exec, exec, s[46:47]
	s_add_i32 s12, s60, 7
	s_mul_i32 s28, s12, s16
	v_readlane_b32 s44, v254, 0
	s_add_i32 s28, s28, s17
	v_mov_b32_e32 v120, v0
	v_readlane_b32 s45, v254, 1
	s_cmp_lt_i32 s28, 0x20000
	s_mov_b64 s[46:47], -1
	s_waitcnt lgkmcnt(0)
	s_barrier
	s_cbranch_scc1 .LBB0_637
	s_load_dwordx2 s[46:47], s[44:45], 0xd8
	v_mov_b32_e32 v65, v61
	s_waitcnt lgkmcnt(0)
	v_lshl_add_u64 v[4:5], s[46:47], 0, v[64:65]
	s_mov_b64 s[46:47], 0

; __device__ __forceinline__ bool bg_decode(int st, int wg, int NW, int lane, KP kp, const float*& src, int& ldS, bf16_t*& dst, int& o2) {
;     const int g = st * NW + wg;
;     if (g >= BG_STEPS) { src = kp->in[27] + lane; ldS = 0; dst = nullptr; o2 = 0; return false; }
;     const int l = g / 98304, r = g - l * 98304;
.LBB0_649:
	s_or_b64 exec, exec, s[46:47]
	s_add_i32 s12, s60, 8
	s_mul_i32 s28, s12, s16
	v_readlane_b32 s46, v254, 0
	s_add_i32 s28, s28, s17
	v_readlane_b32 s47, v254, 1
	s_cmp_lt_i32 s28, 0x20000
	s_mov_b64 s[48:49], -1
	s_cbranch_scc1 .LBB0_651
	s_load_dwordx2 s[48:49], s[46:47], 0xd8
	v_mov_b32_e32 v65, v61
	s_waitcnt lgkmcnt(0)
	v_lshl_add_u64 v[2:3], s[48:49], 0, v[64:65]
	s_mov_b64 s[48:49], 0

; __device__ __forceinline__ bool bg_decode(int st, int wg, int NW, int lane, KP kp, const float*& src, int& ldS, bf16_t*& dst, int& o2) {
;     const int g = st * NW + wg;
;     if (g >= BG_STEPS) { src = kp->in[27] + lane; ldS = 0; dst = nullptr; o2 = 0; return false; }
;     const int l = g / 98304, r = g - l * 98304;
.LBB0_661:
	s_or_b64 exec, exec, s[48:49]
	s_add_i32 s12, s60, 9
	s_mul_i32 s28, s12, s16
	v_readlane_b32 s44, v254, 0
	s_add_i32 s28, s28, s17
	v_readlane_b32 s45, v254, 1
	s_cmp_lt_i32 s28, 0x20000
	s_mov_b64 s[48:49], -1
	s_cbranch_scc1 .LBB0_663
	s_load_dwordx2 s[48:49], s[44:45], 0xd8
	v_mov_b32_e32 v65, v61
	s_waitcnt lgkmcnt(0)
	v_lshl_add_u64 v[2:3], s[48:49], 0, v[64:65]
	s_mov_b64 s[48:49], 0

; __device__ __forceinline__ bool bg_decode(int st, int wg, int NW, int lane, KP kp, const float*& src, int& ldS, bf16_t*& dst, int& o2) {
;     const int g = st * NW + wg;
;     if (g >= BG_STEPS) { src = kp->in[27] + lane; ldS = 0; dst = nullptr; o2 = 0; return false; }
;     const int l = g / 98304, r = g - l * 98304;
.LBB0_673:
	s_or_b64 exec, exec, s[44:45]
	s_add_i32 s12, s60, 10
	s_mul_i32 s28, s12, s16
	v_readlane_b32 s44, v254, 0
	s_add_i32 s28, s28, s17
	v_readlane_b32 s45, v254, 1
	s_cmp_lt_i32 s28, 0x20000
	s_mov_b64 s[46:47], -1
	s_cbranch_scc1 .LBB0_675
	s_load_dwordx2 s[46:47], s[44:45], 0xd8
	v_mov_b32_e32 v65, v61
	s_waitcnt lgkmcnt(0)
	v_lshl_add_u64 v[4:5], s[46:47], 0, v[64:65]
	s_mov_b64 s[46:47], 0

; #define SEG_LD64(dst, off, base) asm volatile("global_load_dwordx2 %0, %1, %2" : "=v"(dst) : "v"(off), "s"(base) : "memory")
; #define BG_I(x) bg_issue1<x>(bg, bgwg, bgNW, bglane)
; __device__ __forceinline__ bool bg_decode(int st, int wg, int NW, int lane, KP kp, const float*& src, int& ldS, bf16_t*& dst, int& o2) {
;     const int g = st * NW + wg;
;     if (g >= BG_STEPS) { src = kp->in[27] + lane; ldS = 0; dst = nullptr; o2 = 0; return false; }
;     const int l = g / 98304, r = g - l * 98304;
; __device__ __forceinline__ void hy_fft_phase(LAS unsigned char* lds, int bid, int G, const bf16_t* vgT, bf16_t* zT, const float* a3, const float* wout, const float* skip, float* filt, float4* gspec) {
;     ...
;             {   u32x2 gq[16], gh;
; #pragma unroll
;                 for (int i = 0; i < 16; ++i) { const unsigned off = 8u * tid + 4096u * i; SEG_LD64(gq[i], off, GS); }
;                 { const unsigned off = 8u * (FN / 2); SEG_LD64(gh, off, GS); }
;                 BG_I(0);
.LBB0_688:
	s_or_b64 exec, exec, s[46:47]
	v_mov_b32_e32 v114, v0
	s_add_i32 s12, s60, 11
	v_lshlrev_b32_e32 v4, 3, v114
	global_load_dwordx2 v[38:39], v4, s[20:21]
	v_add_u32_e32 v5, 0x1000, v4
	global_load_dwordx2 v[36:37], v5, s[20:21]
	v_add_u32_e32 v5, 0x2000, v4
	global_load_dwordx2 v[34:35], v5, s[20:21]
	v_add_u32_e32 v5, 0x3000, v4
	global_load_dwordx2 v[32:33], v5, s[20:21]
	v_add_u32_e32 v5, 0x4000, v4
	global_load_dwordx2 v[30:31], v5, s[20:21]
	v_add_u32_e32 v5, 0x5000, v4
	global_load_dwordx2 v[28:29], v5, s[20:21]
	v_add_u32_e32 v5, 0x6000, v4
	global_load_dwordx2 v[26:27], v5, s[20:21]
	v_add_u32_e32 v5, 0x7000, v4
	global_load_dwordx2 v[24:25], v5, s[20:21]
	v_add_u32_e32 v5, 0x8000, v4
	global_load_dwordx2 v[22:23], v5, s[20:21]
	v_add_u32_e32 v5, 0x9000, v4
	global_load_dwordx2 v[20:21], v5, s[20:21]
	v_add_u32_e32 v5, 0xa000, v4
	global_load_dwordx2 v[18:19], v5, s[20:21]
	v_add_u32_e32 v5, 0xb000, v4
	global_load_dwordx2 v[16:17], v5, s[20:21]
	v_add_u32_e32 v5, 0xc000, v4
	global_load_dwordx2 v[14:15], v5, s[20:21]
	v_add_u32_e32 v5, 0xd000, v4
	global_load_dwordx2 v[12:13], v5, s[20:21]
	v_add_u32_e32 v5, 0xe000, v4
	global_load_dwordx2 v[10:11], v5, s[20:21]
	v_add_u32_e32 v4, 0xf000, v4
	global_load_dwordx2 v[8:9], v4, s[20:21]
	global_load_dwordx2 v[6:7], v119, s[20:21]
	s_mul_i32 s28, s12, s16
	v_readlane_b32 s46, v254, 0
	s_add_i32 s28, s28, s17
	v_readlane_b32 s47, v254, 1
	s_cmp_lt_i32 s28, 0x20000
	s_mov_b64 s[48:49], -1
	s_cbranch_scc1 .LBB0_690
	s_load_dwordx2 s[48:49], s[46:47], 0xd8
	v_mov_b32_e32 v65, v61
	s_waitcnt lgkmcnt(0)
	v_lshl_add_u64 v[40:41], s[48:49], 0, v[64:65]
	s_mov_b64 s[48:49], 0

; #define BG_I(x) bg_issue1<x>(bg, bgwg, bgNW, bglane)
; #define BG_F(y) bg_finish1<y, 32>(bg)
; __device__ __forceinline__ bool bg_decode(int st, int wg, int NW, int lane, KP kp, const float*& src, int& ldS, bf16_t*& dst, int& o2) {
;     const int g = st * NW + wg;
;     if (g >= BG_STEPS) { src = kp->in[27] + lane; ldS = 0; dst = nullptr; o2 = 0; return false; }
;     const int l = g / 98304, r = g - l * 98304;
; __device__ __forceinline__ void hy_fft_phase(LAS unsigned char* lds, int bid, int G, const bf16_t* vgT, bf16_t* zT, const float* a3, const float* wout, const float* skip, float* filt, float4* gspec) {
;     ...
;             BG_I(1); fft_r4_pass<true>(z, tid, NTHR); __syncthreads(); BG_F(0);
;             BG_I(0); fft_r16_pass<true, 2>(z, tid); __syncthreads(); BG_F(1); BG_I(1); fft_r16_pass<true, 6>(z, tid); __syncthreads(); BG_F(0); BG_I(0); fft_r16_pass<true, 10>(z, tid); __syncthreads(); BG_F(1);
.LBB0_702:
	s_or_b64 exec, exec, s[48:49]
	s_add_i32 s12, s60, 12
	s_mul_i32 s28, s12, s16
	v_readlane_b32 s44, v254, 0
	s_add_i32 s28, s28, s17
	v_mov_b32_e32 v128, v0
	v_readlane_b32 s45, v254, 1
	s_cmp_lt_i32 s28, 0x20000
	s_mov_b64 s[48:49], -1
	s_waitcnt lgkmcnt(0)
	s_barrier
	s_cbranch_scc1 .LBB0_704
	s_load_dwordx2 s[48:49], s[44:45], 0xd8
	v_mov_b32_e32 v65, v61
	s_waitcnt lgkmcnt(0)
	v_lshl_add_u64 v[2:3], s[48:49], 0, v[64:65]
	s_mov_b64 s[48:49], 0

; #define BG_I(x) bg_issue1<x>(bg, bgwg, bgNW, bglane)
; #define BG_F(y) bg_finish1<y, 32>(bg)
; __device__ __forceinline__ bool bg_decode(int st, int wg, int NW, int lane, KP kp, const float*& src, int& ldS, bf16_t*& dst, int& o2) {
;     const int g = st * NW + wg;
;     if (g >= BG_STEPS) { src = kp->in[27] + lane; ldS = 0; dst = nullptr; o2 = 0; return false; }
;     const int l = g / 98304, r = g - l * 98304;
; __device__ __forceinline__ void hy_fft_phase(LAS unsigned char* lds, int bid, int G, const bf16_t* vgT, bf16_t* zT, const float* a3, const float* wout, const float* skip, float* filt, float4* gspec) {
;     ...
;             BG_I(1); fft_r4_pass<true>(z, tid, NTHR); __syncthreads(); BG_F(0);
;             BG_I(0); fft_r16_pass<true, 2>(z, tid); __syncthreads(); BG_F(1); BG_I(1); fft_r16_pass<true, 6>(z, tid); __syncthreads(); BG_F(0); BG_I(0); fft_r16_pass<true, 10>(z, tid); __syncthreads(); BG_F(1);
.LBB0_717:
	s_or_b64 exec, exec, s[44:45]
	s_add_i32 s12, s60, 13
	s_mul_i32 s28, s12, s16
	v_readlane_b32 s44, v254, 0
	s_add_i32 s28, s28, s17
	v_readlane_b32 s45, v254, 1
	s_cmp_lt_i32 s28, 0x20000
	s_mov_b64 s[46:47], -1
	s_cbranch_scc1 .LBB0_719
	s_load_dwordx2 s[46:47], s[44:45], 0xd8
	v_mov_b32_e32 v65, v61
	s_waitcnt lgkmcnt(0)
	v_lshl_add_u64 v[2:3], s[46:47], 0, v[64:65]
	s_mov_b64 s[46:47], 0

; #define BG_I(x) bg_issue1<x>(bg, bgwg, bgNW, bglane)
; #define BG_F(y) bg_finish1<y, 32>(bg)
; __device__ __forceinline__ bool bg_decode(int st, int wg, int NW, int lane, KP kp, const float*& src, int& ldS, bf16_t*& dst, int& o2) {
;     const int g = st * NW + wg;
;     if (g >= BG_STEPS) { src = kp->in[27] + lane; ldS = 0; dst = nullptr; o2 = 0; return false; }
;     const int l = g / 98304, r = g - l * 98304;
; __device__ __forceinline__ void hy_fft_phase(LAS unsigned char* lds, int bid, int G, const bf16_t* vgT, bf16_t* zT, const float* a3, const float* wout, const float* skip, float* filt, float4* gspec) {
;     ...
;             BG_I(1); fft_r4_pass<true>(z, tid, NTHR); __syncthreads(); BG_F(0);
;             BG_I(0); fft_r16_pass<true, 2>(z, tid); __syncthreads(); BG_F(1); BG_I(1); fft_r16_pass<true, 6>(z, tid); __syncthreads(); BG_F(0); BG_I(0); fft_r16_pass<true, 10>(z, tid); __syncthreads(); BG_F(1);
.LBB0_729:
	s_or_b64 exec, exec, s[46:47]
	s_add_i32 s12, s60, 14
	s_mul_i32 s28, s12, s16
	v_readlane_b32 s46, v254, 0
	s_add_i32 s28, s28, s17
	v_readlane_b32 s47, v254, 1
	s_cmp_lt_i32 s28, 0x20000
	s_mov_b64 s[48:49], -1
	s_cbranch_scc1 .LBB0_731
	s_load_dwordx2 s[48:49], s[46:47], 0xd8
	v_mov_b32_e32 v65, v61
	s_waitcnt lgkmcnt(0)
	v_lshl_add_u64 v[2:3], s[48:49], 0, v[64:65]
	s_mov_b64 s[48:49], 0

; #define BG_I(x) bg_issue1<x>(bg, bgwg, bgNW, bglane)
; #define BG_F(y) bg_finish1<y, 32>(bg)
; __device__ __forceinline__ bool bg_decode(int st, int wg, int NW, int lane, KP kp, const float*& src, int& ldS, bf16_t*& dst, int& o2) {
;     const int g = st * NW + wg;
;     if (g >= BG_STEPS) { src = kp->in[27] + lane; ldS = 0; dst = nullptr; o2 = 0; return false; }
;     const int l = g / 98304, r = g - l * 98304;
; __device__ __forceinline__ void hy_fft_phase(LAS unsigned char* lds, int bid, int G, const bf16_t* vgT, bf16_t* zT, const float* a3, const float* wout, const float* skip, float* filt, float4* gspec) {
;     ...
;             BG_I(1); fft_r4_pass<true>(z, tid, NTHR); __syncthreads(); BG_F(0);
;             BG_I(0); fft_r16_pass<true, 2>(z, tid); __syncthreads(); BG_F(1); BG_I(1); fft_r16_pass<true, 6>(z, tid); __syncthreads(); BG_F(0); BG_I(0); fft_r16_pass<true, 10>(z, tid); __syncthreads(); BG_F(1);
.LBB0_741:
	s_or_b64 exec, exec, s[48:49]
	s_add_i32 s12, s60, 15
	s_mul_i32 s28, s12, s16
	v_readlane_b32 s44, v254, 0
	s_add_i32 s28, s28, s17
	v_readlane_b32 s45, v254, 1
	s_cmp_lt_i32 s28, 0x20000
	s_mov_b64 s[48:49], -1
	s_cbranch_scc1 .LBB0_743
	s_load_dwordx2 s[48:49], s[44:45], 0xd8
	v_mov_b32_e32 v65, v61
	s_waitcnt lgkmcnt(0)
	v_lshl_add_u64 v[2:3], s[48:49], 0, v[64:65]
	s_mov_b64 s[48:49], 0

; #define BG_I(x) bg_issue1<x>(bg, bgwg, bgNW, bglane)
; #define BG_F(y) bg_finish1<y, 32>(bg)
; __device__ __forceinline__ void hy_fft_phase(LAS unsigned char* lds, int bid, int G, const bf16_t* vgT, bf16_t* zT, const float* a3, const float* wout, const float* skip, float* filt, float4* gspec) {
;     ...
;     { const int nst = (BG_STEPS + bgNW - 1) / bgNW;
;       if (bg.st < nst) { BG_I(0);
; #pragma unroll 1
;         while (bg.st < nst) { BG_I(1); BG_F(0); BG_I(0); BG_F(1); }
;         bg_finish1<0, 0>(bg); } }
.LBB0_775:
	s_abs_i32 s0, s16
	v_cvt_f32_u32_e32 v1, s0
	s_sub_i32 s3, 0, s0
	s_add_i32 s1, s16, 0x1ffff
	s_xor_b32 s2, s1, s16
	v_rcp_iflag_f32_e32 v1, v1
	s_abs_i32 s1, s1
	s_ashr_i32 s2, s2, 31
	v_mul_f32_e32 v1, 0x4f7ffffe, v1
	v_cvt_u32_f32_e32 v1, v1
	s_nop 0
	v_readfirstlane_b32 s4, v1
	s_mul_i32 s3, s3, s4
	s_mul_hi_u32 s3, s4, s3
	s_add_i32 s4, s4, s3
	s_mul_hi_u32 s3, s1, s4
	s_mul_i32 s4, s3, s0
	s_sub_i32 s1, s1, s4
	s_add_i32 s5, s3, 1
	s_sub_i32 s4, s1, s0
	s_cmp_ge_u32 s1, s0
	s_cselect_b32 s3, s5, s3
	s_cselect_b32 s1, s4, s1
	s_add_i32 s4, s3, 1
	s_cmp_ge_u32 s1, s0
	s_cselect_b32 s0, s4, s3
	s_xor_b32 s0, s0, s2
	s_sub_i32 s12, s0, s2
	s_cmp_lt_i32 s60, s12
	s_cbranch_scc0 .LBB0_816
	s_mul_i32 s6, s60, s16
	v_readlane_b32 s0, v254, 0
	s_add_i32 s6, s6, s17
	v_readlane_b32 s1, v254, 1
	s_cmp_lt_i32 s6, 0x20000
	s_cbranch_scc1 .LBB0_779
	s_load_dwordx2 s[2:3], s[0:1], 0xd8
	v_lshlrev_b32_e32 v2, 2, v58
	v_mov_b32_e32 v3, 0
	s_waitcnt lgkmcnt(0)
	v_lshl_add_u64 v[4:5], s[2:3], 0, v[2:3]
	s_cbranch_execz .LBB0_780
	s_mov_b64 s[2:3], 0
	v_mov_b64_e32 v[2:3], 0
	s_mov_b32 s0, 0
	s_branch .LBB0_786

; #define BG_I(x) bg_issue1<x>(bg, bgwg, bgNW, bglane)
; #define BG_F(y) bg_finish1<y, 32>(bg)
; __device__ __forceinline__ void hy_fft_phase(LAS unsigned char* lds, int bid, int G, const bf16_t* vgT, bf16_t* zT, const float* a3, const float* wout, const float* skip, float* filt, float4* gspec) {
;     ...
;       if (bg.st < nst) { BG_I(0);
; #pragma unroll 1
;         while (bg.st < nst) { BG_I(1); BG_F(0); BG_I(0); BG_F(1); }
;         bg_finish1<0, 0>(bg); } }
.LBB0_789:
	v_readlane_b32 s6, v254, 0
	s_add_i32 s1, s14, s17
	v_readlane_b32 s7, v254, 1
	s_mov_b64 s[8:9], -1
	s_cmp_lt_i32 s1, 0x20000
	v_lshlrev_b32_e32 v12, 2, v58
	s_cbranch_scc1 .LBB0_791
	s_load_dwordx2 s[8:9], s[6:7], 0xd8
	v_mov_b32_e32 v13, v5
	s_waitcnt lgkmcnt(0)
	v_lshl_add_u64 v[14:15], s[8:9], 0, v[12:13]
	s_mov_b64 s[8:9], 0

; #define BG_I(x) bg_issue1<x>(bg, bgwg, bgNW, bglane)
; #define BG_F(y) bg_finish1<y, 32>(bg)
; __device__ __forceinline__ void hy_fft_phase(LAS unsigned char* lds, int bid, int G, const bf16_t* vgT, bf16_t* zT, const float* a3, const float* wout, const float* skip, float* filt, float4* gspec) {
;     ...
;       if (bg.st < nst) { BG_I(0);
; #pragma unroll 1
;         while (bg.st < nst) { BG_I(1); BG_F(0); BG_I(0); BG_F(1); }
;         bg_finish1<0, 0>(bg); } }
.LBB0_801:
	s_or_b64 exec, exec, s[8:9]
	v_readlane_b32 s0, v254, 0
	s_add_i32 s7, s22, s17
	v_readlane_b32 s1, v254, 1
	s_cmp_lt_i32 s7, 0x20000
	s_mov_b64 s[8:9], -1
	s_cbranch_scc1 .LBB0_803
	s_load_dwordx2 s[8:9], s[0:1], 0xd8
	v_mov_b32_e32 v13, v5
	s_waitcnt lgkmcnt(0)
	v_lshl_add_u64 v[14:15], s[8:9], 0, v[12:13]
	s_mov_b64 s[8:9], 0

; __device__ __forceinline__ int tid_fresh() { int t = threadIdx.x; asm volatile("" : "+v"(t)); return t; }
;     __device__ __forceinline__ void a_off4(const Unit& u, int r0, int r1, unsigned& o00, unsigned& o01, unsigned& o10, unsigned& o11) const { o00 = a_off(u, r0); o01 = a_off(u, r1); o10 = a_off(u, HALF + r0); o11 = a_off(u, HALF + r1); }
;     __device__ __forceinline__ unsigned b_off(int R, int C) const { return (unsigned)(R * K + C) * 2u; }
;     __device__ __forceinline__ size_t b_kstep() const { return (size_t)(BK * 2); }
;     __device__ __forceinline__ size_t b_hstep() const { return (size_t)HALF * 16; }
; template <class Epi, class Sched>
; __device__ __forceinline__ void gemm_phase(LAS unsigned char* lds, const int K, const Sched& S, const Epi& E) {
;     const int tid = tid_fresh(), wid = __builtin_amdgcn_readfirstlane(tid >> 6), lane = tid & 63, wr = wid >> 2, wc = wid & 3, fr = lane & 15, fq = lane >> 4;
;     const int nt = K / BK;
;     int R0, C0, R1, C1; stage_rc(tid * 16, R0, C0); stage_rc(tid * 16 + 8192, R1, C1);
;     const int Rb0 = Epi::PERM ? ((R0 & ~31) + perm32(R0 & 31)) : R0, Rb1 = Epi::PERM ? ((R1 & ~31) + perm32(R1 & 31)) : R1;
;     const unsigned voffB0 = S.b_off(Rb0, C0), voffB1 = S.b_off(Rb1, C1);
;     const size_t kstep = (size_t)(BK * 2);
;     const size_t kstepB = S.b_kstep(), hstep = S.b_hstep();
;     const unsigned ldsw = (unsigned)wid * 1024u;
;     const int aoff = lds_byte(wr * 64 + fr, fq * 8), boff = lds_byte(wc * 32 + fr, fq * 8);
;     __device__ __forceinline__ void a_off4(const Unit& u, int r0, int r1, unsigned& o00, unsigned& o01, unsigned& o10, unsigned& o11) const {
;         const int p0 = u.pm * BM + r0, p1 = u.pm * BM + r1, p2 = p0 + HALF, p3 = p1 + HALF;
;         if (u.e >= NE) { o00 = (unsigned)p0 * (unsigned)(D * 2); o01 = (unsigned)p1 * (unsigned)(D * 2); o10 = (unsigned)p2 * (unsigned)(D * 2); o11 = (unsigned)p3 * (unsigned)(D * 2); return; }
;         const int* lp = list + u.e * T;
;         int v0 = lp[p0], v1 = lp[p1], v2 = lp[p2], v3 = lp[p3];
;         asm volatile("" : "+v"(v0), "+v"(v1), "+v"(v2), "+v"(v3));
;         const int c = cnt[u.e];
;         o00 = p0 < c ? (unsigned)v0 * (unsigned)(D * 2) : 0u; o01 = p1 < c ? (unsigned)v1 * (unsigned)(D * 2) : 0u;
;         o10 = p2 < c ? (unsigned)v2 * (unsigned)(D * 2) : 0u; o11 = p3 < c ? (unsigned)v3 * (unsigned)(D * 2) : 0u;
;     }
.LBB0_1077:
	s_or_b64 exec, exec, s[0:1]
	v_readlane_b32 s2, v254, 5
	v_readlane_b32 s0, v254, 0
	s_and_b32 s3, s2, 3
	v_readlane_b32 s1, v254, 1
	s_lshl_b32 s29, s28, 2
	v_writelane_b32 v254, s3, 27
	s_lshl_b32 s3, s3, 12
	v_mov_b32_e32 v6, v0
	s_waitcnt lgkmcnt(0)
	s_barrier
	v_readlane_b32 s84, v254, 0
	v_readlane_b32 s85, v254, 1
	s_nop 1
	s_load_dwordx2 s[74:75], s[84:85], 0xd8
	s_load_dwordx2 s[76:77], s[84:85], 0xe0
	s_load_dwordx2 s[78:79], s[84:85], 0x118
	v_and_b32_e32 v248, 63, v0
	v_lshrrev_b32_e32 v250, 6, v0
	v_lshlrev_b32_e32 v249, 4, v248
	v_lshlrev_b32_e32 v248, 2, v248
	v_readlane_b32 s86, v254, 4
	v_readlane_b32 s87, v255, 40
	v_readfirstlane_b32 s88, v250
	s_nop 3
	s_lshl_b32 s71, s86, 3
	s_sub_u32 s71, s71, 1
	s_lshl_b32 s71, s71, 2
	s_lshl_b32 s87, s87, 3
	s_add_u32 s87, s87, s88
	s_add_u32 s87, s87, 0x20000
	s_lshl_b32 s70, s87, 2
	s_mov_b32 s82, 0
	s_waitcnt lgkmcnt(0)
	v_writelane_b32 v255, s3, 24
	s_cmp_lt_i32 s2, s29
	s_nop 0
	v_readfirstlane_b32 s30, v6
	s_cbranch_scc0 .LBB0_1099
	v_ashrrev_i32_e32 v1, 31, v6
	v_lshrrev_b32_e32 v1, 26, v1
	v_add_u32_e32 v1, v6, v1
	v_ashrrev_i32_e32 v9, 6, v1
	v_bfe_i32 v1, v6, 27, 1
	v_lshlrev_b32_e32 v2, 4, v6
	v_lshrrev_b32_e32 v1, 22, v1
	v_add_u32_e32 v1, v2, v1
	v_and_b32_e32 v1, 0xfffffc00, v1
	v_sub_u32_e32 v1, v2, v1
	v_lshrrev_b32_e32 v3, 4, v1
	v_bitop3_b32 v10, v3, v1, 32 bitop3:0x6c
	v_ashrrev_i32_e32 v1, 31, v1
	v_lshrrev_b32_e32 v1, 26, v1
	s_load_dwordx2 s[0:1], s[0:1], 0x118
	v_lshlrev_b32_e32 v3, 3, v9
	v_add_u32_e32 v1, v10, v1
	v_and_b32_e32 v3, -16, v3
	v_ashrrev_i32_e32 v8, 6, v1
	v_add_u32_e32 v2, 0x2000, v2
	v_add_u32_e32 v1, v8, v3
	v_ashrrev_i32_e32 v3, 31, v2
	v_lshrrev_b32_e32 v3, 22, v3
	v_add_u32_e32 v3, v2, v3
	s_waitcnt lgkmcnt(0)
	s_add_u32 s31, s0, 0x3ec30000
	v_ashrrev_i32_e32 v11, 10, v3
	v_readlane_b32 s3, v254, 5
	s_addc_u32 s33, s1, 0
	v_mul_i32_i24_e32 v3, 0x400, v11
	s_and_b32 s2, s3, -4
	v_sub_u32_e32 v2, v2, v3
	s_add_i32 s2, s2, 0
	v_lshrrev_b32_e32 v3, 4, v2
	s_add_i32 s2, s2, 0x21160
	v_bitop3_b32 v12, v3, v2, 32 bitop3:0x6c
	v_mov_b32_e32 v3, s2
	ds_read_b32 v3, v3
	v_ashrrev_i32_e32 v4, 31, v12
	v_lshrrev_b32_e32 v4, 26, v4
	v_lshlrev_b32_e32 v2, 3, v11
	v_add_u32_e32 v4, v12, v4
	s_waitcnt lgkmcnt(0)
	v_lshlrev_b32_e32 v5, 2, v3
	v_add_u32_e32 v5, 0, v5
	v_add_u32_e32 v5, 0x21040, v5
	ds_read_b32 v5, v5
	v_and_b32_e32 v2, -16, v2
	v_ashrrev_i32_e32 v13, 6, v4
	s_ashr_i32 s8, s3, 2
	v_add_u32_e32 v146, v13, v2
	s_waitcnt lgkmcnt(0)
	v_sub_u32_e32 v2, s8, v5
	v_lshlrev_b32_e32 v7, 8, v2
	v_add_u32_e32 v2, v7, v1
	v_add_u32_e32 v4, v7, v146
	v_cmp_gt_i32_e32 vcc, 64, v3
	v_readfirstlane_b32 s6, v3
	v_add_u32_e32 v14, 0x80, v2
	v_add_u32_e32 v15, 0x80, v4
	s_cbranch_vccz .LBB0_1080
	s_lshl_b32 s2, s6, 13
	s_ashr_i32 s3, s2, 31
	s_lshl_b64 s[2:3], s[2:3], 2
	s_add_u32 s2, s31, s2
	s_addc_u32 s3, s33, s3
	v_ashrrev_i32_e32 v3, 31, v2
	v_lshl_add_u64 v[16:17], v[2:3], 2, s[2:3]
	v_ashrrev_i32_e32 v5, 31, v4
	v_lshl_add_u64 v[18:19], v[4:5], 2, s[2:3]
	global_load_dword v3, v[16:17], off
	global_load_dword v5, v[18:19], off
	global_load_dword v20, v[18:19], off offset:512
	global_load_dword v21, v[16:17], off offset:512
	s_lshl_b32 s2, s6, 2
	s_add_i32 s2, s2, 0
	s_add_i32 s2, s2, 0x21660
	v_mov_b32_e32 v16, s2
	s_waitcnt vmcnt(0)
	ds_read_b32 v17, v16
	v_lshlrev_b32_e32 v3, 12, v3
	v_lshlrev_b32_e32 v5, 12, v5
	v_lshlrev_b32_e32 v16, 12, v21
	v_lshlrev_b32_e32 v18, 12, v20
	s_waitcnt lgkmcnt(0)
	v_cmp_lt_i32_e32 vcc, v2, v17
	s_nop 1
	v_cndmask_b32_e32 v3, 0, v3, vcc
	v_cmp_lt_i32_e32 vcc, v4, v17
	s_nop 1
	v_cndmask_b32_e32 v5, 0, v5, vcc
	v_cmp_lt_i32_e32 vcc, v14, v17
	s_nop 1
	v_cndmask_b32_e32 v16, 0, v16, vcc
	v_cmp_lt_i32_e32 vcc, v15, v17
	s_nop 1
	v_cndmask_b32_e32 v17, 0, v18, vcc
	s_cbranch_execz .LBB0_1081
	s_branch .LBB0_1082

; #define PG8_STAGE(bufoff, gbase, v0, v1) do { \
;         __builtin_amdgcn_global_load_lds((const unsigned*)((const char*)(gbase) + (v0)), (LAS unsigned*)(lds + (bufoff) + ldsw), 16, 0, 0); \
;         __builtin_amdgcn_global_load_lds((const unsigned*)((const char*)(gbase) + (v1)), (LAS unsigned*)(lds + (bufoff) + ldsw + 8192), 16, 0, 0); } while (0)
; #define PG8_LDA(dst, b, h) do { _Pragma("unroll") for (int m = 0; m < 4; ++m) _Pragma("unroll") for (int k = 0; k < 2; ++k) dst[m][k] = *(const LAS bf16x8*)(lds + PG8_SA(b, h) + aoff + m * 2048 + k * 1024); } while (0)
; #define PG8_LDB(dst, b, h) do { _Pragma("unroll") for (int n = 0; n < 2; ++n) _Pragma("unroll") for (int k = 0; k < 2; ++k) dst[n][k] = *(const LAS bf16x8*)(lds + PG8_SB(b, h) + boff + n * 2048 + k * 1024); } while (0)
; #define PG8_MMA(ai, bj, At, Bt) do { __builtin_amdgcn_s_setprio(1); _Pragma("unroll") for (int m = 0; m < 4; ++m) _Pragma("unroll") for (int n = 0; n < 2; ++n) _Pragma("unroll") for (int k = 0; k < 2; ++k) \
;         acc[ai][bj][m][n] = __builtin_amdgcn_mfma_f32_16x16x32_bf16(Bt[n][k], At[m][k], acc[ai][bj][m][n], 0, 0, 0); __builtin_amdgcn_s_setprio(0); } while (0)
; #define PG8_WAIT_V(n) asm volatile("s_waitcnt vmcnt(" #n ")" ::: "memory")
; #define PG8_WAIT_L(n) asm volatile("s_waitcnt lgkmcnt(" #n ")" ::: "memory")
; #define PG8_BAR __builtin_amdgcn_s_barrier()
; #define PG8_SCHED __builtin_amdgcn_sched_barrier(0)
; template <class Epi, class Sched>
; __device__ __forceinline__ void gemm_phase(LAS unsigned char* lds, const int K, const Sched& S, const Epi& E) {
;     ...
;             PG8_LDB(B0, 0, 0); PG8_SCHED; PG8_LDA(At, 0, 0); PG8_STAGE(PG8_SA(1, 1), a1, c10, c11);
;             PG8_WAIT_L(8); PG8_BAR; PG8_WAIT_L(0); PG8_MMA(0, 0, At, B0); PG8_BAR; PG8_SCHED;
;             PG8_LDB(B1, 0, 1); PG8_STAGE(PG8_SB(0, 0), b2, voffB0, voffB1);
;             PG8_BAR; PG8_WAIT_L(0); PG8_MMA(0, 1, At, B1); PG8_BAR;
;             PG8_LDA(At, 0, 1); PG8_STAGE(PG8_SA(0, 0), a2, x00, x01);
;             PG8_BAR; PG8_WAIT_L(0); PG8_MMA(1, 0, At, B0); PG8_BAR; PG8_SCHED;
;             PG8_STAGE(PG8_SB(0, 1), b2 + hstep, voffB0, voffB1);
;             PG8_WAIT_V(6); PG8_BAR; PG8_MMA(1, 1, At, B1); PG8_BAR;
.LBB0_1094:
	v_add_u32_e32 v139, s46, v149
	s_add_u32 s22, s0, s20
	ds_read_b128 v[160:163], v139
	ds_read_b128 v[164:167], v139 offset:1024
	ds_read_b128 v[168:171], v139 offset:2048
	ds_read_b128 v[172:175], v139 offset:3072
	s_addc_u32 s23, s1, s21
	s_add_u32 s24, s22, 0x34c30100
	s_addc_u32 s25, s23, 0
	s_cmpk_eq_i32 s20, 0xf00
	s_cselect_b64 vcc, -1, 0
	s_and_b64 s[22:23], vcc, exec
	v_cndmask_b32_e32 v134, v158, v156, vcc
	s_cselect_b32 s27, s3, s25
	s_cselect_b32 s26, s2, s24
	v_cndmask_b32_e32 v139, v138, v154, vcc
	s_cselect_b32 s23, s19, s15
	s_cselect_b32 s22, s18, s13
	v_cndmask_b32_e32 v204, v136, v155, vcc
	s_add_u32 s24, s22, 0x20000
	s_addc_u32 s25, s23, 0
	v_lshl_add_u64 v[206:207], v[144:145], 0, s[20:21]
	s_add_i32 m0, s37, 0xc000
	ds_read_b128 v[176:179], v151
	ds_read_b128 v[180:183], v151 offset:1024
	ds_read_b128 v[184:187], v151 offset:2048
	ds_read_b128 v[188:191], v151 offset:3072
	ds_read_b128 v[192:195], v151 offset:4096
	ds_read_b128 v[196:199], v151 offset:5120
	ds_read_b128 v[200:203], v151 offset:6144
	ds_read_b128 v[208:211], v151 offset:7168
	global_load_lds_dwordx4 v[206:207], off
	v_lshl_add_u64 v[206:207], v[142:143], 0, s[20:21]
	s_add_i32 m0, s37, 0xe000
	s_nop 0
	global_load_lds_dwordx4 v[206:207], off
	s_waitcnt lgkmcnt(8)
	s_barrier
	s_waitcnt lgkmcnt(0)
	s_setprio 1
	s_waitcnt lgkmcnt(0)
	v_mfma_f32_16x16x32_bf16 v[126:129], v[160:163], v[176:179], v[126:129]
	v_mfma_f32_16x16x32_bf16 v[122:125], v[168:171], v[176:179], v[122:125]
	v_mfma_f32_16x16x32_bf16 v[110:113], v[160:163], v[184:187], v[110:113]
	v_mfma_f32_16x16x32_bf16 v[106:109], v[168:171], v[184:187], v[106:109]
	v_mfma_f32_16x16x32_bf16 v[94:97], v[160:163], v[192:195], v[94:97]
	v_mfma_f32_16x16x32_bf16 v[90:93], v[168:171], v[192:195], v[90:93]
	v_mfma_f32_16x16x32_bf16 v[78:81], v[160:163], v[200:203], v[78:81]
	v_mfma_f32_16x16x32_bf16 v[74:77], v[168:171], v[200:203], v[74:77]
	v_mfma_f32_16x16x32_bf16 v[126:129], v[164:167], v[180:183], v[126:129]
	v_mfma_f32_16x16x32_bf16 v[122:125], v[172:175], v[180:183], v[122:125]
	v_mfma_f32_16x16x32_bf16 v[110:113], v[164:167], v[188:191], v[110:113]
	v_mfma_f32_16x16x32_bf16 v[106:109], v[172:175], v[188:191], v[106:109]
	v_mfma_f32_16x16x32_bf16 v[94:97], v[164:167], v[196:199], v[94:97]
	v_mfma_f32_16x16x32_bf16 v[90:93], v[172:175], v[196:199], v[90:93]
	v_mfma_f32_16x16x32_bf16 v[78:81], v[164:167], v[208:211], v[78:81]
	v_mfma_f32_16x16x32_bf16 v[74:77], v[172:175], v[208:211], v[74:77]
	s_setprio 0
	s_barrier
	s_add_i32 s55, s46, s36
	v_add_u32_e32 v141, s48, v149
	v_lshl_add_u64 v[206:207], s[22:23], 0, v[130:131]
	s_mov_b32 m0, s55
	ds_read_b128 v[212:215], v141
	ds_read_b128 v[216:219], v141 offset:1024
	ds_read_b128 v[220:223], v141 offset:2048
	ds_read_b128 v[224:227], v141 offset:3072
	global_load_lds_dwordx4 v[206:207], off
	v_lshl_add_u64 v[228:229], s[22:23], 0, v[132:133]
	s_add_i32 m0, s55, 0x2000
	s_nop 0
	global_load_lds_dwordx4 v[228:229], off
	s_barrier
	s_waitcnt lgkmcnt(0)
	s_setprio 1
	s_waitcnt lgkmcnt(0)
	v_mfma_f32_16x16x32_bf16 v[118:121], v[212:215], v[176:179], v[118:121]
	v_mfma_f32_16x16x32_bf16 v[114:117], v[220:223], v[176:179], v[114:117]
	v_mfma_f32_16x16x32_bf16 v[102:105], v[212:215], v[184:187], v[102:105]
	v_mfma_f32_16x16x32_bf16 v[98:101], v[220:223], v[184:187], v[98:101]
	v_mfma_f32_16x16x32_bf16 v[86:89], v[212:215], v[192:195], v[86:89]
	v_mfma_f32_16x16x32_bf16 v[82:85], v[220:223], v[192:195], v[82:85]
	v_mfma_f32_16x16x32_bf16 v[70:73], v[212:215], v[200:203], v[70:73]
	v_mfma_f32_16x16x32_bf16 v[66:69], v[220:223], v[200:203], v[66:69]
	v_mfma_f32_16x16x32_bf16 v[118:121], v[216:219], v[180:183], v[118:121]
	v_mfma_f32_16x16x32_bf16 v[114:117], v[224:227], v[180:183], v[114:117]
	v_mfma_f32_16x16x32_bf16 v[102:105], v[216:219], v[188:191], v[102:105]
	v_mfma_f32_16x16x32_bf16 v[98:101], v[224:227], v[188:191], v[98:101]
	v_mfma_f32_16x16x32_bf16 v[86:89], v[216:219], v[196:199], v[86:89]
	v_mfma_f32_16x16x32_bf16 v[82:85], v[224:227], v[196:199], v[82:85]
	v_mfma_f32_16x16x32_bf16 v[70:73], v[216:219], v[208:211], v[70:73]
	v_mfma_f32_16x16x32_bf16 v[66:69], v[224:227], v[208:211], v[66:69]
	s_setprio 0
	s_mov_b32 m0, s37
	s_barrier
	ds_read_b128 v[176:179], v151 offset:16384
	ds_read_b128 v[180:183], v151 offset:17408
	ds_read_b128 v[184:187], v151 offset:18432
	ds_read_b128 v[188:191], v151 offset:19456
	ds_read_b128 v[192:195], v151 offset:20480
	ds_read_b128 v[196:199], v151 offset:21504
	ds_read_b128 v[200:203], v151 offset:22528
	ds_read_b128 v[208:211], v151 offset:23552
	global_load_lds_dwordx4 v134, s[26:27]
	s_mov_b32 m0, s38
	v_mov_b32_e32 v205, v135
	global_load_lds_dwordx4 v204, s[26:27]
	s_barrier
	s_waitcnt lgkmcnt(0)
	v_lshl_add_u64 v[230:231], s[26:27], 0, v[134:135]
	v_lshl_add_u64 v[204:205], s[26:27], 0, v[204:205]
	s_setprio 1
	s_waitcnt lgkmcnt(0)
	v_mfma_f32_16x16x32_bf16 v[62:65], v[160:163], v[176:179], v[62:65]
	v_mfma_f32_16x16x32_bf16 v[58:61], v[168:171], v[176:179], v[58:61]
	v_mfma_f32_16x16x32_bf16 v[46:49], v[160:163], v[184:187], v[46:49]
	v_mfma_f32_16x16x32_bf16 v[42:45], v[168:171], v[184:187], v[42:45]
	v_mfma_f32_16x16x32_bf16 v[30:33], v[160:163], v[192:195], v[30:33]
	v_mfma_f32_16x16x32_bf16 v[26:29], v[168:171], v[192:195], v[26:29]
	v_mfma_f32_16x16x32_bf16 v[14:17], v[160:163], v[200:203], v[14:17]
	v_mfma_f32_16x16x32_bf16 v[10:13], v[168:171], v[200:203], v[10:13]
	v_mfma_f32_16x16x32_bf16 v[62:65], v[164:167], v[180:183], v[62:65]
	v_mfma_f32_16x16x32_bf16 v[58:61], v[172:175], v[180:183], v[58:61]
	v_mfma_f32_16x16x32_bf16 v[46:49], v[164:167], v[188:191], v[46:49]
	v_mfma_f32_16x16x32_bf16 v[42:45], v[172:175], v[188:191], v[42:45]
	v_mfma_f32_16x16x32_bf16 v[30:33], v[164:167], v[196:199], v[30:33]
	v_mfma_f32_16x16x32_bf16 v[26:29], v[172:175], v[196:199], v[26:29]
	v_mfma_f32_16x16x32_bf16 v[14:17], v[164:167], v[208:211], v[14:17]
	v_mfma_f32_16x16x32_bf16 v[10:13], v[172:175], v[208:211], v[10:13]
	s_setprio 0
	s_barrier
; #define PG8_STAGE(bufoff, gbase, v0, v1) do { \
;         __builtin_amdgcn_global_load_lds((const unsigned*)((const char*)(gbase) + (v0)), (LAS unsigned*)(lds + (bufoff) + ldsw), 16, 0, 0); \
;         __builtin_amdgcn_global_load_lds((const unsigned*)((const char*)(gbase) + (v1)), (LAS unsigned*)(lds + (bufoff) + ldsw + 8192), 16, 0, 0); } while (0)
; #define PG8_LDA(dst, b, h) do { _Pragma("unroll") for (int m = 0; m < 4; ++m) _Pragma("unroll") for (int k = 0; k < 2; ++k) dst[m][k] = *(const LAS bf16x8*)(lds + PG8_SA(b, h) + aoff + m * 2048 + k * 1024); } while (0)
; #define PG8_LDB(dst, b, h) do { _Pragma("unroll") for (int n = 0; n < 2; ++n) _Pragma("unroll") for (int k = 0; k < 2; ++k) dst[n][k] = *(const LAS bf16x8*)(lds + PG8_SB(b, h) + boff + n * 2048 + k * 1024); } while (0)
; #define PG8_MMA(ai, bj, At, Bt) do { __builtin_amdgcn_s_setprio(1); _Pragma("unroll") for (int m = 0; m < 4; ++m) _Pragma("unroll") for (int n = 0; n < 2; ++n) _Pragma("unroll") for (int k = 0; k < 2; ++k) \
;         acc[ai][bj][m][n] = __builtin_amdgcn_mfma_f32_16x16x32_bf16(Bt[n][k], At[m][k], acc[ai][bj][m][n], 0, 0, 0); __builtin_amdgcn_s_setprio(0); } while (0)
; #define PG8_WAIT_V(n) asm volatile("s_waitcnt vmcnt(" #n ")" ::: "memory")
; #define PG8_WAIT_L(n) asm volatile("s_waitcnt lgkmcnt(" #n ")" ::: "memory")
; #define PG8_BAR __builtin_amdgcn_s_barrier()
; #define PG8_SCHED __builtin_amdgcn_sched_barrier(0)
; template <class Epi, class Sched>
; __device__ __forceinline__ void gemm_phase(LAS unsigned char* lds, const int K, const Sched& S, const Epi& E) {
;     ...
;             PG8_WAIT_V(6); PG8_BAR; PG8_MMA(1, 1, At, B1); PG8_BAR;
;             PG8_LDB(B0, 1, 0); PG8_SCHED; PG8_LDA(At, 1, 0); PG8_STAGE(PG8_SA(0, 1), a2, x10, x11);
;             PG8_WAIT_L(8); PG8_BAR; PG8_WAIT_L(0); PG8_MMA(0, 0, At, B0); PG8_BAR; PG8_SCHED;
;             PG8_LDB(B1, 1, 1); PG8_STAGE(PG8_SB(1, 0), b3, voffB0, voffB1);
;             PG8_BAR; PG8_WAIT_L(0); PG8_MMA(0, 1, At, B1); PG8_BAR;
;             PG8_LDA(At, 1, 1); PG8_STAGE(PG8_SA(1, 0), a3, x00, x01);
;             PG8_BAR; PG8_WAIT_L(0); PG8_MMA(1, 0, At, B0); PG8_BAR; PG8_SCHED;
	s_add_i32 s55, s48, s36
	v_lshl_add_u64 v[160:161], v[206:207], 0, s[4:5]
	s_mov_b32 m0, s55
	s_nop 0
	global_load_lds_dwordx4 v[160:161], off
	v_lshl_add_u64 v[160:161], v[228:229], 0, s[4:5]
	s_add_i32 m0, s55, 0x2000
	s_nop 0
	global_load_lds_dwordx4 v[160:161], off
	s_waitcnt vmcnt(6)
	s_barrier
	s_setprio 1
	v_mfma_f32_16x16x32_bf16 v[54:57], v[212:215], v[176:179], v[54:57]
	v_mfma_f32_16x16x32_bf16 v[50:53], v[220:223], v[176:179], v[50:53]
	v_mfma_f32_16x16x32_bf16 v[38:41], v[212:215], v[184:187], v[38:41]
	v_mfma_f32_16x16x32_bf16 v[34:37], v[220:223], v[184:187], v[34:37]
	v_mfma_f32_16x16x32_bf16 v[22:25], v[212:215], v[192:195], v[22:25]
	v_mfma_f32_16x16x32_bf16 v[18:21], v[220:223], v[192:195], v[18:21]
	v_mfma_f32_16x16x32_bf16 v[6:9], v[212:215], v[200:203], v[6:9]
	v_mfma_f32_16x16x32_bf16 v[2:5], v[220:223], v[200:203], v[2:5]
	v_mfma_f32_16x16x32_bf16 v[54:57], v[216:219], v[180:183], v[54:57]
	v_mfma_f32_16x16x32_bf16 v[50:53], v[224:227], v[180:183], v[50:53]
	v_mfma_f32_16x16x32_bf16 v[38:41], v[216:219], v[188:191], v[38:41]
	v_mfma_f32_16x16x32_bf16 v[34:37], v[224:227], v[188:191], v[34:37]
	v_mfma_f32_16x16x32_bf16 v[22:25], v[216:219], v[196:199], v[22:25]
	v_mfma_f32_16x16x32_bf16 v[18:21], v[224:227], v[196:199], v[18:21]
	v_mfma_f32_16x16x32_bf16 v[6:9], v[216:219], v[208:211], v[6:9]
	v_mfma_f32_16x16x32_bf16 v[2:5], v[224:227], v[208:211], v[2:5]
	s_setprio 0
	s_add_i32 s55, 0, 0x18000
	v_add_u32_e32 v134, s55, v149
	s_barrier
	ds_read_b128 v[160:163], v134
	ds_read_b128 v[164:167], v134 offset:1024
	ds_read_b128 v[168:171], v134 offset:2048
	ds_read_b128 v[172:175], v134 offset:3072
	s_mov_b32 m0, s39
	ds_read_b128 v[176:179], v151 offset:32768
	ds_read_b128 v[180:183], v151 offset:33792
	ds_read_b128 v[184:187], v151 offset:34816
	ds_read_b128 v[188:191], v151 offset:35840
	ds_read_b128 v[192:195], v151 offset:36864
	ds_read_b128 v[196:199], v151 offset:37888
	ds_read_b128 v[200:203], v151 offset:38912
	ds_read_b128 v[208:211], v151 offset:39936
	v_cndmask_b32_e32 v134, v140, v153, vcc
	global_load_lds_dwordx4 v139, s[26:27]
	s_mov_b32 m0, s40
	s_nop 0
	global_load_lds_dwordx4 v134, s[26:27]
	s_waitcnt lgkmcnt(8)
	s_barrier
	s_waitcnt lgkmcnt(0)
	s_setprio 1
	s_waitcnt lgkmcnt(0)
	v_mfma_f32_16x16x32_bf16 v[126:129], v[160:163], v[176:179], v[126:129]
	v_mfma_f32_16x16x32_bf16 v[122:125], v[168:171], v[176:179], v[122:125]
	v_mfma_f32_16x16x32_bf16 v[110:113], v[160:163], v[184:187], v[110:113]
	v_mfma_f32_16x16x32_bf16 v[106:109], v[168:171], v[184:187], v[106:109]
	v_mfma_f32_16x16x32_bf16 v[94:97], v[160:163], v[192:195], v[94:97]
	v_mfma_f32_16x16x32_bf16 v[90:93], v[168:171], v[192:195], v[90:93]
	v_mfma_f32_16x16x32_bf16 v[78:81], v[160:163], v[200:203], v[78:81]
	v_mfma_f32_16x16x32_bf16 v[74:77], v[168:171], v[200:203], v[74:77]
	v_mfma_f32_16x16x32_bf16 v[126:129], v[164:167], v[180:183], v[126:129]
	v_mfma_f32_16x16x32_bf16 v[122:125], v[172:175], v[180:183], v[122:125]
	v_mfma_f32_16x16x32_bf16 v[110:113], v[164:167], v[188:191], v[110:113]
	v_mfma_f32_16x16x32_bf16 v[106:109], v[172:175], v[188:191], v[106:109]
	v_mfma_f32_16x16x32_bf16 v[94:97], v[164:167], v[196:199], v[94:97]
	v_mfma_f32_16x16x32_bf16 v[90:93], v[172:175], v[196:199], v[90:93]
	v_mfma_f32_16x16x32_bf16 v[78:81], v[164:167], v[208:211], v[78:81]
	v_mfma_f32_16x16x32_bf16 v[74:77], v[172:175], v[208:211], v[74:77]
	s_setprio 0
	s_barrier
	s_add_i32 s26, 0, 0x1c000
	s_add_i32 s27, s55, s36
	v_add_u32_e32 v134, s26, v149
	v_lshl_add_u64 v[206:207], s[24:25], 0, v[130:131]
	s_mov_b32 m0, s27
	ds_read_b128 v[212:215], v134
	ds_read_b128 v[216:219], v134 offset:1024
	ds_read_b128 v[220:223], v134 offset:2048
	ds_read_b128 v[224:227], v134 offset:3072
	global_load_lds_dwordx4 v[206:207], off
	v_lshl_add_u64 v[206:207], s[24:25], 0, v[132:133]
	s_add_i32 m0, s27, 0x2000
	s_nop 0
	global_load_lds_dwordx4 v[206:207], off
	s_barrier
	s_waitcnt lgkmcnt(0)
	s_setprio 1
	s_waitcnt lgkmcnt(0)
	v_mfma_f32_16x16x32_bf16 v[118:121], v[212:215], v[176:179], v[118:121]
	v_mfma_f32_16x16x32_bf16 v[114:117], v[220:223], v[176:179], v[114:117]
	v_mfma_f32_16x16x32_bf16 v[102:105], v[212:215], v[184:187], v[102:105]
	v_mfma_f32_16x16x32_bf16 v[98:101], v[220:223], v[184:187], v[98:101]
	v_mfma_f32_16x16x32_bf16 v[86:89], v[212:215], v[192:195], v[86:89]
	v_mfma_f32_16x16x32_bf16 v[82:85], v[220:223], v[192:195], v[82:85]
	v_mfma_f32_16x16x32_bf16 v[70:73], v[212:215], v[200:203], v[70:73]
	v_mfma_f32_16x16x32_bf16 v[66:69], v[220:223], v[200:203], v[66:69]
	v_mfma_f32_16x16x32_bf16 v[118:121], v[216:219], v[180:183], v[118:121]
	v_mfma_f32_16x16x32_bf16 v[114:117], v[224:227], v[180:183], v[114:117]
	v_mfma_f32_16x16x32_bf16 v[102:105], v[216:219], v[188:191], v[102:105]
	v_mfma_f32_16x16x32_bf16 v[98:101], v[224:227], v[188:191], v[98:101]
	v_mfma_f32_16x16x32_bf16 v[86:89], v[216:219], v[196:199], v[86:89]
	v_mfma_f32_16x16x32_bf16 v[82:85], v[224:227], v[196:199], v[82:85]
	v_mfma_f32_16x16x32_bf16 v[70:73], v[216:219], v[208:211], v[70:73]
	v_mfma_f32_16x16x32_bf16 v[66:69], v[224:227], v[208:211], v[66:69]
	s_setprio 0
	s_mov_b32 m0, s43
	v_lshl_add_u64 v[206:207], v[230:231], 0, s[10:11]
	s_barrier
	ds_read_b128 v[176:179], v151 offset:49152
	ds_read_b128 v[180:183], v151 offset:50176
	ds_read_b128 v[184:187], v151 offset:51200
	ds_read_b128 v[188:191], v151 offset:52224
	ds_read_b128 v[192:195], v151 offset:53248
	ds_read_b128 v[196:199], v151 offset:54272
	ds_read_b128 v[200:203], v151 offset:55296
	ds_read_b128 v[208:211], v151 offset:56320
	global_load_lds_dwordx4 v[206:207], off
	v_lshl_add_u64 v[204:205], v[204:205], 0, s[10:11]
	s_mov_b32 m0, s44
	s_nop 0
	global_load_lds_dwordx4 v[204:205], off
	s_barrier
; __device__ __forceinline__ unsigned cvt_pk_bf16(float lo, float hi) { unsigned r; asm volatile("v_cvt_pk_bf16_f32 %0, %1, %2" : "=v"(r) : "v"(lo), "v"(hi)); return r; }
; __device__ __forceinline__ bool bg_decode(int st, int wg, int NW, int lane, KP kp, const float*& src, int& ldS, bf16_t*& dst, int& o2) {
;     ...
;     if (r < 65536) {
;         const int e = r >> 10, kc = (r >> 2) & 255, kind = (r >> 1) & 1, cc = r & 1, n = cc * 256 + lane;
;         ldS = FF; o2 = 256 * 8;
;         src = kp->in[27 + kind] + ((size_t)(l * NE + e) * D + kc * 8) * FF + n;
;         const int drow = (n >> 7) * 256 + kind * 128 + (n & 127);
;         dst = (bf16_t*)(ws + WS_WGU) + l * WGU_L + (size_t)e * 1024 * D + ((size_t)kc * 1024 + drow) * 8;
; template <int BANK, int WAITN> __device__ __forceinline__ void bg_finish1(BgState& b) {
;     if (WAITN == 32) asm volatile("s_waitcnt vmcnt(32)" ::: "memory"); else asm volatile("s_waitcnt vmcnt(0)" ::: "memory");
;     asm volatile("" : BG_TIE16(BANK * 32) :: "memory");
;     asm volatile("" : BG_TIE16(BANK * 32 + 16) :: "memory");
;     bf16_t* dst = b.dst[BANK];
;     if (dst != nullptr) {
; #pragma unroll
;         for (int c = 0; c < 4; ++c) { u32x4 w;
;             w.x = cvt_pk_bf16(b.r[(BANK * 8 + 0) * 4 + c], b.r[(BANK * 8 + 1) * 4 + c]); w.y = cvt_pk_bf16(b.r[(BANK * 8 + 2) * 4 + c], b.r[(BANK * 8 + 3) * 4 + c]);
;             w.z = cvt_pk_bf16(b.r[(BANK * 8 + 4) * 4 + c], b.r[(BANK * 8 + 5) * 4 + c]); w.w = cvt_pk_bf16(b.r[(BANK * 8 + 6) * 4 + c], b.r[(BANK * 8 + 7) * 4 + c]);
;             bf16_t* dp = dst + (c & 1) * 512 + (c >> 1) * b.o2[BANK];
;             asm volatile("global_store_dwordx4 %0, %1, off\n\ts_nop 1" :: "v"(dp), "v"(w) : "memory"); }
;     }
	s_waitcnt lgkmcnt(0)
	s_setprio 1
	s_waitcnt lgkmcnt(0)
	v_mfma_f32_16x16x32_bf16 v[62:65], v[160:163], v[176:179], v[62:65]
	v_mfma_f32_16x16x32_bf16 v[58:61], v[168:171], v[176:179], v[58:61]
	v_mfma_f32_16x16x32_bf16 v[46:49], v[160:163], v[184:187], v[46:49]
	v_mfma_f32_16x16x32_bf16 v[42:45], v[168:171], v[184:187], v[42:45]
	v_mfma_f32_16x16x32_bf16 v[30:33], v[160:163], v[192:195], v[30:33]
	v_mfma_f32_16x16x32_bf16 v[26:29], v[168:171], v[192:195], v[26:29]
	v_mfma_f32_16x16x32_bf16 v[14:17], v[160:163], v[200:203], v[14:17]
	v_mfma_f32_16x16x32_bf16 v[10:13], v[168:171], v[200:203], v[10:13]
	v_mfma_f32_16x16x32_bf16 v[62:65], v[164:167], v[180:183], v[62:65]
	v_mfma_f32_16x16x32_bf16 v[58:61], v[172:175], v[180:183], v[58:61]
	v_mfma_f32_16x16x32_bf16 v[46:49], v[164:167], v[188:191], v[46:49]
	v_mfma_f32_16x16x32_bf16 v[42:45], v[172:175], v[188:191], v[42:45]
	v_mfma_f32_16x16x32_bf16 v[30:33], v[164:167], v[196:199], v[30:33]
	v_mfma_f32_16x16x32_bf16 v[26:29], v[172:175], v[196:199], v[26:29]
	v_mfma_f32_16x16x32_bf16 v[14:17], v[164:167], v[208:211], v[14:17]
	v_mfma_f32_16x16x32_bf16 v[10:13], v[172:175], v[208:211], v[10:13]
	s_setprio 0
	s_barrier
	s_add_u32 s22, s22, 0x20800
	s_addc_u32 s23, s23, 0
	s_add_i32 s24, s26, s36
	v_lshl_add_u64 v[160:161], s[22:23], 0, v[130:131]
	s_mov_b32 m0, s24
	s_nop 0
	global_load_lds_dwordx4 v[160:161], off
	v_lshl_add_u64 v[160:161], s[22:23], 0, v[132:133]
	s_add_i32 m0, s24, 0x2000
	s_nop 0
	global_load_lds_dwordx4 v[160:161], off
	s_mov_b32 s83, 0
	s_cmp_eq_u32 s82, 0
	s_cbranch_scc1 .Lpb0_l1
	s_waitcnt vmcnt(8)
	v_cvt_pk_bf16_f32 v244, v236, v237
	v_cvt_pk_bf16_f32 v245, v238, v239
	v_cvt_pk_bf16_f32 v246, v240, v241
	v_cvt_pk_bf16_f32 v247, v242, v243
	global_store_dwordx4 v249, v[244:247], s[80:81]
	s_mov_b32 s82, 0
	s_mov_b32 s83, 1
.Lpb0_l1:
	s_cmp_ge_u32 s70, 0xa0000
	s_cbranch_scc1 .Lpb0_l2
	s_lshr_b32 s84, s70, 2
	s_sub_u32 s84, s84, 0x18000
	s_lshr_b32 s85, s84, 10
	s_lshl_b32 s85, s85, 22
	s_bfe_u32 s86, s84, 0x80002
	s_lshl_b32 s86, s86, 14
	s_add_u32 s85, s85, s86
	s_and_b32 s86, s84, 1
	s_and_b32 s87, s70, 3
	s_lshl_b32 s88, s86, 10
	s_lshl_b32 s89, s87, 8
	s_add_u32 s88, s88, s89
	s_add_u32 s88, s88, s85
	s_add_u32 s88, s88, 0x10000000
	s_bitcmp1_b32 s84, 1
	s_cselect_b64 s[72:73], s[76:77], s[74:75]
	s_add_u32 s72, s72, s88
	s_addc_u32 s73, s73, 0
	s_lshl_b32 s88, s86, 13
	s_add_u32 s88, s88, s85
	s_lshr_b32 s89, s87, 1
	s_lshl_b32 s89, s89, 12
	s_add_u32 s88, s88, s89
	s_and_b32 s89, s87, 1
	s_lshl_b32 s89, s89, 10
	s_add_u32 s88, s88, s89
	s_bfe_u32 s89, s84, 0x10001
	s_lshl_b32 s89, s89, 11
	s_add_u32 s88, s88, s89
	s_add_u32 s88, s88, 0x14430000
	s_add_u32 s80, s78, s88
	s_addc_u32 s81, s79, 0
	global_load_dword v236, v248, s[72:73]
	global_load_dword v237, v248, s[72:73] offset:2048
	s_add_u32 s72, s72, 0x1000
	s_addc_u32 s73, s73, 0
	global_load_dword v238, v248, s[72:73]
	global_load_dword v239, v248, s[72:73] offset:2048
	s_add_u32 s72, s72, 0x1000
	s_addc_u32 s73, s73, 0
	global_load_dword v240, v248, s[72:73]
	global_load_dword v241, v248, s[72:73] offset:2048
	s_add_u32 s72, s72, 0x1000
	s_addc_u32 s73, s73, 0
	global_load_dword v242, v248, s[72:73]
	global_load_dword v243, v248, s[72:73] offset:2048
	s_add_u32 s70, s70, 1
	s_and_b32 s84, s70, 3
	s_cmp_eq_u32 s84, 0
	s_cselect_b32 s84, s71, 0
	s_add_u32 s70, s70, s84
	s_mov_b32 s82, 1
	s_add_u32 s83, s83, 8
.Lpb0_l2:
	s_cmp_eq_u32 s83, 9
	s_cbranch_scc1 .Lpb0_w15
	s_cmp_eq_u32 s83, 8
	s_cbranch_scc1 .Lpb0_w14
	s_cmp_eq_u32 s83, 1
	s_cbranch_scc1 .Lpb0_w7
	s_waitcnt vmcnt(6)
	s_branch .Lpb0_j
.Lpb0_w15:
	s_waitcnt vmcnt(15)
	s_branch .Lpb0_j
.Lpb0_w14:
	s_waitcnt vmcnt(14)
	s_branch .Lpb0_j
.Lpb0_w7:
	s_waitcnt vmcnt(7)
.Lpb0_j:
	s_barrier
	s_setprio 1
	v_mfma_f32_16x16x32_bf16 v[54:57], v[212:215], v[176:179], v[54:57]
	v_mfma_f32_16x16x32_bf16 v[50:53], v[220:223], v[176:179], v[50:53]
	v_mfma_f32_16x16x32_bf16 v[38:41], v[212:215], v[184:187], v[38:41]
	v_mfma_f32_16x16x32_bf16 v[34:37], v[220:223], v[184:187], v[34:37]
	v_mfma_f32_16x16x32_bf16 v[22:25], v[212:215], v[192:195], v[22:25]
	v_mfma_f32_16x16x32_bf16 v[18:21], v[220:223], v[192:195], v[18:21]
	v_mfma_f32_16x16x32_bf16 v[6:9], v[212:215], v[200:203], v[6:9]
	v_mfma_f32_16x16x32_bf16 v[2:5], v[220:223], v[200:203], v[2:5]
	v_mfma_f32_16x16x32_bf16 v[54:57], v[216:219], v[180:183], v[54:57]
	v_mfma_f32_16x16x32_bf16 v[50:53], v[224:227], v[180:183], v[50:53]
	v_mfma_f32_16x16x32_bf16 v[38:41], v[216:219], v[188:191], v[38:41]
	v_mfma_f32_16x16x32_bf16 v[34:37], v[224:227], v[188:191], v[34:37]
	v_mfma_f32_16x16x32_bf16 v[22:25], v[216:219], v[196:199], v[22:25]
	v_mfma_f32_16x16x32_bf16 v[18:21], v[224:227], v[196:199], v[18:21]
	v_mfma_f32_16x16x32_bf16 v[6:9], v[216:219], v[208:211], v[6:9]
	v_mfma_f32_16x16x32_bf16 v[2:5], v[224:227], v[208:211], v[2:5]
	s_setprio 0
	s_add_i32 s54, s54, 2
	s_add_u32 s13, s13, 0x40000
	s_addc_u32 s15, s15, 0
	s_add_u32 s20, s20, 0x100
	s_addc_u32 s21, s21, 0
	s_cmp_gt_u32 s54, 29
	s_barrier
	s_cbranch_scc0 .LBB0_1094
; __device__ __forceinline__ unsigned cvt_pk_bf16(float lo, float hi) { unsigned r; asm volatile("v_cvt_pk_bf16_f32 %0, %1, %2" : "=v"(r) : "v"(lo), "v"(hi)); return r; }
; __device__ __forceinline__ float fdivf(float a, float b) { return a * __builtin_amdgcn_rcpf(b); }
;     __device__ __forceinline__ void operator()(const f32x4 (&acc)[2][2][4][2], const Unit& u, int wr, int wc, int fr, int fq) const {
;         const int row0 = u.rbase + wr * 64 + fr, col0 = u.pn * HALF + wc * 32 + 8 * fq;
; #pragma unroll
;         for (int ai = 0; ai < 2; ++ai)
; #pragma unroll
;             for (int m = 0; m < 4; ++m) { bf16_t* rowp = O + (size_t)(row0 + ai * HALF + m * 16) * FF + col0;
;                 float h[8];
; #pragma unroll
;                 for (int n = 0; n < 2; ++n)
; #pragma unroll
;                     for (int j = 0; j < 4; ++j) { const float g = acc[ai][0][m][n][j], up = acc[ai][1][m][n][j]; h[n * 4 + j] = fdivf(g, 1.f + __expf(-g)) * up; }
;                 u32x4 w; w.x = cvt_pk_bf16(h[0], h[1]); w.y = cvt_pk_bf16(h[2], h[3]); w.z = cvt_pk_bf16(h[4], h[5]); w.w = cvt_pk_bf16(h[6], h[7]);
;                 *(u32x4*)rowp = w; }
;     }
	v_mul_f32_e32 v134, 0xbfb8aa3b, v126
	v_exp_f32_e32 v134, v134
	v_mul_f32_e32 v136, 0xbfb8aa3b, v127
	v_exp_f32_e32 v136, v136
	v_add_u32_e32 v138, v157, v137
	v_add_f32_e32 v134, 1.0, v134
	v_rcp_f32_e32 v134, v134
	v_add_f32_e32 v136, 1.0, v136
	v_rcp_f32_e32 v136, v136
	v_ashrrev_i32_e32 v139, 31, v138
	v_mul_f32_e32 v126, v126, v134
	v_mul_f32_e32 v118, v126, v118
	v_mul_f32_e32 v126, v127, v136
	v_mul_f32_e32 v127, 0xbfb8aa3b, v128
	v_exp_f32_e32 v127, v127
	v_mul_f32_e32 v134, 0xbfb8aa3b, v129
	v_exp_f32_e32 v134, v134
	v_mul_f32_e32 v119, v126, v119
	v_add_f32_e32 v126, 1.0, v127
	v_rcp_f32_e32 v126, v126
	v_add_f32_e32 v127, 1.0, v134
	v_mul_f32_e32 v134, 0xbfb8aa3b, v122
	v_rcp_f32_e32 v127, v127
	v_exp_f32_e32 v134, v134
	v_mul_f32_e32 v126, v128, v126
	v_mul_f32_e32 v120, v126, v120
	v_mul_f32_e32 v126, v129, v127
	v_add_f32_e32 v127, 1.0, v134
	v_rcp_f32_e32 v127, v127
	v_mul_f32_e32 v128, 0xbfb8aa3b, v123
	v_exp_f32_e32 v128, v128
	v_mul_f32_e32 v121, v126, v121
	v_mul_f32_e32 v122, v122, v127
	v_mul_f32_e32 v122, v122, v114
	v_add_f32_e32 v114, 1.0, v128
	v_mul_f32_e32 v126, 0xbfb8aa3b, v124
	v_rcp_f32_e32 v114, v114
	v_exp_f32_e32 v126, v126
	v_mul_f32_e32 v127, 0xbfb8aa3b, v125
	v_exp_f32_e32 v127, v127
	v_mul_f32_e32 v114, v123, v114
	v_add_f32_e32 v123, 1.0, v126
	v_rcp_f32_e32 v123, v123
	v_add_f32_e32 v126, 1.0, v127
	v_rcp_f32_e32 v126, v126
	v_mul_f32_e32 v127, v114, v115
	v_mul_f32_e32 v114, v124, v123
	v_mul_f32_e32 v123, v114, v116
	v_mul_f32_e32 v114, v125, v126
	v_cvt_pk_bf16_f32 v116, v118, v119
	v_mul_f32_e32 v119, 0xbfb8aa3b, v110
	v_mul_f32_e32 v124, v114, v117
	v_cvt_pk_bf16_f32 v117, v120, v121
	v_exp_f32_e32 v120, v119
	v_mul_f32_e32 v119, 0xbfb8aa3b, v111
	v_exp_f32_e32 v121, v119
	v_lshl_or_b32 v140, s53, 7, v150
	v_add_f32_e32 v120, 1.0, v120
	v_rcp_f32_e32 v120, v120
	v_add_f32_e32 v121, 1.0, v121
	v_rcp_f32_e32 v121, v121
	v_lshlrev_b64 v[138:139], 10, v[138:139]
	v_ashrrev_i32_e32 v141, 31, v140
	v_lshl_add_u64 v[138:139], s[6:7], 0, v[138:139]
	v_mul_f32_e32 v110, v110, v120
	v_lshl_add_u64 v[114:115], v[140:141], 1, v[138:139]
	v_mul_f32_e32 v102, v110, v102
	v_mul_f32_e32 v110, v111, v121
	v_mul_f32_e32 v111, 0xbfb8aa3b, v112
	v_cvt_pk_bf16_f32 v118, v122, v127
	v_cvt_pk_bf16_f32 v119, v123, v124
	global_store_dwordx4 v[114:115], v[116:119], off
	v_exp_f32_e32 v111, v111
	v_mul_f32_e32 v103, v110, v103
	v_mul_f32_e32 v116, 0xbfb8aa3b, v113
	v_exp_f32_e32 v116, v116
	v_add_f32_e32 v110, 1.0, v111
	v_rcp_f32_e32 v110, v110
	v_mov_b32_e32 v157, v152
	v_add_f32_e32 v111, 1.0, v116
	v_mul_f32_e32 v116, 0xbfb8aa3b, v106
	v_rcp_f32_e32 v111, v111
	v_exp_f32_e32 v116, v116
	v_mul_f32_e32 v110, v112, v110
	v_mul_f32_e32 v104, v110, v104
	v_mul_f32_e32 v110, v113, v111
	v_add_f32_e32 v111, 1.0, v116
	v_rcp_f32_e32 v111, v111
	v_mul_f32_e32 v112, 0xbfb8aa3b, v107
	v_exp_f32_e32 v112, v112
	v_mul_f32_e32 v105, v110, v105
	v_mul_f32_e32 v106, v106, v111
	v_mul_f32_e32 v106, v106, v98
	v_add_f32_e32 v98, 1.0, v112
	v_mul_f32_e32 v110, 0xbfb8aa3b, v108
	v_rcp_f32_e32 v98, v98
	v_exp_f32_e32 v110, v110
	v_mul_f32_e32 v111, 0xbfb8aa3b, v109
	v_exp_f32_e32 v111, v111
	v_mul_f32_e32 v98, v107, v98
	v_add_f32_e32 v107, 1.0, v110
	v_rcp_f32_e32 v107, v107
	v_add_f32_e32 v110, 1.0, v111
	v_rcp_f32_e32 v110, v110
	v_mul_f32_e32 v111, v98, v99
	v_mul_f32_e32 v98, v108, v107
	v_mul_f32_e32 v107, v98, v100
	v_mul_f32_e32 v98, v109, v110
	v_mul_f32_e32 v101, v98, v101
	v_cvt_pk_bf16_f32 v98, v102, v103
	v_mul_f32_e32 v102, 0xbfb8aa3b, v94
	v_cvt_pk_bf16_f32 v99, v104, v105
	v_exp_f32_e32 v104, v102
	v_mul_f32_e32 v102, 0xbfb8aa3b, v95
	v_exp_f32_e32 v105, v102
	v_add_co_u32_e32 v102, vcc, s42, v114
	v_add_f32_e32 v104, 1.0, v104
	v_rcp_f32_e32 v104, v104
	v_add_f32_e32 v105, 1.0, v105
	v_rcp_f32_e32 v105, v105
	v_addc_co_u32_e32 v103, vcc, 0, v115, vcc
	v_mul_f32_e32 v94, v94, v104
	v_mul_f32_e32 v86, v94, v86
	v_mul_f32_e32 v94, v95, v105
	v_mul_f32_e32 v95, 0xbfb8aa3b, v96
	v_cvt_pk_bf16_f32 v100, v106, v111
	v_cvt_pk_bf16_f32 v101, v107, v101
	global_store_dwordx4 v[102:103], v[98:101], off
	v_exp_f32_e32 v95, v95
	v_mul_f32_e32 v87, v94, v87
	v_mul_f32_e32 v98, 0xbfb8aa3b, v97
	v_exp_f32_e32 v98, v98
	v_add_f32_e32 v94, 1.0, v95
	v_rcp_f32_e32 v94, v94
	s_mov_b32 s53, s12
	v_add_f32_e32 v95, 1.0, v98
	v_mul_f32_e32 v98, 0xbfb8aa3b, v90
	v_rcp_f32_e32 v95, v95
	v_exp_f32_e32 v98, v98
	v_mul_f32_e32 v94, v96, v94
	v_mul_f32_e32 v88, v94, v88
	v_mul_f32_e32 v94, v97, v95
	v_add_f32_e32 v95, 1.0, v98
	v_rcp_f32_e32 v95, v95
	v_mul_f32_e32 v96, 0xbfb8aa3b, v91
	v_exp_f32_e32 v96, v96
	v_mul_f32_e32 v89, v94, v89
	v_mul_f32_e32 v90, v90, v95
	v_mul_f32_e32 v90, v90, v82
	v_add_f32_e32 v82, 1.0, v96
	v_mul_f32_e32 v94, 0xbfb8aa3b, v92
	v_rcp_f32_e32 v82, v82
	v_exp_f32_e32 v94, v94
	v_mul_f32_e32 v95, 0xbfb8aa3b, v93
	v_exp_f32_e32 v95, v95
	v_mul_f32_e32 v82, v91, v82
	v_add_f32_e32 v91, 1.0, v94
	v_rcp_f32_e32 v91, v91
	v_add_f32_e32 v94, 1.0, v95
	v_rcp_f32_e32 v94, v94
	v_mul_f32_e32 v95, v82, v83
	v_mul_f32_e32 v82, v92, v91
	v_mul_f32_e32 v91, v82, v84
	v_mul_f32_e32 v82, v93, v94
	v_mul_f32_e32 v85, v82, v85
	v_cvt_pk_bf16_f32 v82, v86, v87
	v_mul_f32_e32 v86, 0xbfb8aa3b, v78
	v_cvt_pk_bf16_f32 v83, v88, v89
	v_exp_f32_e32 v88, v86
	v_mul_f32_e32 v86, 0xbfb8aa3b, v79
	v_exp_f32_e32 v89, v86
	v_add_co_u32_e32 v86, vcc, s45, v114
	v_add_f32_e32 v88, 1.0, v88
	v_rcp_f32_e32 v88, v88
	v_add_f32_e32 v89, 1.0, v89
	v_rcp_f32_e32 v89, v89
	v_addc_co_u32_e32 v87, vcc, 0, v115, vcc
	v_mul_f32_e32 v78, v78, v88
	v_mul_f32_e32 v70, v78, v70
	v_mul_f32_e32 v78, v79, v89
	v_mul_f32_e32 v79, 0xbfb8aa3b, v80
	v_cvt_pk_bf16_f32 v84, v90, v95
; __device__ __forceinline__ unsigned cvt_pk_bf16(float lo, float hi) { unsigned r; asm volatile("v_cvt_pk_bf16_f32 %0, %1, %2" : "=v"(r) : "v"(lo), "v"(hi)); return r; }
; __device__ __forceinline__ float fdivf(float a, float b) { return a * __builtin_amdgcn_rcpf(b); }
;     __device__ __forceinline__ void operator()(const f32x4 (&acc)[2][2][4][2], const Unit& u, int wr, int wc, int fr, int fq) const {
;         const int row0 = u.rbase + wr * 64 + fr, col0 = u.pn * HALF + wc * 32 + 8 * fq;
; #pragma unroll
;         for (int ai = 0; ai < 2; ++ai)
; #pragma unroll
;             for (int m = 0; m < 4; ++m) { bf16_t* rowp = O + (size_t)(row0 + ai * HALF + m * 16) * FF + col0;
;                 float h[8];
; #pragma unroll
;                 for (int n = 0; n < 2; ++n)
; #pragma unroll
;                     for (int j = 0; j < 4; ++j) { const float g = acc[ai][0][m][n][j], up = acc[ai][1][m][n][j]; h[n * 4 + j] = fdivf(g, 1.f + __expf(-g)) * up; }
;                 u32x4 w; w.x = cvt_pk_bf16(h[0], h[1]); w.y = cvt_pk_bf16(h[2], h[3]); w.z = cvt_pk_bf16(h[4], h[5]); w.w = cvt_pk_bf16(h[6], h[7]);
;                 *(u32x4*)rowp = w; }
;     }
	v_cvt_pk_bf16_f32 v85, v91, v85
	global_store_dwordx4 v[86:87], v[82:85], off
	v_exp_f32_e32 v79, v79
	v_mul_f32_e32 v71, v78, v71
	v_mul_f32_e32 v82, 0xbfb8aa3b, v81
	v_exp_f32_e32 v82, v82
	v_add_f32_e32 v78, 1.0, v79
	v_rcp_f32_e32 v78, v78
	v_mov_b32_e32 v158, v156
	v_add_f32_e32 v79, 1.0, v82
	v_mul_f32_e32 v82, 0xbfb8aa3b, v74
	v_rcp_f32_e32 v79, v79
	v_exp_f32_e32 v82, v82
	v_mul_f32_e32 v78, v80, v78
	v_mul_f32_e32 v72, v78, v72
	v_mul_f32_e32 v78, v81, v79
	v_add_f32_e32 v79, 1.0, v82
	v_rcp_f32_e32 v79, v79
	v_mul_f32_e32 v80, 0xbfb8aa3b, v75
	v_exp_f32_e32 v80, v80
	v_mul_f32_e32 v73, v78, v73
	v_mul_f32_e32 v74, v74, v79
	v_mul_f32_e32 v74, v74, v66
	v_add_f32_e32 v66, 1.0, v80
	v_mul_f32_e32 v78, 0xbfb8aa3b, v76
	v_rcp_f32_e32 v66, v66
	v_exp_f32_e32 v78, v78
	v_mul_f32_e32 v79, 0xbfb8aa3b, v77
	v_exp_f32_e32 v79, v79
	v_mul_f32_e32 v66, v75, v66
	v_add_f32_e32 v75, 1.0, v78
	v_rcp_f32_e32 v75, v75
	v_add_f32_e32 v78, 1.0, v79
	v_rcp_f32_e32 v78, v78
	v_mul_f32_e32 v79, v66, v67
	v_mul_f32_e32 v66, v76, v75
	v_mul_f32_e32 v75, v66, v68
	v_mul_f32_e32 v66, v77, v78
	v_mul_f32_e32 v69, v66, v69
	v_cvt_pk_bf16_f32 v66, v70, v71
	v_mul_f32_e32 v70, 0xbfb8aa3b, v62
	v_cvt_pk_bf16_f32 v67, v72, v73
	v_exp_f32_e32 v72, v70
	v_mul_f32_e32 v70, 0xbfb8aa3b, v63
	v_exp_f32_e32 v73, v70
	v_add_co_u32_e32 v70, vcc, s47, v114
	v_add_f32_e32 v72, 1.0, v72
	v_rcp_f32_e32 v72, v72
	v_add_f32_e32 v73, 1.0, v73
	v_rcp_f32_e32 v73, v73
	v_addc_co_u32_e32 v71, vcc, 0, v115, vcc
	v_mul_f32_e32 v62, v62, v72
	v_mul_f32_e32 v54, v62, v54
	v_mul_f32_e32 v62, v63, v73
	v_mul_f32_e32 v63, 0xbfb8aa3b, v64
	v_cvt_pk_bf16_f32 v68, v74, v79
	v_cvt_pk_bf16_f32 v69, v75, v69
	global_store_dwordx4 v[70:71], v[66:69], off
	v_exp_f32_e32 v63, v63
	v_mul_f32_e32 v55, v62, v55
	v_mul_f32_e32 v66, 0xbfb8aa3b, v65
	v_exp_f32_e32 v66, v66
	v_add_f32_e32 v62, 1.0, v63
	v_rcp_f32_e32 v62, v62
	v_mov_b32_e32 v136, v155
	v_add_f32_e32 v63, 1.0, v66
	v_mul_f32_e32 v66, 0xbfb8aa3b, v58
	v_rcp_f32_e32 v63, v63
	v_exp_f32_e32 v66, v66
	v_mul_f32_e32 v62, v64, v62
	v_mul_f32_e32 v56, v62, v56
	v_mul_f32_e32 v62, v65, v63
	v_add_f32_e32 v63, 1.0, v66
	v_rcp_f32_e32 v63, v63
	v_mul_f32_e32 v64, 0xbfb8aa3b, v59
	v_exp_f32_e32 v64, v64
	v_mul_f32_e32 v57, v62, v57
	v_mul_f32_e32 v58, v58, v63
	v_mul_f32_e32 v58, v58, v50
	v_add_f32_e32 v50, 1.0, v64
	v_mul_f32_e32 v62, 0xbfb8aa3b, v60
	v_rcp_f32_e32 v50, v50
	v_exp_f32_e32 v62, v62
	v_mul_f32_e32 v63, 0xbfb8aa3b, v61
	v_exp_f32_e32 v63, v63
	v_mul_f32_e32 v50, v59, v50
	v_add_f32_e32 v59, 1.0, v62
	v_rcp_f32_e32 v59, v59
	v_add_f32_e32 v62, 1.0, v63
	v_rcp_f32_e32 v62, v62
	v_mul_f32_e32 v63, v50, v51
	v_mul_f32_e32 v50, v60, v59
	v_mul_f32_e32 v59, v50, v52
	v_mul_f32_e32 v50, v61, v62
	v_mul_f32_e32 v53, v50, v53
	v_cvt_pk_bf16_f32 v50, v54, v55
	v_mul_f32_e32 v54, 0xbfb8aa3b, v46
	v_cvt_pk_bf16_f32 v51, v56, v57
	v_exp_f32_e32 v56, v54
	v_mul_f32_e32 v54, 0xbfb8aa3b, v47
	v_exp_f32_e32 v57, v54
	v_add_co_u32_e32 v54, vcc, s49, v114
	v_add_f32_e32 v56, 1.0, v56
	v_rcp_f32_e32 v56, v56
	v_add_f32_e32 v57, 1.0, v57
	v_rcp_f32_e32 v57, v57
	v_addc_co_u32_e32 v55, vcc, 0, v115, vcc
	v_mul_f32_e32 v46, v46, v56
	v_mul_f32_e32 v38, v46, v38
	v_mul_f32_e32 v46, v47, v57
	v_mul_f32_e32 v47, 0xbfb8aa3b, v48
	v_cvt_pk_bf16_f32 v52, v58, v63
	v_cvt_pk_bf16_f32 v53, v59, v53
	global_store_dwordx4 v[54:55], v[50:53], off
	v_exp_f32_e32 v47, v47
	v_mul_f32_e32 v39, v46, v39
	v_mul_f32_e32 v50, 0xbfb8aa3b, v49
	v_exp_f32_e32 v50, v50
	v_add_f32_e32 v46, 1.0, v47
	v_rcp_f32_e32 v46, v46
	v_mov_b32_e32 v138, v154
	v_add_f32_e32 v47, 1.0, v50
	v_mul_f32_e32 v50, 0xbfb8aa3b, v42
	v_rcp_f32_e32 v47, v47
	v_exp_f32_e32 v50, v50
	v_mul_f32_e32 v46, v48, v46
	v_mul_f32_e32 v40, v46, v40
	v_mul_f32_e32 v46, v49, v47
	v_add_f32_e32 v47, 1.0, v50
	v_rcp_f32_e32 v47, v47
	v_mul_f32_e32 v48, 0xbfb8aa3b, v43
	v_exp_f32_e32 v48, v48
	v_mul_f32_e32 v41, v46, v41
	v_mul_f32_e32 v42, v42, v47
	v_mul_f32_e32 v42, v42, v34
	v_add_f32_e32 v34, 1.0, v48
	v_mul_f32_e32 v46, 0xbfb8aa3b, v44
	v_rcp_f32_e32 v34, v34
; __device__ __forceinline__ unsigned cvt_pk_bf16(float lo, float hi) { unsigned r; asm volatile("v_cvt_pk_bf16_f32 %0, %1, %2" : "=v"(r) : "v"(lo), "v"(hi)); return r; }
; __device__ __forceinline__ float fdivf(float a, float b) { return a * __builtin_amdgcn_rcpf(b); }
; #define PG8_WAIT_V(n) asm volatile("s_waitcnt vmcnt(" #n ")" ::: "memory")
; #define PG8_BAR __builtin_amdgcn_s_barrier()
; template <class Epi, class Sched>
; __device__ __forceinline__ void gemm_phase(LAS unsigned char* lds, const int K, const Sched& S, const Epi& E) {
;     ...
;         if (!has_next) break;
; #pragma unroll
;         for (int a = 0; a < 2; ++a)
; #pragma unroll
;             for (int b = 0; b < 2; ++b)
; #pragma unroll
;                 for (int m = 0; m < 4; ++m)
; #pragma unroll
;                     for (int n = 0; n < 2; ++n) acc[a][b][m][n] = (f32x4){0.f, 0.f, 0.f, 0.f};
;         cur = nxt; cB = nB; c00 = n00; c01 = n01; c10 = n10; c11 = n11; ++ui;
;     }
;     PG8_WAIT_V(0);
;     if (wr == 0) PG8_BAR;
;     PG8_BAR;
;     __device__ __forceinline__ void operator()(const f32x4 (&acc)[2][2][4][2], const Unit& u, int wr, int wc, int fr, int fq) const {
;         const int row0 = u.rbase + wr * 64 + fr, col0 = u.pn * HALF + wc * 32 + 8 * fq;
; #pragma unroll
;         for (int ai = 0; ai < 2; ++ai)
; #pragma unroll
;             for (int m = 0; m < 4; ++m) { bf16_t* rowp = O + (size_t)(row0 + ai * HALF + m * 16) * FF + col0;
;                 float h[8];
; #pragma unroll
;                 for (int n = 0; n < 2; ++n)
; #pragma unroll
;                     for (int j = 0; j < 4; ++j) { const float g = acc[ai][0][m][n][j], up = acc[ai][1][m][n][j]; h[n * 4 + j] = fdivf(g, 1.f + __expf(-g)) * up; }
;                 u32x4 w; w.x = cvt_pk_bf16(h[0], h[1]); w.y = cvt_pk_bf16(h[2], h[3]); w.z = cvt_pk_bf16(h[4], h[5]); w.w = cvt_pk_bf16(h[6], h[7]);
;                 *(u32x4*)rowp = w; }
;     }
	v_exp_f32_e32 v46, v46
	v_mul_f32_e32 v47, 0xbfb8aa3b, v45
	v_exp_f32_e32 v47, v47
	v_mul_f32_e32 v34, v43, v34
	v_add_f32_e32 v43, 1.0, v46
	v_rcp_f32_e32 v43, v43
	v_add_f32_e32 v46, 1.0, v47
	v_rcp_f32_e32 v46, v46
	v_mul_f32_e32 v47, v34, v35
	v_mul_f32_e32 v34, v44, v43
	v_mul_f32_e32 v43, v34, v36
	v_mul_f32_e32 v34, v45, v46
	v_mul_f32_e32 v37, v34, v37
	v_cvt_pk_bf16_f32 v34, v38, v39
	v_mul_f32_e32 v38, 0xbfb8aa3b, v30
	v_cvt_pk_bf16_f32 v35, v40, v41
	v_exp_f32_e32 v40, v38
	v_mul_f32_e32 v38, 0xbfb8aa3b, v31
	v_exp_f32_e32 v41, v38
	v_add_co_u32_e32 v38, vcc, s50, v114
	v_add_f32_e32 v40, 1.0, v40
	v_rcp_f32_e32 v40, v40
	v_add_f32_e32 v41, 1.0, v41
	v_rcp_f32_e32 v41, v41
	v_addc_co_u32_e32 v39, vcc, 0, v115, vcc
	v_mul_f32_e32 v30, v30, v40
	v_mul_f32_e32 v22, v30, v22
	v_mul_f32_e32 v30, v31, v41
	v_mul_f32_e32 v31, 0xbfb8aa3b, v32
	v_cvt_pk_bf16_f32 v36, v42, v47
	v_cvt_pk_bf16_f32 v37, v43, v37
	global_store_dwordx4 v[38:39], v[34:37], off
	v_exp_f32_e32 v31, v31
	v_mul_f32_e32 v23, v30, v23
	v_mul_f32_e32 v34, 0xbfb8aa3b, v33
	v_exp_f32_e32 v34, v34
	v_add_f32_e32 v30, 1.0, v31
	v_rcp_f32_e32 v30, v30
	v_mov_b32_e32 v140, v153
	v_add_f32_e32 v31, 1.0, v34
	v_mul_f32_e32 v34, 0xbfb8aa3b, v26
	v_rcp_f32_e32 v31, v31
	v_exp_f32_e32 v34, v34
	v_mul_f32_e32 v30, v32, v30
	v_mul_f32_e32 v24, v30, v24
	v_mul_f32_e32 v30, v33, v31
	v_add_f32_e32 v31, 1.0, v34
	v_rcp_f32_e32 v31, v31
	v_mul_f32_e32 v32, 0xbfb8aa3b, v27
	v_exp_f32_e32 v32, v32
	v_mul_f32_e32 v25, v30, v25
	v_mul_f32_e32 v26, v26, v31
	v_mul_f32_e32 v26, v26, v18
	v_add_f32_e32 v18, 1.0, v32
	v_mul_f32_e32 v30, 0xbfb8aa3b, v28
	v_rcp_f32_e32 v18, v18
	v_exp_f32_e32 v30, v30
	v_mul_f32_e32 v31, 0xbfb8aa3b, v29
	v_exp_f32_e32 v31, v31
	v_mul_f32_e32 v18, v27, v18
	v_add_f32_e32 v27, 1.0, v30
	v_rcp_f32_e32 v27, v27
	v_add_f32_e32 v30, 1.0, v31
	v_rcp_f32_e32 v30, v30
	v_mul_f32_e32 v31, v18, v19
	v_mul_f32_e32 v18, v28, v27
	v_mul_f32_e32 v27, v18, v20
	v_mul_f32_e32 v18, v29, v30
	v_mul_f32_e32 v21, v18, v21
	v_cvt_pk_bf16_f32 v18, v22, v23
	v_mul_f32_e32 v22, 0xbfb8aa3b, v14
	v_cvt_pk_bf16_f32 v19, v24, v25
	v_exp_f32_e32 v24, v22
	v_mul_f32_e32 v22, 0xbfb8aa3b, v15
	v_exp_f32_e32 v25, v22
	v_add_co_u32_e32 v22, vcc, s51, v114
	v_add_f32_e32 v24, 1.0, v24
	v_rcp_f32_e32 v24, v24
	v_add_f32_e32 v25, 1.0, v25
	v_rcp_f32_e32 v25, v25
	v_addc_co_u32_e32 v23, vcc, 0, v115, vcc
	v_mul_f32_e32 v14, v14, v24
	v_mul_f32_e32 v6, v14, v6
	v_mul_f32_e32 v14, v15, v25
	v_mul_f32_e32 v15, 0xbfb8aa3b, v16
	v_cvt_pk_bf16_f32 v20, v26, v31
	v_cvt_pk_bf16_f32 v21, v27, v21
	global_store_dwordx4 v[22:23], v[18:21], off
	v_exp_f32_e32 v15, v15
	v_mul_f32_e32 v7, v14, v7
	v_mul_f32_e32 v18, 0xbfb8aa3b, v17
	v_exp_f32_e32 v18, v18
	v_add_f32_e32 v14, 1.0, v15
	v_rcp_f32_e32 v14, v14
	s_mov_b64 s[20:21], s[18:19]
	v_add_f32_e32 v15, 1.0, v18
	v_mul_f32_e32 v18, 0xbfb8aa3b, v10
	v_rcp_f32_e32 v15, v15
	v_exp_f32_e32 v18, v18
	v_mul_f32_e32 v14, v16, v14
	v_mul_f32_e32 v8, v14, v8
	v_mul_f32_e32 v14, v17, v15
	v_add_f32_e32 v15, 1.0, v18
	v_rcp_f32_e32 v15, v15
	v_mul_f32_e32 v16, 0xbfb8aa3b, v11
	v_exp_f32_e32 v16, v16
	v_mul_f32_e32 v9, v14, v9
	v_mul_f32_e32 v10, v10, v15
	v_mul_f32_e32 v10, v10, v2
	v_add_f32_e32 v2, 1.0, v16
	v_mul_f32_e32 v14, 0xbfb8aa3b, v12
	v_rcp_f32_e32 v2, v2
	v_exp_f32_e32 v14, v14
	v_mul_f32_e32 v15, 0xbfb8aa3b, v13
	v_exp_f32_e32 v15, v15
	v_mul_f32_e32 v2, v11, v2
	v_add_f32_e32 v11, 1.0, v14
	v_rcp_f32_e32 v11, v11
	v_add_f32_e32 v14, 1.0, v15
	v_rcp_f32_e32 v14, v14
	v_mul_f32_e32 v15, v2, v3
	v_mul_f32_e32 v2, v12, v11
	v_mul_f32_e32 v11, v2, v4
	v_mul_f32_e32 v2, v13, v14
	v_mul_f32_e32 v5, v2, v5
	v_cvt_pk_bf16_f32 v2, v6, v7
	v_add_co_u32_e32 v6, vcc, 0x2c000, v114
	v_cvt_pk_bf16_f32 v3, v8, v9
	v_cvt_pk_bf16_f32 v4, v10, v15
	v_cvt_pk_bf16_f32 v5, v11, v5
	s_nop 1
	v_addc_co_u32_e32 v7, vcc, 0, v115, vcc
	s_and_b64 vcc, exec, s[16:17]
	global_store_dwordx4 v[6:7], v[2:5], off
	s_cbranch_vccz .LBB0_1085
	s_waitcnt vmcnt(0)
	s_cmpk_gt_u32 s30, 0xff
	s_cbranch_scc1 .LBB0_1098
	s_barrier

; __device__ __forceinline__ unsigned cvt_pk_bf16(float lo, float hi) { unsigned r; asm volatile("v_cvt_pk_bf16_f32 %0, %1, %2" : "=v"(r) : "v"(lo), "v"(hi)); return r; }
; __device__ __forceinline__ bool bg_decode(int st, int wg, int NW, int lane, KP kp, const float*& src, int& ldS, bf16_t*& dst, int& o2) {
;     ...
;     if (r < 65536) {
;         const int e = r >> 10, kc = (r >> 2) & 255, kind = (r >> 1) & 1, cc = r & 1, n = cc * 256 + lane;
;         ldS = FF; o2 = 256 * 8;
;         src = kp->in[27 + kind] + ((size_t)(l * NE + e) * D + kc * 8) * FF + n;
;         const int drow = (n >> 7) * 256 + kind * 128 + (n & 127);
;         dst = (bf16_t*)(ws + WS_WGU) + l * WGU_L + (size_t)e * 1024 * D + ((size_t)kc * 1024 + drow) * 8;
; template <int BANK, int WAITN> __device__ __forceinline__ void bg_finish1(BgState& b) {
;     if (WAITN == 32) asm volatile("s_waitcnt vmcnt(32)" ::: "memory"); else asm volatile("s_waitcnt vmcnt(0)" ::: "memory");
;     asm volatile("" : BG_TIE16(BANK * 32) :: "memory");
;     asm volatile("" : BG_TIE16(BANK * 32 + 16) :: "memory");
;     bf16_t* dst = b.dst[BANK];
;     if (dst != nullptr) {
; #pragma unroll
;         for (int c = 0; c < 4; ++c) { u32x4 w;
;             w.x = cvt_pk_bf16(b.r[(BANK * 8 + 0) * 4 + c], b.r[(BANK * 8 + 1) * 4 + c]); w.y = cvt_pk_bf16(b.r[(BANK * 8 + 2) * 4 + c], b.r[(BANK * 8 + 3) * 4 + c]);
;             w.z = cvt_pk_bf16(b.r[(BANK * 8 + 4) * 4 + c], b.r[(BANK * 8 + 5) * 4 + c]); w.w = cvt_pk_bf16(b.r[(BANK * 8 + 6) * 4 + c], b.r[(BANK * 8 + 7) * 4 + c]);
;             bf16_t* dp = dst + (c & 1) * 512 + (c >> 1) * b.o2[BANK];
;             asm volatile("global_store_dwordx4 %0, %1, off\n\ts_nop 1" :: "v"(dp), "v"(w) : "memory"); }
;     }
.LBB0_1099:
.Lpb0_drain:
	s_cmp_eq_u32 s82, 0
	s_cbranch_scc1 .Lpb0_d1
	s_waitcnt vmcnt(0)
	v_cvt_pk_bf16_f32 v244, v236, v237
	v_cvt_pk_bf16_f32 v245, v238, v239
	v_cvt_pk_bf16_f32 v246, v240, v241
	v_cvt_pk_bf16_f32 v247, v242, v243
	global_store_dwordx4 v249, v[244:247], s[80:81]
	s_mov_b32 s82, 0
.Lpb0_d1:
	s_cmp_ge_u32 s70, 0xa0000
	s_cbranch_scc1 .Lpb0_dend
	s_lshr_b32 s84, s70, 2
	s_sub_u32 s84, s84, 0x18000
	s_lshr_b32 s85, s84, 10
	s_lshl_b32 s85, s85, 22
	s_bfe_u32 s86, s84, 0x80002
	s_lshl_b32 s86, s86, 14
	s_add_u32 s85, s85, s86
	s_and_b32 s86, s84, 1
	s_and_b32 s87, s70, 3
	s_lshl_b32 s88, s86, 10
	s_lshl_b32 s89, s87, 8
	s_add_u32 s88, s88, s89
	s_add_u32 s88, s88, s85
	s_add_u32 s88, s88, 0x10000000
	s_bitcmp1_b32 s84, 1
	s_cselect_b64 s[72:73], s[76:77], s[74:75]
	s_add_u32 s72, s72, s88
	s_addc_u32 s73, s73, 0
	s_lshl_b32 s88, s86, 13
	s_add_u32 s88, s88, s85
	s_lshr_b32 s89, s87, 1
	s_lshl_b32 s89, s89, 12
	s_add_u32 s88, s88, s89
	s_and_b32 s89, s87, 1
	s_lshl_b32 s89, s89, 10
	s_add_u32 s88, s88, s89
	s_bfe_u32 s89, s84, 0x10001
	s_lshl_b32 s89, s89, 11
	s_add_u32 s88, s88, s89
	s_add_u32 s88, s88, 0x14430000
	s_add_u32 s80, s78, s88
	s_addc_u32 s81, s79, 0
	global_load_dword v236, v248, s[72:73]
	global_load_dword v237, v248, s[72:73] offset:2048
	s_add_u32 s72, s72, 0x1000
	s_addc_u32 s73, s73, 0
	global_load_dword v238, v248, s[72:73]
	global_load_dword v239, v248, s[72:73] offset:2048
	s_add_u32 s72, s72, 0x1000
	s_addc_u32 s73, s73, 0
	global_load_dword v240, v248, s[72:73]
	global_load_dword v241, v248, s[72:73] offset:2048
	s_add_u32 s72, s72, 0x1000
	s_addc_u32 s73, s73, 0
	global_load_dword v242, v248, s[72:73]
	global_load_dword v243, v248, s[72:73] offset:2048
	s_add_u32 s70, s70, 1
	s_and_b32 s84, s70, 3
	s_cmp_eq_u32 s84, 0
	s_cselect_b32 s84, s71, 0
	s_add_u32 s70, s70, s84
	s_mov_b32 s82, 1
	s_branch .Lpb0_drain

; __device__ __forceinline__ int tid_fresh() { int t = threadIdx.x; asm volatile("" : "+v"(t)); return t; }
;     __device__ __forceinline__ void a_off4(const Unit& u, int r0, int r1, unsigned& o00, unsigned& o01, unsigned& o10, unsigned& o11) const { o00 = a_off(u, r0); o01 = a_off(u, r1); o10 = a_off(u, HALF + r0); o11 = a_off(u, HALF + r1); }
;     __device__ __forceinline__ unsigned b_off(int R, int C) const { return (unsigned)(R * K + C) * 2u; }
;     __device__ __forceinline__ size_t b_kstep() const { return (size_t)(BK * 2); }
;     __device__ __forceinline__ size_t b_hstep() const { return (size_t)HALF * 16; }
; template <class Epi, class Sched>
; __device__ __forceinline__ void gemm_phase(LAS unsigned char* lds, const int K, const Sched& S, const Epi& E) {
;     const int tid = tid_fresh(), wid = __builtin_amdgcn_readfirstlane(tid >> 6), lane = tid & 63, wr = wid >> 2, wc = wid & 3, fr = lane & 15, fq = lane >> 4;
;     const int nt = K / BK;
;     int R0, C0, R1, C1; stage_rc(tid * 16, R0, C0); stage_rc(tid * 16 + 8192, R1, C1);
;     const int Rb0 = Epi::PERM ? ((R0 & ~31) + perm32(R0 & 31)) : R0, Rb1 = Epi::PERM ? ((R1 & ~31) + perm32(R1 & 31)) : R1;
;     const unsigned voffB0 = S.b_off(Rb0, C0), voffB1 = S.b_off(Rb1, C1);
;     const size_t kstep = (size_t)(BK * 2);
;     const size_t kstepB = S.b_kstep(), hstep = S.b_hstep();
;     const unsigned ldsw = (unsigned)wid * 1024u;
;     const int aoff = lds_byte(wr * 64 + fr, fq * 8), boff = lds_byte(wc * 32 + fr, fq * 8);
;     __device__ __forceinline__ void a_off4(const Unit& u, int r0, int r1, unsigned& o00, unsigned& o01, unsigned& o10, unsigned& o11) const {
;         const int p0 = u.pm * BM + r0, p1 = u.pm * BM + r1, p2 = p0 + HALF, p3 = p1 + HALF;
;         if (u.e >= NE) { o00 = (unsigned)p0 * (unsigned)(D * 2); o01 = (unsigned)p1 * (unsigned)(D * 2); o10 = (unsigned)p2 * (unsigned)(D * 2); o11 = (unsigned)p3 * (unsigned)(D * 2); return; }
;         const int* lp = list + u.e * T;
;         int v0 = lp[p0], v1 = lp[p1], v2 = lp[p2], v3 = lp[p3];
;         asm volatile("" : "+v"(v0), "+v"(v1), "+v"(v2), "+v"(v3));
;         const int c = cnt[u.e];
;         o00 = p0 < c ? (unsigned)v0 * (unsigned)(D * 2) : 0u; o01 = p1 < c ? (unsigned)v1 * (unsigned)(D * 2) : 0u;
;         o10 = p2 < c ? (unsigned)v2 * (unsigned)(D * 2) : 0u; o11 = p3 < c ? (unsigned)v3 * (unsigned)(D * 2) : 0u;
;     }
.LBB0_1814:
	s_or_b64 exec, exec, s[0:1]
	v_readlane_b32 s0, v254, 0
	v_readlane_b32 s1, v254, 1
	s_lshl_b32 s29, s28, 2
	v_readlane_b32 s2, v254, 5
	v_mov_b32_e32 v6, v0
	s_waitcnt lgkmcnt(0)
	s_barrier
	v_readlane_b32 s84, v254, 0
	v_readlane_b32 s85, v254, 1
	s_nop 1
	s_load_dwordx2 s[74:75], s[84:85], 0xe8
	s_load_dwordx2 s[78:79], s[84:85], 0x118
	v_and_b32_e32 v248, 63, v0
	v_lshrrev_b32_e32 v250, 6, v0
	v_lshlrev_b32_e32 v249, 4, v248
	v_lshlrev_b32_e32 v248, 2, v248
	v_readlane_b32 s86, v254, 4
	v_readlane_b32 s87, v255, 40
	v_readfirstlane_b32 s88, v250
	s_nop 3
	s_lshl_b32 s71, s86, 3
	s_sub_u32 s71, s71, 1
	s_lshl_b32 s71, s71, 2
	s_lshl_b32 s87, s87, 3
	s_add_u32 s87, s87, s88
	s_add_u32 s87, s87, 0x28000
	s_lshl_b32 s70, s87, 2
	s_mov_b32 s82, 0
	s_waitcnt lgkmcnt(0)
	s_cmp_lt_i32 s2, s29
	s_nop 0
	v_readfirstlane_b32 s30, v6
	s_cbranch_scc0 .LBB0_1836
	v_ashrrev_i32_e32 v1, 31, v6
	v_lshrrev_b32_e32 v1, 26, v1
	v_add_u32_e32 v1, v6, v1
	v_ashrrev_i32_e32 v9, 6, v1
	v_bfe_i32 v1, v6, 27, 1
	v_lshlrev_b32_e32 v2, 4, v6
	v_lshrrev_b32_e32 v1, 22, v1
	v_add_u32_e32 v1, v2, v1
	v_and_b32_e32 v1, 0xfffffc00, v1
	v_sub_u32_e32 v1, v2, v1
	v_lshrrev_b32_e32 v3, 4, v1
	v_bitop3_b32 v10, v3, v1, 32 bitop3:0x6c
	v_ashrrev_i32_e32 v1, 31, v1
	v_lshrrev_b32_e32 v1, 26, v1
	s_load_dwordx2 s[0:1], s[0:1], 0x118
	v_lshlrev_b32_e32 v3, 3, v9
	v_add_u32_e32 v1, v10, v1
	v_and_b32_e32 v3, -16, v3
	v_ashrrev_i32_e32 v8, 6, v1
	v_add_u32_e32 v2, 0x2000, v2
	v_add_u32_e32 v1, v8, v3
	v_ashrrev_i32_e32 v3, 31, v2
	v_lshrrev_b32_e32 v3, 22, v3
	v_add_u32_e32 v3, v2, v3
	s_waitcnt lgkmcnt(0)
	s_add_u32 s31, s0, 0x3ec30000
	v_ashrrev_i32_e32 v11, 10, v3
	v_readlane_b32 s3, v254, 5
	s_addc_u32 s33, s1, 0
	v_mul_i32_i24_e32 v3, 0x400, v11
	s_and_b32 s2, s3, -4
	v_sub_u32_e32 v2, v2, v3
	s_add_i32 s2, s2, 0
	v_lshrrev_b32_e32 v3, 4, v2
	s_add_i32 s2, s2, 0x21160
	v_bitop3_b32 v12, v3, v2, 32 bitop3:0x6c
	v_mov_b32_e32 v3, s2
	ds_read_b32 v3, v3
	v_ashrrev_i32_e32 v4, 31, v12
	v_lshrrev_b32_e32 v4, 26, v4
	v_lshlrev_b32_e32 v2, 3, v11
	v_add_u32_e32 v4, v12, v4
	s_waitcnt lgkmcnt(0)
	v_lshlrev_b32_e32 v5, 2, v3
	v_add_u32_e32 v5, 0, v5
	v_add_u32_e32 v5, 0x21040, v5
	ds_read_b32 v5, v5
	v_and_b32_e32 v2, -16, v2
	v_ashrrev_i32_e32 v13, 6, v4
	s_ashr_i32 s8, s3, 2
	v_add_u32_e32 v146, v13, v2
	s_waitcnt lgkmcnt(0)
	v_sub_u32_e32 v2, s8, v5
	v_lshlrev_b32_e32 v7, 8, v2
	v_add_u32_e32 v2, v7, v1
	v_add_u32_e32 v4, v7, v146
	v_cmp_gt_i32_e32 vcc, 64, v3
	v_readfirstlane_b32 s6, v3
	v_add_u32_e32 v14, 0x80, v2
	v_add_u32_e32 v15, 0x80, v4
	s_cbranch_vccz .LBB0_1817
	s_lshl_b32 s2, s6, 13
	s_ashr_i32 s3, s2, 31
	s_lshl_b64 s[2:3], s[2:3], 2
	s_add_u32 s2, s31, s2
	s_addc_u32 s3, s33, s3
	v_ashrrev_i32_e32 v3, 31, v2
	v_lshl_add_u64 v[16:17], v[2:3], 2, s[2:3]
	v_ashrrev_i32_e32 v5, 31, v4
	v_lshl_add_u64 v[18:19], v[4:5], 2, s[2:3]
	global_load_dword v3, v[16:17], off
	global_load_dword v5, v[18:19], off
	global_load_dword v20, v[18:19], off offset:512
	global_load_dword v21, v[16:17], off offset:512
	s_lshl_b32 s2, s6, 2
	s_add_i32 s2, s2, 0
	s_add_i32 s2, s2, 0x21660
	v_mov_b32_e32 v16, s2
	s_waitcnt vmcnt(0)
	ds_read_b32 v17, v16
	v_lshlrev_b32_e32 v3, 12, v3
	v_lshlrev_b32_e32 v5, 12, v5
	v_lshlrev_b32_e32 v16, 12, v21
	v_lshlrev_b32_e32 v18, 12, v20
	s_waitcnt lgkmcnt(0)
	v_cmp_lt_i32_e32 vcc, v2, v17
	s_nop 1
	v_cndmask_b32_e32 v3, 0, v3, vcc
	v_cmp_lt_i32_e32 vcc, v4, v17
	s_nop 1
	v_cndmask_b32_e32 v5, 0, v5, vcc
	v_cmp_lt_i32_e32 vcc, v14, v17
	s_nop 1
	v_cndmask_b32_e32 v16, 0, v16, vcc
	v_cmp_lt_i32_e32 vcc, v15, v17
	s_nop 1
	v_cndmask_b32_e32 v17, 0, v18, vcc
	s_cbranch_execz .LBB0_1818
	s_branch .LBB0_1819

; #define PG8_STAGE(bufoff, gbase, v0, v1) do { \
;         __builtin_amdgcn_global_load_lds((const unsigned*)((const char*)(gbase) + (v0)), (LAS unsigned*)(lds + (bufoff) + ldsw), 16, 0, 0); \
;         __builtin_amdgcn_global_load_lds((const unsigned*)((const char*)(gbase) + (v1)), (LAS unsigned*)(lds + (bufoff) + ldsw + 8192), 16, 0, 0); } while (0)
; #define PG8_LDA(dst, b, h) do { _Pragma("unroll") for (int m = 0; m < 4; ++m) _Pragma("unroll") for (int k = 0; k < 2; ++k) dst[m][k] = *(const LAS bf16x8*)(lds + PG8_SA(b, h) + aoff + m * 2048 + k * 1024); } while (0)
; #define PG8_LDB(dst, b, h) do { _Pragma("unroll") for (int n = 0; n < 2; ++n) _Pragma("unroll") for (int k = 0; k < 2; ++k) dst[n][k] = *(const LAS bf16x8*)(lds + PG8_SB(b, h) + boff + n * 2048 + k * 1024); } while (0)
; #define PG8_MMA(ai, bj, At, Bt) do { __builtin_amdgcn_s_setprio(1); _Pragma("unroll") for (int m = 0; m < 4; ++m) _Pragma("unroll") for (int n = 0; n < 2; ++n) _Pragma("unroll") for (int k = 0; k < 2; ++k) \
;         acc[ai][bj][m][n] = __builtin_amdgcn_mfma_f32_16x16x32_bf16(Bt[n][k], At[m][k], acc[ai][bj][m][n], 0, 0, 0); __builtin_amdgcn_s_setprio(0); } while (0)
; #define PG8_WAIT_V(n) asm volatile("s_waitcnt vmcnt(" #n ")" ::: "memory")
; #define PG8_WAIT_L(n) asm volatile("s_waitcnt lgkmcnt(" #n ")" ::: "memory")
; #define PG8_BAR __builtin_amdgcn_s_barrier()
; #define PG8_SCHED __builtin_amdgcn_sched_barrier(0)
; template <class Epi, class Sched>
; __device__ __forceinline__ void gemm_phase(LAS unsigned char* lds, const int K, const Sched& S, const Epi& E) {
;     ...
;             PG8_LDB(B0, 0, 0); PG8_SCHED; PG8_LDA(At, 0, 0); PG8_STAGE(PG8_SA(1, 1), a1, c10, c11);
;             PG8_WAIT_L(8); PG8_BAR; PG8_WAIT_L(0); PG8_MMA(0, 0, At, B0); PG8_BAR; PG8_SCHED;
;             PG8_LDB(B1, 0, 1); PG8_STAGE(PG8_SB(0, 0), b2, voffB0, voffB1);
;             PG8_BAR; PG8_WAIT_L(0); PG8_MMA(0, 1, At, B1); PG8_BAR;
;             PG8_LDA(At, 0, 1); PG8_STAGE(PG8_SA(0, 0), a2, x00, x01);
;             PG8_BAR; PG8_WAIT_L(0); PG8_MMA(1, 0, At, B0); PG8_BAR; PG8_SCHED;
;             PG8_STAGE(PG8_SB(0, 1), b2 + hstep, voffB0, voffB1);
;             PG8_WAIT_V(6); PG8_BAR; PG8_MMA(1, 1, At, B1); PG8_BAR;
.LBB0_1831:
	v_add_u32_e32 v139, s46, v149
	s_add_u32 s22, s0, s20
	ds_read_b128 v[160:163], v139
	ds_read_b128 v[164:167], v139 offset:1024
	ds_read_b128 v[168:171], v139 offset:2048
	ds_read_b128 v[172:175], v139 offset:3072
	s_addc_u32 s23, s1, s21
	s_add_u32 s24, s22, 0x34c30100
	s_addc_u32 s25, s23, 0
	s_cmpk_eq_i32 s20, 0xf00
	s_cselect_b64 vcc, -1, 0
	s_and_b64 s[22:23], vcc, exec
	v_cndmask_b32_e32 v134, v158, v156, vcc
	s_cselect_b32 s27, s3, s25
	s_cselect_b32 s26, s2, s24
	v_cndmask_b32_e32 v139, v138, v154, vcc
	s_cselect_b32 s23, s19, s15
	s_cselect_b32 s22, s18, s13
	v_cndmask_b32_e32 v224, v136, v155, vcc
	s_add_u32 s24, s22, 0x20000
	s_addc_u32 s25, s23, 0
	v_lshl_add_u64 v[208:209], v[144:145], 0, s[20:21]
	s_add_i32 m0, s37, 0xc000
	ds_read_b128 v[176:179], v151
	ds_read_b128 v[180:183], v151 offset:1024
	ds_read_b128 v[184:187], v151 offset:2048
	ds_read_b128 v[188:191], v151 offset:3072
	ds_read_b128 v[192:195], v151 offset:4096
	ds_read_b128 v[196:199], v151 offset:5120
	ds_read_b128 v[200:203], v151 offset:6144
	ds_read_b128 v[204:207], v151 offset:7168
	global_load_lds_dwordx4 v[208:209], off
	v_lshl_add_u64 v[208:209], v[142:143], 0, s[20:21]
	s_add_i32 m0, s37, 0xe000
	s_nop 0
	global_load_lds_dwordx4 v[208:209], off
	s_waitcnt lgkmcnt(8)
	s_barrier
	s_waitcnt lgkmcnt(0)
	s_setprio 1
	s_waitcnt lgkmcnt(0)
	v_mfma_f32_16x16x32_bf16 v[126:129], v[160:163], v[176:179], v[126:129]
	v_mfma_f32_16x16x32_bf16 v[122:125], v[168:171], v[176:179], v[122:125]
	v_mfma_f32_16x16x32_bf16 v[110:113], v[160:163], v[184:187], v[110:113]
	v_mfma_f32_16x16x32_bf16 v[106:109], v[168:171], v[184:187], v[106:109]
	v_mfma_f32_16x16x32_bf16 v[94:97], v[160:163], v[192:195], v[94:97]
	v_mfma_f32_16x16x32_bf16 v[90:93], v[168:171], v[192:195], v[90:93]
	v_mfma_f32_16x16x32_bf16 v[78:81], v[160:163], v[200:203], v[78:81]
	v_mfma_f32_16x16x32_bf16 v[74:77], v[168:171], v[200:203], v[74:77]
	v_mfma_f32_16x16x32_bf16 v[126:129], v[164:167], v[180:183], v[126:129]
	v_mfma_f32_16x16x32_bf16 v[122:125], v[172:175], v[180:183], v[122:125]
	v_mfma_f32_16x16x32_bf16 v[110:113], v[164:167], v[188:191], v[110:113]
	v_mfma_f32_16x16x32_bf16 v[106:109], v[172:175], v[188:191], v[106:109]
	v_mfma_f32_16x16x32_bf16 v[94:97], v[164:167], v[196:199], v[94:97]
	v_mfma_f32_16x16x32_bf16 v[90:93], v[172:175], v[196:199], v[90:93]
	v_mfma_f32_16x16x32_bf16 v[78:81], v[164:167], v[204:207], v[78:81]
	v_mfma_f32_16x16x32_bf16 v[74:77], v[172:175], v[204:207], v[74:77]
	s_setprio 0
	s_barrier
	s_add_i32 s54, s46, s36
	v_add_u32_e32 v141, s48, v149
	v_lshl_add_u64 v[226:227], s[22:23], 0, v[130:131]
	s_mov_b32 m0, s54
	ds_read_b128 v[208:211], v141
	ds_read_b128 v[212:215], v141 offset:1024
	ds_read_b128 v[216:219], v141 offset:2048
	ds_read_b128 v[220:223], v141 offset:3072
	global_load_lds_dwordx4 v[226:227], off
	v_lshl_add_u64 v[228:229], s[22:23], 0, v[132:133]
	s_add_i32 m0, s54, 0x2000
	s_nop 0
	global_load_lds_dwordx4 v[228:229], off
	s_barrier
	s_waitcnt lgkmcnt(0)
	s_setprio 1
	s_waitcnt lgkmcnt(0)
	v_mfma_f32_16x16x32_bf16 v[118:121], v[208:211], v[176:179], v[118:121]
	v_mfma_f32_16x16x32_bf16 v[114:117], v[216:219], v[176:179], v[114:117]
	v_mfma_f32_16x16x32_bf16 v[102:105], v[208:211], v[184:187], v[102:105]
	v_mfma_f32_16x16x32_bf16 v[98:101], v[216:219], v[184:187], v[98:101]
	v_mfma_f32_16x16x32_bf16 v[86:89], v[208:211], v[192:195], v[86:89]
	v_mfma_f32_16x16x32_bf16 v[82:85], v[216:219], v[192:195], v[82:85]
	v_mfma_f32_16x16x32_bf16 v[70:73], v[208:211], v[200:203], v[70:73]
	v_mfma_f32_16x16x32_bf16 v[66:69], v[216:219], v[200:203], v[66:69]
	v_mfma_f32_16x16x32_bf16 v[118:121], v[212:215], v[180:183], v[118:121]
	v_mfma_f32_16x16x32_bf16 v[114:117], v[220:223], v[180:183], v[114:117]
	v_mfma_f32_16x16x32_bf16 v[102:105], v[212:215], v[188:191], v[102:105]
	v_mfma_f32_16x16x32_bf16 v[98:101], v[220:223], v[188:191], v[98:101]
	v_mfma_f32_16x16x32_bf16 v[86:89], v[212:215], v[196:199], v[86:89]
	v_mfma_f32_16x16x32_bf16 v[82:85], v[220:223], v[196:199], v[82:85]
	v_mfma_f32_16x16x32_bf16 v[70:73], v[212:215], v[204:207], v[70:73]
	v_mfma_f32_16x16x32_bf16 v[66:69], v[220:223], v[204:207], v[66:69]
	s_setprio 0
	s_mov_b32 m0, s37
	s_barrier
	ds_read_b128 v[176:179], v151 offset:16384
	ds_read_b128 v[180:183], v151 offset:17408
	ds_read_b128 v[184:187], v151 offset:18432
	ds_read_b128 v[188:191], v151 offset:19456
	ds_read_b128 v[192:195], v151 offset:20480
	ds_read_b128 v[196:199], v151 offset:21504
	ds_read_b128 v[200:203], v151 offset:22528
	ds_read_b128 v[204:207], v151 offset:23552
	global_load_lds_dwordx4 v134, s[26:27]
	s_mov_b32 m0, s38
	v_mov_b32_e32 v225, v135
	global_load_lds_dwordx4 v224, s[26:27]
	s_barrier
	s_waitcnt lgkmcnt(0)
	v_lshl_add_u64 v[230:231], s[26:27], 0, v[134:135]
	v_lshl_add_u64 v[224:225], s[26:27], 0, v[224:225]
	s_setprio 1
	s_waitcnt lgkmcnt(0)
	v_mfma_f32_16x16x32_bf16 v[62:65], v[160:163], v[176:179], v[62:65]
	v_mfma_f32_16x16x32_bf16 v[58:61], v[168:171], v[176:179], v[58:61]
	v_mfma_f32_16x16x32_bf16 v[46:49], v[160:163], v[184:187], v[46:49]
	v_mfma_f32_16x16x32_bf16 v[42:45], v[168:171], v[184:187], v[42:45]
	v_mfma_f32_16x16x32_bf16 v[30:33], v[160:163], v[192:195], v[30:33]
	v_mfma_f32_16x16x32_bf16 v[26:29], v[168:171], v[192:195], v[26:29]
	v_mfma_f32_16x16x32_bf16 v[14:17], v[160:163], v[200:203], v[14:17]
	v_mfma_f32_16x16x32_bf16 v[10:13], v[168:171], v[200:203], v[10:13]
	v_mfma_f32_16x16x32_bf16 v[62:65], v[164:167], v[180:183], v[62:65]
	v_mfma_f32_16x16x32_bf16 v[58:61], v[172:175], v[180:183], v[58:61]
	v_mfma_f32_16x16x32_bf16 v[46:49], v[164:167], v[188:191], v[46:49]
	v_mfma_f32_16x16x32_bf16 v[42:45], v[172:175], v[188:191], v[42:45]
	v_mfma_f32_16x16x32_bf16 v[30:33], v[164:167], v[196:199], v[30:33]
	v_mfma_f32_16x16x32_bf16 v[26:29], v[172:175], v[196:199], v[26:29]
	v_mfma_f32_16x16x32_bf16 v[14:17], v[164:167], v[204:207], v[14:17]
	v_mfma_f32_16x16x32_bf16 v[10:13], v[172:175], v[204:207], v[10:13]
	s_setprio 0
	s_barrier
; #define PG8_STAGE(bufoff, gbase, v0, v1) do { \
;         __builtin_amdgcn_global_load_lds((const unsigned*)((const char*)(gbase) + (v0)), (LAS unsigned*)(lds + (bufoff) + ldsw), 16, 0, 0); \
;         __builtin_amdgcn_global_load_lds((const unsigned*)((const char*)(gbase) + (v1)), (LAS unsigned*)(lds + (bufoff) + ldsw + 8192), 16, 0, 0); } while (0)
; #define PG8_LDA(dst, b, h) do { _Pragma("unroll") for (int m = 0; m < 4; ++m) _Pragma("unroll") for (int k = 0; k < 2; ++k) dst[m][k] = *(const LAS bf16x8*)(lds + PG8_SA(b, h) + aoff + m * 2048 + k * 1024); } while (0)
; #define PG8_LDB(dst, b, h) do { _Pragma("unroll") for (int n = 0; n < 2; ++n) _Pragma("unroll") for (int k = 0; k < 2; ++k) dst[n][k] = *(const LAS bf16x8*)(lds + PG8_SB(b, h) + boff + n * 2048 + k * 1024); } while (0)
; #define PG8_MMA(ai, bj, At, Bt) do { __builtin_amdgcn_s_setprio(1); _Pragma("unroll") for (int m = 0; m < 4; ++m) _Pragma("unroll") for (int n = 0; n < 2; ++n) _Pragma("unroll") for (int k = 0; k < 2; ++k) \
;         acc[ai][bj][m][n] = __builtin_amdgcn_mfma_f32_16x16x32_bf16(Bt[n][k], At[m][k], acc[ai][bj][m][n], 0, 0, 0); __builtin_amdgcn_s_setprio(0); } while (0)
; #define PG8_WAIT_V(n) asm volatile("s_waitcnt vmcnt(" #n ")" ::: "memory")
; #define PG8_WAIT_L(n) asm volatile("s_waitcnt lgkmcnt(" #n ")" ::: "memory")
; #define PG8_BAR __builtin_amdgcn_s_barrier()
; #define PG8_SCHED __builtin_amdgcn_sched_barrier(0)
; template <class Epi, class Sched>
; __device__ __forceinline__ void gemm_phase(LAS unsigned char* lds, const int K, const Sched& S, const Epi& E) {
;     ...
;             PG8_WAIT_V(6); PG8_BAR; PG8_MMA(1, 1, At, B1); PG8_BAR;
;             PG8_LDB(B0, 1, 0); PG8_SCHED; PG8_LDA(At, 1, 0); PG8_STAGE(PG8_SA(0, 1), a2, x10, x11);
;             PG8_WAIT_L(8); PG8_BAR; PG8_WAIT_L(0); PG8_MMA(0, 0, At, B0); PG8_BAR; PG8_SCHED;
;             PG8_LDB(B1, 1, 1); PG8_STAGE(PG8_SB(1, 0), b3, voffB0, voffB1);
;             PG8_BAR; PG8_WAIT_L(0); PG8_MMA(0, 1, At, B1); PG8_BAR;
;             PG8_LDA(At, 1, 1); PG8_STAGE(PG8_SA(1, 0), a3, x00, x01);
;             PG8_BAR; PG8_WAIT_L(0); PG8_MMA(1, 0, At, B0); PG8_BAR; PG8_SCHED;
	s_add_i32 s54, s48, s36
	v_lshl_add_u64 v[160:161], v[226:227], 0, s[4:5]
	s_mov_b32 m0, s54
	s_nop 0
	global_load_lds_dwordx4 v[160:161], off
	v_lshl_add_u64 v[160:161], v[228:229], 0, s[4:5]
	s_add_i32 m0, s54, 0x2000
	s_nop 0
	global_load_lds_dwordx4 v[160:161], off
	s_waitcnt vmcnt(6)
	s_barrier
	s_setprio 1
	v_mfma_f32_16x16x32_bf16 v[54:57], v[208:211], v[176:179], v[54:57]
	v_mfma_f32_16x16x32_bf16 v[50:53], v[216:219], v[176:179], v[50:53]
	v_mfma_f32_16x16x32_bf16 v[38:41], v[208:211], v[184:187], v[38:41]
	v_mfma_f32_16x16x32_bf16 v[34:37], v[216:219], v[184:187], v[34:37]
	v_mfma_f32_16x16x32_bf16 v[22:25], v[208:211], v[192:195], v[22:25]
	v_mfma_f32_16x16x32_bf16 v[18:21], v[216:219], v[192:195], v[18:21]
	v_mfma_f32_16x16x32_bf16 v[6:9], v[208:211], v[200:203], v[6:9]
	v_mfma_f32_16x16x32_bf16 v[2:5], v[216:219], v[200:203], v[2:5]
	v_mfma_f32_16x16x32_bf16 v[54:57], v[212:215], v[180:183], v[54:57]
	v_mfma_f32_16x16x32_bf16 v[50:53], v[220:223], v[180:183], v[50:53]
	v_mfma_f32_16x16x32_bf16 v[38:41], v[212:215], v[188:191], v[38:41]
	v_mfma_f32_16x16x32_bf16 v[34:37], v[220:223], v[188:191], v[34:37]
	v_mfma_f32_16x16x32_bf16 v[22:25], v[212:215], v[196:199], v[22:25]
	v_mfma_f32_16x16x32_bf16 v[18:21], v[220:223], v[196:199], v[18:21]
	v_mfma_f32_16x16x32_bf16 v[6:9], v[212:215], v[204:207], v[6:9]
	v_mfma_f32_16x16x32_bf16 v[2:5], v[220:223], v[204:207], v[2:5]
	s_setprio 0
	s_add_i32 s54, 0, 0x18000
	v_add_u32_e32 v134, s54, v149
	s_barrier
	ds_read_b128 v[160:163], v134
	ds_read_b128 v[164:167], v134 offset:1024
	ds_read_b128 v[168:171], v134 offset:2048
	ds_read_b128 v[172:175], v134 offset:3072
	s_mov_b32 m0, s39
	ds_read_b128 v[176:179], v151 offset:32768
	ds_read_b128 v[180:183], v151 offset:33792
	ds_read_b128 v[184:187], v151 offset:34816
	ds_read_b128 v[188:191], v151 offset:35840
	ds_read_b128 v[192:195], v151 offset:36864
	ds_read_b128 v[196:199], v151 offset:37888
	ds_read_b128 v[200:203], v151 offset:38912
	ds_read_b128 v[204:207], v151 offset:39936
	v_cndmask_b32_e32 v134, v140, v153, vcc
	global_load_lds_dwordx4 v139, s[26:27]
	s_mov_b32 m0, s40
	s_nop 0
	global_load_lds_dwordx4 v134, s[26:27]
	s_waitcnt lgkmcnt(8)
	s_barrier
	s_waitcnt lgkmcnt(0)
	s_setprio 1
	s_waitcnt lgkmcnt(0)
	v_mfma_f32_16x16x32_bf16 v[126:129], v[160:163], v[176:179], v[126:129]
	v_mfma_f32_16x16x32_bf16 v[122:125], v[168:171], v[176:179], v[122:125]
	v_mfma_f32_16x16x32_bf16 v[110:113], v[160:163], v[184:187], v[110:113]
	v_mfma_f32_16x16x32_bf16 v[106:109], v[168:171], v[184:187], v[106:109]
	v_mfma_f32_16x16x32_bf16 v[94:97], v[160:163], v[192:195], v[94:97]
	v_mfma_f32_16x16x32_bf16 v[90:93], v[168:171], v[192:195], v[90:93]
	v_mfma_f32_16x16x32_bf16 v[78:81], v[160:163], v[200:203], v[78:81]
	v_mfma_f32_16x16x32_bf16 v[74:77], v[168:171], v[200:203], v[74:77]
	v_mfma_f32_16x16x32_bf16 v[126:129], v[164:167], v[180:183], v[126:129]
	v_mfma_f32_16x16x32_bf16 v[122:125], v[172:175], v[180:183], v[122:125]
	v_mfma_f32_16x16x32_bf16 v[110:113], v[164:167], v[188:191], v[110:113]
	v_mfma_f32_16x16x32_bf16 v[106:109], v[172:175], v[188:191], v[106:109]
	v_mfma_f32_16x16x32_bf16 v[94:97], v[164:167], v[196:199], v[94:97]
	v_mfma_f32_16x16x32_bf16 v[90:93], v[172:175], v[196:199], v[90:93]
	v_mfma_f32_16x16x32_bf16 v[78:81], v[164:167], v[204:207], v[78:81]
	v_mfma_f32_16x16x32_bf16 v[74:77], v[172:175], v[204:207], v[74:77]
	s_setprio 0
	s_barrier
	s_add_i32 s26, 0, 0x1c000
	s_add_i32 s27, s54, s36
	v_add_u32_e32 v134, s26, v149
	v_lshl_add_u64 v[226:227], s[24:25], 0, v[130:131]
	s_mov_b32 m0, s27
	ds_read_b128 v[208:211], v134
	ds_read_b128 v[212:215], v134 offset:1024
	ds_read_b128 v[216:219], v134 offset:2048
	ds_read_b128 v[220:223], v134 offset:3072
	global_load_lds_dwordx4 v[226:227], off
	v_lshl_add_u64 v[226:227], s[24:25], 0, v[132:133]
	s_add_i32 m0, s27, 0x2000
	s_nop 0
	global_load_lds_dwordx4 v[226:227], off
	s_barrier
	s_waitcnt lgkmcnt(0)
	s_setprio 1
	s_waitcnt lgkmcnt(0)
	v_mfma_f32_16x16x32_bf16 v[118:121], v[208:211], v[176:179], v[118:121]
	v_mfma_f32_16x16x32_bf16 v[114:117], v[216:219], v[176:179], v[114:117]
	v_mfma_f32_16x16x32_bf16 v[102:105], v[208:211], v[184:187], v[102:105]
	v_mfma_f32_16x16x32_bf16 v[98:101], v[216:219], v[184:187], v[98:101]
	v_mfma_f32_16x16x32_bf16 v[86:89], v[208:211], v[192:195], v[86:89]
	v_mfma_f32_16x16x32_bf16 v[82:85], v[216:219], v[192:195], v[82:85]
	v_mfma_f32_16x16x32_bf16 v[70:73], v[208:211], v[200:203], v[70:73]
	v_mfma_f32_16x16x32_bf16 v[66:69], v[216:219], v[200:203], v[66:69]
	v_mfma_f32_16x16x32_bf16 v[118:121], v[212:215], v[180:183], v[118:121]
	v_mfma_f32_16x16x32_bf16 v[114:117], v[220:223], v[180:183], v[114:117]
	v_mfma_f32_16x16x32_bf16 v[102:105], v[212:215], v[188:191], v[102:105]
	v_mfma_f32_16x16x32_bf16 v[98:101], v[220:223], v[188:191], v[98:101]
	v_mfma_f32_16x16x32_bf16 v[86:89], v[212:215], v[196:199], v[86:89]
	v_mfma_f32_16x16x32_bf16 v[82:85], v[220:223], v[196:199], v[82:85]
	v_mfma_f32_16x16x32_bf16 v[70:73], v[212:215], v[204:207], v[70:73]
	v_mfma_f32_16x16x32_bf16 v[66:69], v[220:223], v[204:207], v[66:69]
	s_setprio 0
	s_mov_b32 m0, s43
	v_lshl_add_u64 v[226:227], v[230:231], 0, s[10:11]
	s_barrier
; #define PG8_STAGE(bufoff, gbase, v0, v1) do { \
;         __builtin_amdgcn_global_load_lds((const unsigned*)((const char*)(gbase) + (v0)), (LAS unsigned*)(lds + (bufoff) + ldsw), 16, 0, 0); \
;         __builtin_amdgcn_global_load_lds((const unsigned*)((const char*)(gbase) + (v1)), (LAS unsigned*)(lds + (bufoff) + ldsw + 8192), 16, 0, 0); } while (0)
; #define PG8_LDA(dst, b, h) do { _Pragma("unroll") for (int m = 0; m < 4; ++m) _Pragma("unroll") for (int k = 0; k < 2; ++k) dst[m][k] = *(const LAS bf16x8*)(lds + PG8_SA(b, h) + aoff + m * 2048 + k * 1024); } while (0)
; #define PG8_MMA(ai, bj, At, Bt) do { __builtin_amdgcn_s_setprio(1); _Pragma("unroll") for (int m = 0; m < 4; ++m) _Pragma("unroll") for (int n = 0; n < 2; ++n) _Pragma("unroll") for (int k = 0; k < 2; ++k) \
;         acc[ai][bj][m][n] = __builtin_amdgcn_mfma_f32_16x16x32_bf16(Bt[n][k], At[m][k], acc[ai][bj][m][n], 0, 0, 0); __builtin_amdgcn_s_setprio(0); } while (0)
; #define PG8_WAIT_L(n) asm volatile("s_waitcnt lgkmcnt(" #n ")" ::: "memory")
; #define PG8_BAR __builtin_amdgcn_s_barrier()
; #define PG8_SCHED __builtin_amdgcn_sched_barrier(0)
; template <class Epi, class Sched>
; __device__ __forceinline__ void gemm_phase(LAS unsigned char* lds, const int K, const Sched& S, const Epi& E) {
;     ...
;             PG8_LDA(At, 1, 1); PG8_STAGE(PG8_SA(1, 0), a3, x00, x01);
;             PG8_BAR; PG8_WAIT_L(0); PG8_MMA(1, 0, At, B0); PG8_BAR; PG8_SCHED;
;             PG8_STAGE(PG8_SB(1, 1), b3 + hstep, voffB0, voffB1);
; __device__ __forceinline__ bool bg_decode(int st, int wg, int NW, int lane, KP kp, const float*& src, int& ldS, bf16_t*& dst, int& o2) {
;     ...
;         const int r2 = r - 65536, e = r2 >> 9, kc = (r2 >> 3) & 63, cc = r2 & 7, n = cc * 256 + lane;
;         ldS = D; o2 = 128 * 8;
;         src = kp->in[29] + ((size_t)(l * NE + e) * FF + kc * 8) * D + n;
;         dst = (bf16_t*)(ws + WS_WD) + l * WD_L + (size_t)e * D * FF + ((size_t)kc * D + n) * 8;
	ds_read_b128 v[176:179], v151 offset:49152
	ds_read_b128 v[180:183], v151 offset:50176
	ds_read_b128 v[184:187], v151 offset:51200
	ds_read_b128 v[188:191], v151 offset:52224
	ds_read_b128 v[192:195], v151 offset:53248
	ds_read_b128 v[196:199], v151 offset:54272
	ds_read_b128 v[200:203], v151 offset:55296
	ds_read_b128 v[204:207], v151 offset:56320
	global_load_lds_dwordx4 v[226:227], off
	v_lshl_add_u64 v[224:225], v[224:225], 0, s[10:11]
	s_mov_b32 m0, s44
	s_nop 0
	global_load_lds_dwordx4 v[224:225], off
	s_barrier
	s_waitcnt lgkmcnt(0)
	s_setprio 1
	s_waitcnt lgkmcnt(0)
	v_mfma_f32_16x16x32_bf16 v[62:65], v[160:163], v[176:179], v[62:65]
	v_mfma_f32_16x16x32_bf16 v[58:61], v[168:171], v[176:179], v[58:61]
	v_mfma_f32_16x16x32_bf16 v[46:49], v[160:163], v[184:187], v[46:49]
	v_mfma_f32_16x16x32_bf16 v[42:45], v[168:171], v[184:187], v[42:45]
	v_mfma_f32_16x16x32_bf16 v[30:33], v[160:163], v[192:195], v[30:33]
	v_mfma_f32_16x16x32_bf16 v[26:29], v[168:171], v[192:195], v[26:29]
	v_mfma_f32_16x16x32_bf16 v[14:17], v[160:163], v[200:203], v[14:17]
	v_mfma_f32_16x16x32_bf16 v[10:13], v[168:171], v[200:203], v[10:13]
	v_mfma_f32_16x16x32_bf16 v[62:65], v[164:167], v[180:183], v[62:65]
	v_mfma_f32_16x16x32_bf16 v[58:61], v[172:175], v[180:183], v[58:61]
	v_mfma_f32_16x16x32_bf16 v[46:49], v[164:167], v[188:191], v[46:49]
	v_mfma_f32_16x16x32_bf16 v[42:45], v[172:175], v[188:191], v[42:45]
	v_mfma_f32_16x16x32_bf16 v[30:33], v[164:167], v[196:199], v[30:33]
	v_mfma_f32_16x16x32_bf16 v[26:29], v[172:175], v[196:199], v[26:29]
	v_mfma_f32_16x16x32_bf16 v[14:17], v[164:167], v[204:207], v[14:17]
	v_mfma_f32_16x16x32_bf16 v[10:13], v[172:175], v[204:207], v[10:13]
	s_setprio 0
	s_barrier
	s_add_u32 s22, s22, 0x20800
	s_addc_u32 s23, s23, 0
	s_add_i32 s24, s26, s36
	v_lshl_add_u64 v[160:161], s[22:23], 0, v[130:131]
	s_mov_b32 m0, s24
	s_nop 0
	global_load_lds_dwordx4 v[160:161], off
	v_lshl_add_u64 v[160:161], s[22:23], 0, v[132:133]
	s_add_i32 m0, s24, 0x2000
	s_nop 0
	global_load_lds_dwordx4 v[160:161], off
	s_mov_b32 s83, 0
	s_cmp_eq_u32 s82, 0
	s_cbranch_scc1 .Lpb1_l1
	s_waitcnt vmcnt(8)
	v_cvt_pk_bf16_f32 v244, v236, v237
	v_cvt_pk_bf16_f32 v245, v238, v239
	v_cvt_pk_bf16_f32 v246, v240, v241
	v_cvt_pk_bf16_f32 v247, v242, v243
	global_store_dwordx4 v249, v[244:247], s[80:81]
	s_mov_b32 s82, 0
	s_mov_b32 s83, 1
.Lpb1_l1:
	s_cmp_ge_u32 s70, 0xc0000
	s_cbranch_scc1 .Lpb1_l2
	s_lshr_b32 s84, s70, 2
	s_sub_u32 s84, s84, 0x28000
	s_lshr_b32 s85, s84, 9
	s_bfe_u32 s86, s84, 0x60003
	s_and_b32 s87, s84, 7
	s_and_b32 s88, s70, 3
	s_add_u32 s89, s85, 64
	s_lshl_b32 s89, s89, 22
	s_lshl_b32 s90, s86, 16
	s_add_u32 s89, s89, s90
	s_lshl_b32 s90, s87, 10
	s_add_u32 s89, s89, s90
	s_lshl_b32 s90, s88, 8
	s_add_u32 s89, s89, s90
	s_add_u32 s72, s74, s89
	s_addc_u32 s73, s75, 0
	s_lshl_b32 s89, s85, 21
	s_lshl_b32 s90, s86, 15
	s_add_u32 s89, s89, s90
	s_lshl_b32 s90, s87, 12
	s_add_u32 s89, s89, s90
	s_lshl_b32 s90, s88, 10
	s_add_u32 s89, s89, s90
	s_add_u32 s89, s89, 0x2ca30000
	s_add_u32 s80, s78, s89
	s_addc_u32 s81, s79, 0
	global_load_dword v236, v248, s[72:73]
	s_add_u32 s72, s72, 0x2000
	s_addc_u32 s73, s73, 0
	global_load_dword v237, v248, s[72:73]
	s_add_u32 s72, s72, 0x2000
	s_addc_u32 s73, s73, 0
	global_load_dword v238, v248, s[72:73]
	s_add_u32 s72, s72, 0x2000
	s_addc_u32 s73, s73, 0
	global_load_dword v239, v248, s[72:73]
	s_add_u32 s72, s72, 0x2000
	s_addc_u32 s73, s73, 0
	global_load_dword v240, v248, s[72:73]
	s_add_u32 s72, s72, 0x2000
	s_addc_u32 s73, s73, 0
	global_load_dword v241, v248, s[72:73]
	s_add_u32 s72, s72, 0x2000
	s_addc_u32 s73, s73, 0
	global_load_dword v242, v248, s[72:73]
	s_add_u32 s72, s72, 0x2000
	s_addc_u32 s73, s73, 0
	global_load_dword v243, v248, s[72:73]
	s_add_u32 s70, s70, 1
	s_and_b32 s84, s70, 3
	s_cmp_eq_u32 s84, 0
	s_cselect_b32 s84, s71, 0
	s_add_u32 s70, s70, s84
	s_mov_b32 s82, 1
	s_add_u32 s83, s83, 8

; __device__ __forceinline__ unsigned cvt_pk_bf16(float lo, float hi) { unsigned r; asm volatile("v_cvt_pk_bf16_f32 %0, %1, %2" : "=v"(r) : "v"(lo), "v"(hi)); return r; }
; __device__ __forceinline__ float fdivf(float a, float b) { return a * __builtin_amdgcn_rcpf(b); }
; #define PG8_MMA(ai, bj, At, Bt) do { __builtin_amdgcn_s_setprio(1); _Pragma("unroll") for (int m = 0; m < 4; ++m) _Pragma("unroll") for (int n = 0; n < 2; ++n) _Pragma("unroll") for (int k = 0; k < 2; ++k) \
;         acc[ai][bj][m][n] = __builtin_amdgcn_mfma_f32_16x16x32_bf16(Bt[n][k], At[m][k], acc[ai][bj][m][n], 0, 0, 0); __builtin_amdgcn_s_setprio(0); } while (0)
; #define PG8_WAIT_V(n) asm volatile("s_waitcnt vmcnt(" #n ")" ::: "memory")
; #define PG8_BAR __builtin_amdgcn_s_barrier()
; template <class Epi, class Sched>
; __device__ __forceinline__ void gemm_phase(LAS unsigned char* lds, const int K, const Sched& S, const Epi& E) {
;     ...
;             PG8_WAIT_V(6); PG8_BAR; PG8_MMA(1, 1, At, B1); PG8_BAR;
;         }
;     __device__ __forceinline__ void operator()(const f32x4 (&acc)[2][2][4][2], const Unit& u, int wr, int wc, int fr, int fq) const {
;         const int row0 = u.rbase + wr * 64 + fr, col0 = u.pn * HALF + wc * 32 + 8 * fq;
; #pragma unroll
;         for (int ai = 0; ai < 2; ++ai)
; #pragma unroll
;             for (int m = 0; m < 4; ++m) { bf16_t* rowp = O + (size_t)(row0 + ai * HALF + m * 16) * FF + col0;
;                 float h[8];
; #pragma unroll
;                 for (int n = 0; n < 2; ++n)
; #pragma unroll
;                     for (int j = 0; j < 4; ++j) { const float g = acc[ai][0][m][n][j], up = acc[ai][1][m][n][j]; h[n * 4 + j] = fdivf(g, 1.f + __expf(-g)) * up; }
;                 u32x4 w; w.x = cvt_pk_bf16(h[0], h[1]); w.y = cvt_pk_bf16(h[2], h[3]); w.z = cvt_pk_bf16(h[4], h[5]); w.w = cvt_pk_bf16(h[6], h[7]);
;                 *(u32x4*)rowp = w; }
;     }
.Lpb1_j:
	s_barrier
	s_setprio 1
	v_mfma_f32_16x16x32_bf16 v[54:57], v[208:211], v[176:179], v[54:57]
	v_mfma_f32_16x16x32_bf16 v[50:53], v[216:219], v[176:179], v[50:53]
	v_mfma_f32_16x16x32_bf16 v[38:41], v[208:211], v[184:187], v[38:41]
	v_mfma_f32_16x16x32_bf16 v[34:37], v[216:219], v[184:187], v[34:37]
	v_mfma_f32_16x16x32_bf16 v[22:25], v[208:211], v[192:195], v[22:25]
	v_mfma_f32_16x16x32_bf16 v[18:21], v[216:219], v[192:195], v[18:21]
	v_mfma_f32_16x16x32_bf16 v[6:9], v[208:211], v[200:203], v[6:9]
	v_mfma_f32_16x16x32_bf16 v[2:5], v[216:219], v[200:203], v[2:5]
	v_mfma_f32_16x16x32_bf16 v[54:57], v[212:215], v[180:183], v[54:57]
	v_mfma_f32_16x16x32_bf16 v[50:53], v[220:223], v[180:183], v[50:53]
	v_mfma_f32_16x16x32_bf16 v[38:41], v[212:215], v[188:191], v[38:41]
	v_mfma_f32_16x16x32_bf16 v[34:37], v[220:223], v[188:191], v[34:37]
	v_mfma_f32_16x16x32_bf16 v[22:25], v[212:215], v[196:199], v[22:25]
	v_mfma_f32_16x16x32_bf16 v[18:21], v[220:223], v[196:199], v[18:21]
	v_mfma_f32_16x16x32_bf16 v[6:9], v[212:215], v[204:207], v[6:9]
	v_mfma_f32_16x16x32_bf16 v[2:5], v[220:223], v[204:207], v[2:5]
	s_setprio 0
	s_add_i32 s53, s53, 2
	s_add_u32 s13, s13, 0x40000
	s_addc_u32 s15, s15, 0
	s_add_u32 s20, s20, 0x100
	s_addc_u32 s21, s21, 0
	s_cmp_gt_u32 s53, 29
	s_barrier
	s_cbranch_scc0 .LBB0_1831
	v_mul_f32_e32 v134, 0xbfb8aa3b, v126
	v_exp_f32_e32 v134, v134
	v_mul_f32_e32 v136, 0xbfb8aa3b, v127
	v_exp_f32_e32 v136, v136
	v_add_u32_e32 v138, v157, v137
	v_add_f32_e32 v134, 1.0, v134
	v_rcp_f32_e32 v134, v134
	v_add_f32_e32 v136, 1.0, v136
	v_rcp_f32_e32 v136, v136
	v_readlane_b32 s13, v254, 27
	v_mul_f32_e32 v126, v126, v134
	v_mul_f32_e32 v118, v126, v118
	v_mul_f32_e32 v126, v127, v136
	v_mul_f32_e32 v127, 0xbfb8aa3b, v128
	v_exp_f32_e32 v127, v127
	v_mul_f32_e32 v134, 0xbfb8aa3b, v129
	v_exp_f32_e32 v134, v134
	v_mul_f32_e32 v119, v126, v119
	v_add_f32_e32 v126, 1.0, v127
	v_rcp_f32_e32 v126, v126
	v_add_f32_e32 v127, 1.0, v134
	v_mul_f32_e32 v134, 0xbfb8aa3b, v122
	v_rcp_f32_e32 v127, v127
	v_exp_f32_e32 v134, v134
	v_mul_f32_e32 v126, v128, v126
	v_mul_f32_e32 v120, v126, v120
	v_mul_f32_e32 v126, v129, v127
	v_add_f32_e32 v127, 1.0, v134
	v_rcp_f32_e32 v127, v127
	v_mul_f32_e32 v128, 0xbfb8aa3b, v123
	v_exp_f32_e32 v128, v128
	v_mul_f32_e32 v121, v126, v121
	v_mul_f32_e32 v122, v122, v127
	v_mul_f32_e32 v122, v122, v114
	v_add_f32_e32 v114, 1.0, v128
	v_mul_f32_e32 v126, 0xbfb8aa3b, v124
	v_rcp_f32_e32 v114, v114
	v_exp_f32_e32 v126, v126
	v_mul_f32_e32 v127, 0xbfb8aa3b, v125
	v_exp_f32_e32 v127, v127
	v_mul_f32_e32 v114, v123, v114
	v_add_f32_e32 v123, 1.0, v126
	v_rcp_f32_e32 v123, v123
	v_add_f32_e32 v126, 1.0, v127
	v_rcp_f32_e32 v126, v126
	v_mul_f32_e32 v127, v114, v115
	v_mul_f32_e32 v114, v124, v123
	v_mul_f32_e32 v123, v114, v116
	v_mul_f32_e32 v114, v125, v126
	v_cvt_pk_bf16_f32 v116, v118, v119
	v_mul_f32_e32 v119, 0xbfb8aa3b, v110
	v_mul_f32_e32 v124, v114, v117
	v_cvt_pk_bf16_f32 v117, v120, v121
	v_exp_f32_e32 v120, v119
	v_mul_f32_e32 v119, 0xbfb8aa3b, v111
	v_exp_f32_e32 v121, v119
	v_ashrrev_i32_e32 v139, 31, v138
	v_add_f32_e32 v120, 1.0, v120
	v_rcp_f32_e32 v120, v120
	v_add_f32_e32 v121, 1.0, v121
	v_rcp_f32_e32 v121, v121
	v_lshl_or_b32 v140, s13, 7, v150
	v_lshlrev_b64 v[138:139], 10, v[138:139]
	v_ashrrev_i32_e32 v141, 31, v140
	v_lshl_add_u64 v[138:139], s[6:7], 0, v[138:139]
	v_mul_f32_e32 v110, v110, v120
	v_lshl_add_u64 v[114:115], v[140:141], 1, v[138:139]
	v_mul_f32_e32 v102, v110, v102
	v_mul_f32_e32 v110, v111, v121
	v_mul_f32_e32 v111, 0xbfb8aa3b, v112
	v_cvt_pk_bf16_f32 v118, v122, v127
	v_cvt_pk_bf16_f32 v119, v123, v124
	global_store_dwordx4 v[114:115], v[116:119], off
	v_exp_f32_e32 v111, v111
	v_mul_f32_e32 v103, v110, v103
	v_mul_f32_e32 v116, 0xbfb8aa3b, v113
	v_exp_f32_e32 v116, v116
	v_add_f32_e32 v110, 1.0, v111
	v_rcp_f32_e32 v110, v110
	s_mov_b32 s13, s12
	v_add_f32_e32 v111, 1.0, v116
	v_mul_f32_e32 v116, 0xbfb8aa3b, v106
	v_rcp_f32_e32 v111, v111
	v_exp_f32_e32 v116, v116
	v_mul_f32_e32 v110, v112, v110
	v_mul_f32_e32 v104, v110, v104
	v_mul_f32_e32 v110, v113, v111
	v_add_f32_e32 v111, 1.0, v116
	v_rcp_f32_e32 v111, v111
	v_mul_f32_e32 v112, 0xbfb8aa3b, v107
	v_exp_f32_e32 v112, v112
	v_mul_f32_e32 v105, v110, v105
	v_mul_f32_e32 v106, v106, v111
	v_mul_f32_e32 v106, v106, v98
	v_add_f32_e32 v98, 1.0, v112
	v_mul_f32_e32 v110, 0xbfb8aa3b, v108
	v_rcp_f32_e32 v98, v98
	v_exp_f32_e32 v110, v110
	v_mul_f32_e32 v111, 0xbfb8aa3b, v109
	v_exp_f32_e32 v111, v111
	v_mul_f32_e32 v98, v107, v98
	v_add_f32_e32 v107, 1.0, v110
	v_rcp_f32_e32 v107, v107
	v_add_f32_e32 v110, 1.0, v111
	v_rcp_f32_e32 v110, v110
	v_mul_f32_e32 v111, v98, v99
	v_mul_f32_e32 v98, v108, v107
	v_mul_f32_e32 v107, v98, v100
	v_mul_f32_e32 v98, v109, v110
	v_mul_f32_e32 v101, v98, v101
	v_cvt_pk_bf16_f32 v98, v102, v103
	v_mul_f32_e32 v102, 0xbfb8aa3b, v94
	v_cvt_pk_bf16_f32 v99, v104, v105
	v_exp_f32_e32 v104, v102
	v_mul_f32_e32 v102, 0xbfb8aa3b, v95
	v_exp_f32_e32 v105, v102
	v_add_co_u32_e32 v102, vcc, s42, v114
	v_add_f32_e32 v104, 1.0, v104
	v_rcp_f32_e32 v104, v104
	v_add_f32_e32 v105, 1.0, v105
	v_rcp_f32_e32 v105, v105
	v_addc_co_u32_e32 v103, vcc, 0, v115, vcc
	v_mul_f32_e32 v94, v94, v104
	v_mul_f32_e32 v86, v94, v86
	v_mul_f32_e32 v94, v95, v105
	v_mul_f32_e32 v95, 0xbfb8aa3b, v96
	v_cvt_pk_bf16_f32 v100, v106, v111
	v_cvt_pk_bf16_f32 v101, v107, v101
	global_store_dwordx4 v[102:103], v[98:101], off
	v_exp_f32_e32 v95, v95
	v_mul_f32_e32 v87, v94, v87
	v_mul_f32_e32 v98, 0xbfb8aa3b, v97
	v_exp_f32_e32 v98, v98
	v_add_f32_e32 v94, 1.0, v95
	v_rcp_f32_e32 v94, v94
	v_mov_b32_e32 v157, v152
	v_add_f32_e32 v95, 1.0, v98
; __device__ __forceinline__ unsigned cvt_pk_bf16(float lo, float hi) { unsigned r; asm volatile("v_cvt_pk_bf16_f32 %0, %1, %2" : "=v"(r) : "v"(lo), "v"(hi)); return r; }
; __device__ __forceinline__ float fdivf(float a, float b) { return a * __builtin_amdgcn_rcpf(b); }
;     __device__ __forceinline__ void operator()(const f32x4 (&acc)[2][2][4][2], const Unit& u, int wr, int wc, int fr, int fq) const {
;         const int row0 = u.rbase + wr * 64 + fr, col0 = u.pn * HALF + wc * 32 + 8 * fq;
; #pragma unroll
;         for (int ai = 0; ai < 2; ++ai)
; #pragma unroll
;             for (int m = 0; m < 4; ++m) { bf16_t* rowp = O + (size_t)(row0 + ai * HALF + m * 16) * FF + col0;
;                 float h[8];
; #pragma unroll
;                 for (int n = 0; n < 2; ++n)
; #pragma unroll
;                     for (int j = 0; j < 4; ++j) { const float g = acc[ai][0][m][n][j], up = acc[ai][1][m][n][j]; h[n * 4 + j] = fdivf(g, 1.f + __expf(-g)) * up; }
;                 u32x4 w; w.x = cvt_pk_bf16(h[0], h[1]); w.y = cvt_pk_bf16(h[2], h[3]); w.z = cvt_pk_bf16(h[4], h[5]); w.w = cvt_pk_bf16(h[6], h[7]);
;                 *(u32x4*)rowp = w; }
;     }
	v_mul_f32_e32 v98, 0xbfb8aa3b, v90
	v_rcp_f32_e32 v95, v95
	v_exp_f32_e32 v98, v98
	v_mul_f32_e32 v94, v96, v94
	v_mul_f32_e32 v88, v94, v88
	v_mul_f32_e32 v94, v97, v95
	v_add_f32_e32 v95, 1.0, v98
	v_rcp_f32_e32 v95, v95
	v_mul_f32_e32 v96, 0xbfb8aa3b, v91
	v_exp_f32_e32 v96, v96
	v_mul_f32_e32 v89, v94, v89
	v_mul_f32_e32 v90, v90, v95
	v_mul_f32_e32 v90, v90, v82
	v_add_f32_e32 v82, 1.0, v96
	v_mul_f32_e32 v94, 0xbfb8aa3b, v92
	v_rcp_f32_e32 v82, v82
	v_exp_f32_e32 v94, v94
	v_mul_f32_e32 v95, 0xbfb8aa3b, v93
	v_exp_f32_e32 v95, v95
	v_mul_f32_e32 v82, v91, v82
	v_add_f32_e32 v91, 1.0, v94
	v_rcp_f32_e32 v91, v91
	v_add_f32_e32 v94, 1.0, v95
	v_rcp_f32_e32 v94, v94
	v_mul_f32_e32 v95, v82, v83
	v_mul_f32_e32 v82, v92, v91
	v_mul_f32_e32 v91, v82, v84
	v_mul_f32_e32 v82, v93, v94
	v_mul_f32_e32 v85, v82, v85
	v_cvt_pk_bf16_f32 v82, v86, v87
	v_mul_f32_e32 v86, 0xbfb8aa3b, v78
	v_cvt_pk_bf16_f32 v83, v88, v89
	v_exp_f32_e32 v88, v86
	v_mul_f32_e32 v86, 0xbfb8aa3b, v79
	v_exp_f32_e32 v89, v86
	v_add_co_u32_e32 v86, vcc, s45, v114
	v_add_f32_e32 v88, 1.0, v88
	v_rcp_f32_e32 v88, v88
	v_add_f32_e32 v89, 1.0, v89
	v_rcp_f32_e32 v89, v89
	v_addc_co_u32_e32 v87, vcc, 0, v115, vcc
	v_mul_f32_e32 v78, v78, v88
	v_mul_f32_e32 v70, v78, v70
	v_mul_f32_e32 v78, v79, v89
	v_mul_f32_e32 v79, 0xbfb8aa3b, v80
	v_cvt_pk_bf16_f32 v84, v90, v95
	v_cvt_pk_bf16_f32 v85, v91, v85
	global_store_dwordx4 v[86:87], v[82:85], off
	v_exp_f32_e32 v79, v79
	v_mul_f32_e32 v71, v78, v71
	v_mul_f32_e32 v82, 0xbfb8aa3b, v81
	v_exp_f32_e32 v82, v82
	v_add_f32_e32 v78, 1.0, v79
	v_rcp_f32_e32 v78, v78
	v_writelane_b32 v254, s13, 27
	v_add_f32_e32 v79, 1.0, v82
	v_mul_f32_e32 v82, 0xbfb8aa3b, v74
	v_rcp_f32_e32 v79, v79
	v_exp_f32_e32 v82, v82
	v_mul_f32_e32 v78, v80, v78
	v_mul_f32_e32 v72, v78, v72
	v_mul_f32_e32 v78, v81, v79
	v_add_f32_e32 v79, 1.0, v82
	v_rcp_f32_e32 v79, v79
	v_mul_f32_e32 v80, 0xbfb8aa3b, v75
	v_exp_f32_e32 v80, v80
	v_mul_f32_e32 v73, v78, v73
	v_mul_f32_e32 v74, v74, v79
	v_mul_f32_e32 v74, v74, v66
	v_add_f32_e32 v66, 1.0, v80
	v_mul_f32_e32 v78, 0xbfb8aa3b, v76
	v_rcp_f32_e32 v66, v66
	v_exp_f32_e32 v78, v78
	v_mul_f32_e32 v79, 0xbfb8aa3b, v77
	v_exp_f32_e32 v79, v79
	v_mul_f32_e32 v66, v75, v66
	v_add_f32_e32 v75, 1.0, v78
	v_rcp_f32_e32 v75, v75
	v_add_f32_e32 v78, 1.0, v79
	v_rcp_f32_e32 v78, v78
	v_mul_f32_e32 v79, v66, v67
	v_mul_f32_e32 v66, v76, v75
	v_mul_f32_e32 v75, v66, v68
	v_mul_f32_e32 v66, v77, v78
	v_mul_f32_e32 v69, v66, v69
	v_cvt_pk_bf16_f32 v66, v70, v71
	v_mul_f32_e32 v70, 0xbfb8aa3b, v62
	v_cvt_pk_bf16_f32 v67, v72, v73
	v_exp_f32_e32 v72, v70
	v_mul_f32_e32 v70, 0xbfb8aa3b, v63
	v_exp_f32_e32 v73, v70
	v_add_co_u32_e32 v70, vcc, s47, v114
	v_add_f32_e32 v72, 1.0, v72
	v_rcp_f32_e32 v72, v72
	v_add_f32_e32 v73, 1.0, v73
	v_rcp_f32_e32 v73, v73
	v_addc_co_u32_e32 v71, vcc, 0, v115, vcc
	v_mul_f32_e32 v62, v62, v72
	v_mul_f32_e32 v54, v62, v54
	v_mul_f32_e32 v62, v63, v73
	v_mul_f32_e32 v63, 0xbfb8aa3b, v64
	v_cvt_pk_bf16_f32 v68, v74, v79
	v_cvt_pk_bf16_f32 v69, v75, v69
	global_store_dwordx4 v[70:71], v[66:69], off
	v_exp_f32_e32 v63, v63
	v_mul_f32_e32 v55, v62, v55
	v_mul_f32_e32 v66, 0xbfb8aa3b, v65
	v_exp_f32_e32 v66, v66
	v_add_f32_e32 v62, 1.0, v63
	v_rcp_f32_e32 v62, v62
	v_mov_b32_e32 v158, v156
	v_add_f32_e32 v63, 1.0, v66
	v_mul_f32_e32 v66, 0xbfb8aa3b, v58
	v_rcp_f32_e32 v63, v63
	v_exp_f32_e32 v66, v66
	v_mul_f32_e32 v62, v64, v62
	v_mul_f32_e32 v56, v62, v56
	v_mul_f32_e32 v62, v65, v63
	v_add_f32_e32 v63, 1.0, v66
	v_rcp_f32_e32 v63, v63
	v_mul_f32_e32 v64, 0xbfb8aa3b, v59
	v_exp_f32_e32 v64, v64
	v_mul_f32_e32 v57, v62, v57
	v_mul_f32_e32 v58, v58, v63
	v_mul_f32_e32 v58, v58, v50
	v_add_f32_e32 v50, 1.0, v64
	v_mul_f32_e32 v62, 0xbfb8aa3b, v60
	v_rcp_f32_e32 v50, v50
	v_exp_f32_e32 v62, v62
	v_mul_f32_e32 v63, 0xbfb8aa3b, v61
	v_exp_f32_e32 v63, v63
	v_mul_f32_e32 v50, v59, v50
	v_add_f32_e32 v59, 1.0, v62
	v_rcp_f32_e32 v59, v59
	v_add_f32_e32 v62, 1.0, v63
	v_rcp_f32_e32 v62, v62
	v_mul_f32_e32 v63, v50, v51
	v_mul_f32_e32 v50, v60, v59
	v_mul_f32_e32 v59, v50, v52
	v_mul_f32_e32 v50, v61, v62
	v_mul_f32_e32 v53, v50, v53
	v_cvt_pk_bf16_f32 v50, v54, v55
	v_mul_f32_e32 v54, 0xbfb8aa3b, v46
	v_cvt_pk_bf16_f32 v51, v56, v57
	v_exp_f32_e32 v56, v54
	v_mul_f32_e32 v54, 0xbfb8aa3b, v47
	v_exp_f32_e32 v57, v54
	v_add_co_u32_e32 v54, vcc, s49, v114
	v_add_f32_e32 v56, 1.0, v56
	v_rcp_f32_e32 v56, v56
	v_add_f32_e32 v57, 1.0, v57
	v_rcp_f32_e32 v57, v57
	v_addc_co_u32_e32 v55, vcc, 0, v115, vcc
	v_mul_f32_e32 v46, v46, v56
	v_mul_f32_e32 v38, v46, v38
	v_mul_f32_e32 v46, v47, v57
	v_mul_f32_e32 v47, 0xbfb8aa3b, v48
	v_cvt_pk_bf16_f32 v52, v58, v63
	v_cvt_pk_bf16_f32 v53, v59, v53
	global_store_dwordx4 v[54:55], v[50:53], off
; __device__ __forceinline__ unsigned cvt_pk_bf16(float lo, float hi) { unsigned r; asm volatile("v_cvt_pk_bf16_f32 %0, %1, %2" : "=v"(r) : "v"(lo), "v"(hi)); return r; }
; __device__ __forceinline__ float fdivf(float a, float b) { return a * __builtin_amdgcn_rcpf(b); }
; #define PG8_WAIT_V(n) asm volatile("s_waitcnt vmcnt(" #n ")" ::: "memory")
; #define PG8_BAR __builtin_amdgcn_s_barrier()
; template <class Epi, class Sched>
; __device__ __forceinline__ void gemm_phase(LAS unsigned char* lds, const int K, const Sched& S, const Epi& E) {
;     ...
;         if (!has_next) break;
; #pragma unroll
;         for (int a = 0; a < 2; ++a)
; #pragma unroll
;             for (int b = 0; b < 2; ++b)
; #pragma unroll
;                 for (int m = 0; m < 4; ++m)
; #pragma unroll
;                     for (int n = 0; n < 2; ++n) acc[a][b][m][n] = (f32x4){0.f, 0.f, 0.f, 0.f};
;         cur = nxt; cB = nB; c00 = n00; c01 = n01; c10 = n10; c11 = n11; ++ui;
;     }
;     PG8_WAIT_V(0);
;     if (wr == 0) PG8_BAR;
;     PG8_BAR;
;     __device__ __forceinline__ void operator()(const f32x4 (&acc)[2][2][4][2], const Unit& u, int wr, int wc, int fr, int fq) const {
;         const int row0 = u.rbase + wr * 64 + fr, col0 = u.pn * HALF + wc * 32 + 8 * fq;
; #pragma unroll
;         for (int ai = 0; ai < 2; ++ai)
; #pragma unroll
;             for (int m = 0; m < 4; ++m) { bf16_t* rowp = O + (size_t)(row0 + ai * HALF + m * 16) * FF + col0;
;                 float h[8];
; #pragma unroll
;                 for (int n = 0; n < 2; ++n)
; #pragma unroll
;                     for (int j = 0; j < 4; ++j) { const float g = acc[ai][0][m][n][j], up = acc[ai][1][m][n][j]; h[n * 4 + j] = fdivf(g, 1.f + __expf(-g)) * up; }
;                 u32x4 w; w.x = cvt_pk_bf16(h[0], h[1]); w.y = cvt_pk_bf16(h[2], h[3]); w.z = cvt_pk_bf16(h[4], h[5]); w.w = cvt_pk_bf16(h[6], h[7]);
;                 *(u32x4*)rowp = w; }
;     }
	v_exp_f32_e32 v47, v47
	v_mul_f32_e32 v39, v46, v39
	v_mul_f32_e32 v50, 0xbfb8aa3b, v49
	v_exp_f32_e32 v50, v50
	v_add_f32_e32 v46, 1.0, v47
	v_rcp_f32_e32 v46, v46
	v_mov_b32_e32 v136, v155
	v_add_f32_e32 v47, 1.0, v50
	v_mul_f32_e32 v50, 0xbfb8aa3b, v42
	v_rcp_f32_e32 v47, v47
	v_exp_f32_e32 v50, v50
	v_mul_f32_e32 v46, v48, v46
	v_mul_f32_e32 v40, v46, v40
	v_mul_f32_e32 v46, v49, v47
	v_add_f32_e32 v47, 1.0, v50
	v_rcp_f32_e32 v47, v47
	v_mul_f32_e32 v48, 0xbfb8aa3b, v43
	v_exp_f32_e32 v48, v48
	v_mul_f32_e32 v41, v46, v41
	v_mul_f32_e32 v42, v42, v47
	v_mul_f32_e32 v42, v42, v34
	v_add_f32_e32 v34, 1.0, v48
	v_mul_f32_e32 v46, 0xbfb8aa3b, v44
	v_rcp_f32_e32 v34, v34
	v_exp_f32_e32 v46, v46
	v_mul_f32_e32 v47, 0xbfb8aa3b, v45
	v_exp_f32_e32 v47, v47
	v_mul_f32_e32 v34, v43, v34
	v_add_f32_e32 v43, 1.0, v46
	v_rcp_f32_e32 v43, v43
	v_add_f32_e32 v46, 1.0, v47
	v_rcp_f32_e32 v46, v46
	v_mul_f32_e32 v47, v34, v35
	v_mul_f32_e32 v34, v44, v43
	v_mul_f32_e32 v43, v34, v36
	v_mul_f32_e32 v34, v45, v46
	v_mul_f32_e32 v37, v34, v37
	v_cvt_pk_bf16_f32 v34, v38, v39
	v_mul_f32_e32 v38, 0xbfb8aa3b, v30
	v_cvt_pk_bf16_f32 v35, v40, v41
	v_exp_f32_e32 v40, v38
	v_mul_f32_e32 v38, 0xbfb8aa3b, v31
	v_exp_f32_e32 v41, v38
	v_add_co_u32_e32 v38, vcc, s50, v114
	v_add_f32_e32 v40, 1.0, v40
	v_rcp_f32_e32 v40, v40
	v_add_f32_e32 v41, 1.0, v41
	v_rcp_f32_e32 v41, v41
	v_addc_co_u32_e32 v39, vcc, 0, v115, vcc
	v_mul_f32_e32 v30, v30, v40
	v_mul_f32_e32 v22, v30, v22
	v_mul_f32_e32 v30, v31, v41
	v_mul_f32_e32 v31, 0xbfb8aa3b, v32
	v_cvt_pk_bf16_f32 v36, v42, v47
	v_cvt_pk_bf16_f32 v37, v43, v37
	global_store_dwordx4 v[38:39], v[34:37], off
	v_exp_f32_e32 v31, v31
	v_mul_f32_e32 v23, v30, v23
	v_mul_f32_e32 v34, 0xbfb8aa3b, v33
	v_exp_f32_e32 v34, v34
	v_add_f32_e32 v30, 1.0, v31
	v_rcp_f32_e32 v30, v30
	v_mov_b32_e32 v138, v154
	v_add_f32_e32 v31, 1.0, v34
	v_mul_f32_e32 v34, 0xbfb8aa3b, v26
	v_rcp_f32_e32 v31, v31
	v_exp_f32_e32 v34, v34
	v_mul_f32_e32 v30, v32, v30
	v_mul_f32_e32 v24, v30, v24
	v_mul_f32_e32 v30, v33, v31
	v_add_f32_e32 v31, 1.0, v34
	v_rcp_f32_e32 v31, v31
	v_mul_f32_e32 v32, 0xbfb8aa3b, v27
	v_exp_f32_e32 v32, v32
	v_mul_f32_e32 v25, v30, v25
	v_mul_f32_e32 v26, v26, v31
	v_mul_f32_e32 v26, v26, v18
	v_add_f32_e32 v18, 1.0, v32
	v_mul_f32_e32 v30, 0xbfb8aa3b, v28
	v_rcp_f32_e32 v18, v18
	v_exp_f32_e32 v30, v30
	v_mul_f32_e32 v31, 0xbfb8aa3b, v29
	v_exp_f32_e32 v31, v31
	v_mul_f32_e32 v18, v27, v18
	v_add_f32_e32 v27, 1.0, v30
	v_rcp_f32_e32 v27, v27
	v_add_f32_e32 v30, 1.0, v31
	v_rcp_f32_e32 v30, v30
	v_mul_f32_e32 v31, v18, v19
	v_mul_f32_e32 v18, v28, v27
	v_mul_f32_e32 v27, v18, v20
	v_mul_f32_e32 v18, v29, v30
	v_mul_f32_e32 v21, v18, v21
	v_cvt_pk_bf16_f32 v18, v22, v23
	v_mul_f32_e32 v22, 0xbfb8aa3b, v14
	v_cvt_pk_bf16_f32 v19, v24, v25
	v_exp_f32_e32 v24, v22
	v_mul_f32_e32 v22, 0xbfb8aa3b, v15
	v_exp_f32_e32 v25, v22
	v_add_co_u32_e32 v22, vcc, s51, v114
	v_add_f32_e32 v24, 1.0, v24
	v_rcp_f32_e32 v24, v24
	v_add_f32_e32 v25, 1.0, v25
	v_rcp_f32_e32 v25, v25
	v_addc_co_u32_e32 v23, vcc, 0, v115, vcc
	v_mul_f32_e32 v14, v14, v24
	v_mul_f32_e32 v6, v14, v6
	v_mul_f32_e32 v14, v15, v25
	v_mul_f32_e32 v15, 0xbfb8aa3b, v16
	v_cvt_pk_bf16_f32 v20, v26, v31
	v_cvt_pk_bf16_f32 v21, v27, v21
	global_store_dwordx4 v[22:23], v[18:21], off
	v_exp_f32_e32 v15, v15
	v_mul_f32_e32 v7, v14, v7
	v_mul_f32_e32 v18, 0xbfb8aa3b, v17
	v_exp_f32_e32 v18, v18
	v_add_f32_e32 v14, 1.0, v15
	v_rcp_f32_e32 v14, v14
	v_mov_b32_e32 v140, v153
	v_add_f32_e32 v15, 1.0, v18
	v_mul_f32_e32 v18, 0xbfb8aa3b, v10
	v_rcp_f32_e32 v15, v15
	v_exp_f32_e32 v18, v18
	v_mul_f32_e32 v14, v16, v14
	v_mul_f32_e32 v8, v14, v8
	v_mul_f32_e32 v14, v17, v15
	v_add_f32_e32 v15, 1.0, v18
	v_rcp_f32_e32 v15, v15
	v_mul_f32_e32 v16, 0xbfb8aa3b, v11
	v_exp_f32_e32 v16, v16
	v_mul_f32_e32 v9, v14, v9
	v_mul_f32_e32 v10, v10, v15
	v_mul_f32_e32 v10, v10, v2
	v_add_f32_e32 v2, 1.0, v16
	v_mul_f32_e32 v14, 0xbfb8aa3b, v12
	v_rcp_f32_e32 v2, v2
	v_exp_f32_e32 v14, v14
	v_mul_f32_e32 v15, 0xbfb8aa3b, v13
	v_exp_f32_e32 v15, v15
	v_mul_f32_e32 v2, v11, v2
	v_add_f32_e32 v11, 1.0, v14
	v_rcp_f32_e32 v11, v11
	v_add_f32_e32 v14, 1.0, v15
	v_rcp_f32_e32 v14, v14
	v_mul_f32_e32 v15, v2, v3
	v_mul_f32_e32 v2, v12, v11
	v_mul_f32_e32 v11, v2, v4
	v_mul_f32_e32 v2, v13, v14
	v_mul_f32_e32 v5, v2, v5
	v_cvt_pk_bf16_f32 v2, v6, v7
	v_add_co_u32_e32 v6, vcc, 0x2c000, v114
	s_mov_b64 s[20:21], s[18:19]
	s_nop 0
	v_addc_co_u32_e32 v7, vcc, 0, v115, vcc
	s_and_b64 vcc, exec, s[16:17]
	v_cvt_pk_bf16_f32 v3, v8, v9
	v_cvt_pk_bf16_f32 v4, v10, v15
	v_cvt_pk_bf16_f32 v5, v11, v5
	global_store_dwordx4 v[6:7], v[2:5], off
	s_cbranch_vccz .LBB0_1822
	s_waitcnt vmcnt(0)
	s_cmpk_gt_u32 s30, 0xff
	s_cbranch_scc1 .LBB0_1835
	s_barrier

; __device__ __forceinline__ bool bg_decode(int st, int wg, int NW, int lane, KP kp, const float*& src, int& ldS, bf16_t*& dst, int& o2) {
;     ...
;         const int r2 = r - 65536, e = r2 >> 9, kc = (r2 >> 3) & 63, cc = r2 & 7, n = cc * 256 + lane;
;         ldS = D; o2 = 128 * 8;
;         src = kp->in[29] + ((size_t)(l * NE + e) * FF + kc * 8) * D + n;
;         dst = (bf16_t*)(ws + WS_WD) + l * WD_L + (size_t)e * D * FF + ((size_t)kc * D + n) * 8;
; template <int BANK> __device__ __forceinline__ void bg_issue1(BgState& b, int wg, int NW, int lane) {
;     ...
;     for (int i = 0; i < 8; ++i) { const float* p = src + (size_t)i * ldS;
;         asm volatile("global_load_dword %0, %4, off\n\tglobal_load_dword %1, %4, off offset:256\n\tglobal_load_dword %2, %4, off offset:512\n\tglobal_load_dword %3, %4, off offset:768"
;                      : "=&v"(b.r[(BANK * 8 + i) * 4 + 0]), "=&v"(b.r[(BANK * 8 + i) * 4 + 1]), "=&v"(b.r[(BANK * 8 + i) * 4 + 2]), "=&v"(b.r[(BANK * 8 + i) * 4 + 3]) : "v"(p) : "memory"); }
;     b.st += 1;
; }
.Lpb1_d1:
	s_cmp_ge_u32 s70, 0xc0000
	s_cbranch_scc1 .Lpb1_dend
	s_lshr_b32 s84, s70, 2
	s_sub_u32 s84, s84, 0x28000
	s_lshr_b32 s85, s84, 9
	s_bfe_u32 s86, s84, 0x60003
	s_and_b32 s87, s84, 7
	s_and_b32 s88, s70, 3
	s_add_u32 s89, s85, 64
	s_lshl_b32 s89, s89, 22
	s_lshl_b32 s90, s86, 16
	s_add_u32 s89, s89, s90
	s_lshl_b32 s90, s87, 10
	s_add_u32 s89, s89, s90
	s_lshl_b32 s90, s88, 8
	s_add_u32 s89, s89, s90
	s_add_u32 s72, s74, s89
	s_addc_u32 s73, s75, 0
	s_lshl_b32 s89, s85, 21
	s_lshl_b32 s90, s86, 15
	s_add_u32 s89, s89, s90
	s_lshl_b32 s90, s87, 12
	s_add_u32 s89, s89, s90
	s_lshl_b32 s90, s88, 10
	s_add_u32 s89, s89, s90
	s_add_u32 s89, s89, 0x2ca30000
	s_add_u32 s80, s78, s89
	s_addc_u32 s81, s79, 0
	global_load_dword v236, v248, s[72:73]
	s_add_u32 s72, s72, 0x2000
	s_addc_u32 s73, s73, 0
	global_load_dword v237, v248, s[72:73]
	s_add_u32 s72, s72, 0x2000
	s_addc_u32 s73, s73, 0
	global_load_dword v238, v248, s[72:73]
	s_add_u32 s72, s72, 0x2000
	s_addc_u32 s73, s73, 0
	global_load_dword v239, v248, s[72:73]
	s_add_u32 s72, s72, 0x2000
	s_addc_u32 s73, s73, 0
	global_load_dword v240, v248, s[72:73]
	s_add_u32 s72, s72, 0x2000
	s_addc_u32 s73, s73, 0
	global_load_dword v241, v248, s[72:73]
	s_add_u32 s72, s72, 0x2000
	s_addc_u32 s73, s73, 0
	global_load_dword v242, v248, s[72:73]
	s_add_u32 s72, s72, 0x2000
	s_addc_u32 s73, s73, 0
	global_load_dword v243, v248, s[72:73]
	s_add_u32 s70, s70, 1
	s_and_b32 s84, s70, 3
	s_cmp_eq_u32 s84, 0
	s_cselect_b32 s84, s71, 0
	s_add_u32 s70, s70, s84
	s_mov_b32 s82, 1
	s_branch .Lpb1_drain
